# lean attention loop + GEMM K-loop DMA rebalance (2/4/4/6, waits 8/6/8/6) + inverted GEMM s_setprio roles
# speedup vs baseline: 1.0080x; 1.0080x over previous
.LBB0_378:
	s_add_u32 s28, s36, 0xfff80080
	s_addc_u32 s29, s37, -1
	s_add_i32 s42, 0, 0x10000
	s_cmp_eq_u32 vcc_hi, 28
	s_cselect_b32 s53, s11, s29
	s_cselect_b32 s52, s21, s28
	s_cselect_b32 s51, s41, s79
	s_cselect_b32 s50, vcc_lo, s78
	s_add_i32 s43, 0, 0x14000
	v_add_u32_e32 v140, s42, v169
	v_add_u32_e32 v173, s43, v169
	ds_read_b128 v[128:131], v140
	ds_read_b128 v[132:135], v140 offset:1024
	ds_read_b128 v[136:139], v140 offset:2048
	ds_read_b128 v[140:143], v140 offset:3072
	ds_read_b128 v[156:159], v173
	ds_read_b128 v[160:163], v173 offset:1024
	ds_read_b128 v[164:167], v173 offset:2048
	ds_read_b128 v[174:177], v173 offset:3072
	v_lshl_add_u64 v[182:183], s[36:37], 0, v[152:153]
	s_add_i32 m0, s88, 0xc000
	ds_read_b128 v[178:181], v172
	ds_read_b128 v[194:197], v172 offset:1024
	ds_read_b128 v[198:201], v172 offset:2048
	ds_read_b128 v[202:205], v172 offset:3072
	ds_read_b128 v[206:209], v172 offset:4096
	ds_read_b128 v[224:227], v172 offset:5120
	ds_read_b128 v[228:231], v172 offset:6144
	ds_read_b128 v[232:235], v172 offset:7168
	global_load_lds_dwordx4 v[182:183], off
	v_lshl_add_u64 v[182:183], s[36:37], 0, v[154:155]
	s_add_i32 m0, s88, 0xe000
	s_nop 0
	global_load_lds_dwordx4 v[182:183], off
	s_waitcnt vmcnt(8)
	s_waitcnt lgkmcnt(0)
	s_barrier
	s_setprio 0
	s_waitcnt lgkmcnt(0)
	v_mfma_f32_16x16x32_bf16 v[124:127], v[128:131], v[178:181], v[124:127]
	v_mfma_f32_16x16x32_bf16 v[120:123], v[136:139], v[178:181], v[120:123]
	v_mfma_f32_16x16x32_bf16 v[116:119], v[128:131], v[198:201], v[116:119]
	v_mfma_f32_16x16x32_bf16 v[108:111], v[136:139], v[198:201], v[108:111]
	v_mfma_f32_16x16x32_bf16 v[100:103], v[128:131], v[206:209], v[100:103]
	v_mfma_f32_16x16x32_bf16 v[92:95], v[136:139], v[206:209], v[92:95]
	v_mfma_f32_16x16x32_bf16 v[84:87], v[128:131], v[228:231], v[84:87]
	v_mfma_f32_16x16x32_bf16 v[76:79], v[136:139], v[228:231], v[76:79]
	v_mfma_f32_16x16x32_bf16 v[124:127], v[132:135], v[194:197], v[124:127]
	v_mfma_f32_16x16x32_bf16 v[120:123], v[140:143], v[194:197], v[120:123]
	v_mfma_f32_16x16x32_bf16 v[116:119], v[132:135], v[202:205], v[116:119]
	v_mfma_f32_16x16x32_bf16 v[108:111], v[140:143], v[202:205], v[108:111]
	v_mfma_f32_16x16x32_bf16 v[100:103], v[132:135], v[224:227], v[100:103]
	v_mfma_f32_16x16x32_bf16 v[92:95], v[140:143], v[224:227], v[92:95]
	v_mfma_f32_16x16x32_bf16 v[84:87], v[132:135], v[232:235], v[84:87]
	v_mfma_f32_16x16x32_bf16 v[76:79], v[140:143], v[232:235], v[76:79]
	s_setprio 1
	s_setprio 0
	v_mfma_f32_16x16x32_bf16 v[112:115], v[156:159], v[178:181], v[112:115]
	v_mfma_f32_16x16x32_bf16 v[104:107], v[164:167], v[178:181], v[104:107]
	v_mfma_f32_16x16x32_bf16 v[96:99], v[156:159], v[198:201], v[96:99]
	v_mfma_f32_16x16x32_bf16 v[88:91], v[164:167], v[198:201], v[88:91]
	v_mfma_f32_16x16x32_bf16 v[80:83], v[156:159], v[206:209], v[80:83]
	v_mfma_f32_16x16x32_bf16 v[72:75], v[164:167], v[206:209], v[72:75]
	v_mfma_f32_16x16x32_bf16 v[68:71], v[156:159], v[228:231], v[68:71]
	v_mfma_f32_16x16x32_bf16 v[64:67], v[164:167], v[228:231], v[64:67]
	v_mfma_f32_16x16x32_bf16 v[112:115], v[160:163], v[194:197], v[112:115]
	v_mfma_f32_16x16x32_bf16 v[104:107], v[174:177], v[194:197], v[104:107]
	v_mfma_f32_16x16x32_bf16 v[96:99], v[160:163], v[202:205], v[96:99]
	v_mfma_f32_16x16x32_bf16 v[88:91], v[174:177], v[202:205], v[88:91]
	v_mfma_f32_16x16x32_bf16 v[80:83], v[160:163], v[224:227], v[80:83]
	v_mfma_f32_16x16x32_bf16 v[72:75], v[174:177], v[224:227], v[72:75]
	v_mfma_f32_16x16x32_bf16 v[68:71], v[160:163], v[232:235], v[68:71]
	v_mfma_f32_16x16x32_bf16 v[64:67], v[174:177], v[232:235], v[64:67]
	s_setprio 1
	s_barrier
	s_add_i32 s28, s42, s62
	v_lshl_add_u64 v[182:183], s[50:51], 0, v[146:147]
	s_mov_b32 m0, s28
	ds_read_b128 v[178:181], v172 offset:16384
	ds_read_b128 v[194:197], v172 offset:17408
	ds_read_b128 v[198:201], v172 offset:18432
	ds_read_b128 v[202:205], v172 offset:19456
	ds_read_b128 v[206:209], v172 offset:20480
	ds_read_b128 v[224:227], v172 offset:21504
	ds_read_b128 v[228:231], v172 offset:22528
	ds_read_b128 v[232:235], v172 offset:23552
	global_load_lds_dwordx4 v[182:183], off
	s_add_i32 m0, s28, 0x2000
	s_add_u32 s28, s50, 0x80000
	v_lshl_add_u64 v[210:211], s[50:51], 0, v[150:151]
	s_addc_u32 s29, s51, 0
	s_add_i32 s42, s43, s62
	global_load_lds_dwordx4 v[210:211], off
	v_lshl_add_u64 v[236:237], s[28:29], 0, v[146:147]
	s_mov_b32 m0, s42
	v_lshl_add_u64 v[238:239], s[52:53], 0, v[148:149]
	global_load_lds_dwordx4 v[236:237], off
	v_lshl_add_u64 v[236:237], s[28:29], 0, v[150:151]
	s_add_i32 m0, s42, 0x2000
	s_nop 0
	global_load_lds_dwordx4 v[236:237], off
	v_lshl_add_u64 v[236:237], s[52:53], 0, v[144:145]
	s_waitcnt vmcnt(6)
	s_waitcnt lgkmcnt(0)
	s_barrier
	s_setprio 0
	s_waitcnt lgkmcnt(0)
	v_mfma_f32_16x16x32_bf16 v[60:63], v[128:131], v[178:181], v[60:63]
	v_mfma_f32_16x16x32_bf16 v[56:59], v[136:139], v[178:181], v[56:59]
	v_mfma_f32_16x16x32_bf16 v[52:55], v[128:131], v[198:201], v[52:55]
	v_mfma_f32_16x16x32_bf16 v[44:47], v[136:139], v[198:201], v[44:47]
	v_mfma_f32_16x16x32_bf16 v[36:39], v[128:131], v[206:209], v[36:39]
	v_mfma_f32_16x16x32_bf16 v[28:31], v[136:139], v[206:209], v[28:31]
	v_mfma_f32_16x16x32_bf16 v[20:23], v[128:131], v[228:231], v[20:23]
	v_mfma_f32_16x16x32_bf16 v[12:15], v[136:139], v[228:231], v[12:15]
	v_mfma_f32_16x16x32_bf16 v[60:63], v[132:135], v[194:197], v[60:63]
	v_mfma_f32_16x16x32_bf16 v[56:59], v[140:143], v[194:197], v[56:59]
	v_mfma_f32_16x16x32_bf16 v[52:55], v[132:135], v[202:205], v[52:55]
	v_mfma_f32_16x16x32_bf16 v[44:47], v[140:143], v[202:205], v[44:47]
	v_mfma_f32_16x16x32_bf16 v[36:39], v[132:135], v[224:227], v[36:39]
	v_mfma_f32_16x16x32_bf16 v[28:31], v[140:143], v[224:227], v[28:31]
	v_mfma_f32_16x16x32_bf16 v[20:23], v[132:135], v[232:235], v[20:23]
	v_mfma_f32_16x16x32_bf16 v[12:15], v[140:143], v[232:235], v[12:15]
	s_setprio 1
	s_setprio 0
	v_mfma_f32_16x16x32_bf16 v[48:51], v[156:159], v[178:181], v[48:51]
	v_mfma_f32_16x16x32_bf16 v[40:43], v[164:167], v[178:181], v[40:43]
	v_mfma_f32_16x16x32_bf16 v[32:35], v[156:159], v[198:201], v[32:35]
	v_mfma_f32_16x16x32_bf16 v[24:27], v[164:167], v[198:201], v[24:27]
	v_mfma_f32_16x16x32_bf16 v[16:19], v[156:159], v[206:209], v[16:19]
	v_mfma_f32_16x16x32_bf16 v[8:11], v[164:167], v[206:209], v[8:11]
	v_mfma_f32_16x16x32_bf16 v[4:7], v[156:159], v[228:231], v[4:7]
	v_mfma_f32_16x16x32_bf16 v[0:3], v[164:167], v[228:231], v[0:3]
	v_mfma_f32_16x16x32_bf16 v[48:51], v[160:163], v[194:197], v[48:51]
	v_mfma_f32_16x16x32_bf16 v[40:43], v[174:177], v[194:197], v[40:43]
	v_mfma_f32_16x16x32_bf16 v[32:35], v[160:163], v[202:205], v[32:35]
	v_mfma_f32_16x16x32_bf16 v[24:27], v[174:177], v[202:205], v[24:27]
	v_mfma_f32_16x16x32_bf16 v[16:19], v[160:163], v[224:227], v[16:19]
	v_mfma_f32_16x16x32_bf16 v[8:11], v[174:177], v[224:227], v[8:11]
	v_mfma_f32_16x16x32_bf16 v[4:7], v[160:163], v[232:235], v[4:7]
	v_mfma_f32_16x16x32_bf16 v[0:3], v[174:177], v[232:235], v[0:3]
	s_setprio 1
	s_barrier
	s_add_i32 s42, 0, 0x18000
	s_add_i32 s43, 0, 0x1c000
	v_add_u32_e32 v140, s42, v169
	v_add_u32_e32 v173, s43, v169
	ds_read_b128 v[128:131], v140
	ds_read_b128 v[132:135], v140 offset:1024
	ds_read_b128 v[136:139], v140 offset:2048
	ds_read_b128 v[140:143], v140 offset:3072
	ds_read_b128 v[156:159], v173
	ds_read_b128 v[160:163], v173 offset:1024
	ds_read_b128 v[164:167], v173 offset:2048
	ds_read_b128 v[174:177], v173 offset:3072
	s_add_u32 s28, s52, 0x80000
	s_addc_u32 s29, s53, 0
	s_mov_b32 m0, s26
	v_lshl_add_u64 v[240:241], s[28:29], 0, v[144:145]
	ds_read_b128 v[178:181], v172 offset:32768
	ds_read_b128 v[194:197], v172 offset:33792
	ds_read_b128 v[198:201], v172 offset:34816
	ds_read_b128 v[202:205], v172 offset:35840
	ds_read_b128 v[206:209], v172 offset:36864
	ds_read_b128 v[224:227], v172 offset:37888
	ds_read_b128 v[228:231], v172 offset:38912
	ds_read_b128 v[232:235], v172 offset:39936
	global_load_lds_dwordx4 v[240:241], off
	v_lshl_add_u64 v[240:241], s[28:29], 0, v[148:149]
	s_mov_b32 m0, s27
	s_nop 0
	global_load_lds_dwordx4 v[240:241], off
	s_mov_b32 m0, s88
	s_nop 0
	global_load_lds_dwordx4 v[236:237], off
	s_mov_b32 m0, s89
	s_nop 0
	global_load_lds_dwordx4 v[238:239], off
	s_waitcnt vmcnt(8)
	s_waitcnt lgkmcnt(0)
	s_barrier
	s_setprio 0
	s_waitcnt lgkmcnt(0)
	v_mfma_f32_16x16x32_bf16 v[124:127], v[128:131], v[178:181], v[124:127]
	v_mfma_f32_16x16x32_bf16 v[120:123], v[136:139], v[178:181], v[120:123]
	v_mfma_f32_16x16x32_bf16 v[116:119], v[128:131], v[198:201], v[116:119]
	v_mfma_f32_16x16x32_bf16 v[108:111], v[136:139], v[198:201], v[108:111]
	v_mfma_f32_16x16x32_bf16 v[100:103], v[128:131], v[206:209], v[100:103]
	v_mfma_f32_16x16x32_bf16 v[92:95], v[136:139], v[206:209], v[92:95]
	v_mfma_f32_16x16x32_bf16 v[84:87], v[128:131], v[228:231], v[84:87]
	v_mfma_f32_16x16x32_bf16 v[76:79], v[136:139], v[228:231], v[76:79]
	v_mfma_f32_16x16x32_bf16 v[124:127], v[132:135], v[194:197], v[124:127]
	v_mfma_f32_16x16x32_bf16 v[120:123], v[140:143], v[194:197], v[120:123]
	v_mfma_f32_16x16x32_bf16 v[116:119], v[132:135], v[202:205], v[116:119]
	v_mfma_f32_16x16x32_bf16 v[108:111], v[140:143], v[202:205], v[108:111]
	v_mfma_f32_16x16x32_bf16 v[100:103], v[132:135], v[224:227], v[100:103]
	v_mfma_f32_16x16x32_bf16 v[92:95], v[140:143], v[224:227], v[92:95]
	v_mfma_f32_16x16x32_bf16 v[84:87], v[132:135], v[232:235], v[84:87]
	v_mfma_f32_16x16x32_bf16 v[76:79], v[140:143], v[232:235], v[76:79]
	s_setprio 1
	s_setprio 0
	v_mfma_f32_16x16x32_bf16 v[112:115], v[156:159], v[178:181], v[112:115]
	v_mfma_f32_16x16x32_bf16 v[104:107], v[164:167], v[178:181], v[104:107]
	v_mfma_f32_16x16x32_bf16 v[96:99], v[156:159], v[198:201], v[96:99]
	v_mfma_f32_16x16x32_bf16 v[88:91], v[164:167], v[198:201], v[88:91]
	v_mfma_f32_16x16x32_bf16 v[80:83], v[156:159], v[206:209], v[80:83]
	v_mfma_f32_16x16x32_bf16 v[72:75], v[164:167], v[206:209], v[72:75]
	v_mfma_f32_16x16x32_bf16 v[68:71], v[156:159], v[228:231], v[68:71]
	v_mfma_f32_16x16x32_bf16 v[64:67], v[164:167], v[228:231], v[64:67]
	v_mfma_f32_16x16x32_bf16 v[112:115], v[160:163], v[194:197], v[112:115]
	v_mfma_f32_16x16x32_bf16 v[104:107], v[174:177], v[194:197], v[104:107]
	v_mfma_f32_16x16x32_bf16 v[96:99], v[160:163], v[202:205], v[96:99]
	v_mfma_f32_16x16x32_bf16 v[88:91], v[174:177], v[202:205], v[88:91]
	v_mfma_f32_16x16x32_bf16 v[80:83], v[160:163], v[224:227], v[80:83]
	v_mfma_f32_16x16x32_bf16 v[72:75], v[174:177], v[224:227], v[72:75]
	v_mfma_f32_16x16x32_bf16 v[68:71], v[160:163], v[232:235], v[68:71]
	v_mfma_f32_16x16x32_bf16 v[64:67], v[174:177], v[232:235], v[64:67]
	s_setprio 1
	s_barrier
	s_add_i32 s28, s42, s62
	v_lshl_add_u64 v[182:183], v[182:183], 0, s[68:69]
	s_mov_b32 m0, s28
	ds_read_b128 v[178:181], v172 offset:49152
	ds_read_b128 v[194:197], v172 offset:50176
	ds_read_b128 v[198:201], v172 offset:51200
	ds_read_b128 v[202:205], v172 offset:52224
	ds_read_b128 v[206:209], v172 offset:53248
	ds_read_b128 v[224:227], v172 offset:54272
	ds_read_b128 v[228:231], v172 offset:55296
	ds_read_b128 v[232:235], v172 offset:56320
	global_load_lds_dwordx4 v[182:183], off
	s_add_i32 m0, s28, 0x2000
	s_add_u32 s28, s50, 0x80080
	v_lshl_add_u64 v[182:183], v[210:211], 0, s[68:69]
	s_addc_u32 s29, s51, 0
	s_add_i32 s42, s43, s62
	global_load_lds_dwordx4 v[182:183], off
	v_lshl_add_u64 v[182:183], s[28:29], 0, v[146:147]
	s_mov_b32 m0, s42
	s_nop 0
	global_load_lds_dwordx4 v[182:183], off
	v_lshl_add_u64 v[182:183], s[28:29], 0, v[150:151]
	s_add_i32 m0, s42, 0x2000
	s_nop 0
	global_load_lds_dwordx4 v[182:183], off
	v_lshl_add_u64 v[182:183], v[236:237], 0, s[68:69]
	s_mov_b32 m0, s94
	s_nop 0
	global_load_lds_dwordx4 v[182:183], off
	v_lshl_add_u64 v[182:183], v[238:239], 0, s[68:69]
	s_mov_b32 m0, s95
	s_nop 0
	global_load_lds_dwordx4 v[182:183], off
	s_waitcnt vmcnt(6)
	s_waitcnt lgkmcnt(0)
	s_barrier
	s_setprio 0
	s_waitcnt lgkmcnt(0)
	v_mfma_f32_16x16x32_bf16 v[60:63], v[128:131], v[178:181], v[60:63]
	v_mfma_f32_16x16x32_bf16 v[56:59], v[136:139], v[178:181], v[56:59]
	v_mfma_f32_16x16x32_bf16 v[52:55], v[128:131], v[198:201], v[52:55]
	v_mfma_f32_16x16x32_bf16 v[44:47], v[136:139], v[198:201], v[44:47]
	v_mfma_f32_16x16x32_bf16 v[36:39], v[128:131], v[206:209], v[36:39]
	v_mfma_f32_16x16x32_bf16 v[28:31], v[136:139], v[206:209], v[28:31]
	v_mfma_f32_16x16x32_bf16 v[20:23], v[128:131], v[228:231], v[20:23]
	v_mfma_f32_16x16x32_bf16 v[12:15], v[136:139], v[228:231], v[12:15]
	v_mfma_f32_16x16x32_bf16 v[60:63], v[132:135], v[194:197], v[60:63]
	v_mfma_f32_16x16x32_bf16 v[56:59], v[140:143], v[194:197], v[56:59]
	v_mfma_f32_16x16x32_bf16 v[52:55], v[132:135], v[202:205], v[52:55]
	v_mfma_f32_16x16x32_bf16 v[44:47], v[140:143], v[202:205], v[44:47]
	v_mfma_f32_16x16x32_bf16 v[36:39], v[132:135], v[224:227], v[36:39]
	v_mfma_f32_16x16x32_bf16 v[28:31], v[140:143], v[224:227], v[28:31]
	v_mfma_f32_16x16x32_bf16 v[20:23], v[132:135], v[232:235], v[20:23]
	v_mfma_f32_16x16x32_bf16 v[12:15], v[140:143], v[232:235], v[12:15]
	s_setprio 1
	s_setprio 0
	v_mfma_f32_16x16x32_bf16 v[48:51], v[156:159], v[178:181], v[48:51]
	v_mfma_f32_16x16x32_bf16 v[40:43], v[164:167], v[178:181], v[40:43]
	v_mfma_f32_16x16x32_bf16 v[32:35], v[156:159], v[198:201], v[32:35]
	v_mfma_f32_16x16x32_bf16 v[24:27], v[164:167], v[198:201], v[24:27]
	v_mfma_f32_16x16x32_bf16 v[16:19], v[156:159], v[206:209], v[16:19]
	v_mfma_f32_16x16x32_bf16 v[8:11], v[164:167], v[206:209], v[8:11]
	v_mfma_f32_16x16x32_bf16 v[4:7], v[156:159], v[228:231], v[4:7]
	v_mfma_f32_16x16x32_bf16 v[0:3], v[164:167], v[228:231], v[0:3]
	v_mfma_f32_16x16x32_bf16 v[48:51], v[160:163], v[194:197], v[48:51]
	v_mfma_f32_16x16x32_bf16 v[40:43], v[174:177], v[194:197], v[40:43]
	v_mfma_f32_16x16x32_bf16 v[32:35], v[160:163], v[202:205], v[32:35]
	v_mfma_f32_16x16x32_bf16 v[24:27], v[174:177], v[202:205], v[24:27]
	v_mfma_f32_16x16x32_bf16 v[16:19], v[160:163], v[224:227], v[16:19]
	v_mfma_f32_16x16x32_bf16 v[8:11], v[174:177], v[224:227], v[8:11]
	v_mfma_f32_16x16x32_bf16 v[4:7], v[160:163], v[232:235], v[4:7]
	v_mfma_f32_16x16x32_bf16 v[0:3], v[174:177], v[232:235], v[0:3]
	s_setprio 1
	s_barrier
	s_add_i32 vcc_hi, vcc_hi, 2
	s_add_u32 s36, s36, 0x100
	s_addc_u32 s37, s37, 0
	s_add_u32 s78, s78, 0x100
	s_addc_u32 s79, s79, 0
	s_cmp_gt_u32 vcc_hi, 29
	s_cbranch_scc0 .LBB0_378
	s_and_b64 vcc, exec, s[14:15]
	s_cbranch_vccz .LBB0_381
	s_barrier

.LBB0_682:
	s_add_u32 s18, s16, 0x100
	s_addc_u32 s19, s17, 0
	s_add_u32 s28, s45, s16
	s_addc_u32 s29, s46, s17
	s_cmp_eq_u32 s47, 4
	s_cselect_b32 s36, 0, s18
	s_cselect_b32 s37, 0, s19
	s_cselect_b32 s30, s44, s28
	s_cselect_b32 s31, s9, s29
	s_add_u32 s36, s64, s36
	s_addc_u32 s37, s65, s37
	s_add_i32 s28, 0, 0x10000
	s_add_i32 s29, 0, 0x14000
	v_add_u32_e32 v168, s28, v154
	v_add_u32_e32 v194, s29, v154
	ds_read_b128 v[156:159], v168
	ds_read_b128 v[160:163], v168 offset:1024
	ds_read_b128 v[164:167], v168 offset:2048
	ds_read_b128 v[168:171], v168 offset:3072
	ds_read_b128 v[172:175], v194
	ds_read_b128 v[176:179], v194 offset:1024
	ds_read_b128 v[180:183], v194 offset:2048
	ds_read_b128 v[194:197], v194 offset:3072
	v_lshl_add_u64 v[210:211], v[150:151], 0, s[16:17]
	s_add_i32 m0, s20, 0xc000
	ds_read_b128 v[198:201], v155
	ds_read_b128 v[202:205], v155 offset:1024
	ds_read_b128 v[206:209], v155 offset:2048
	ds_read_b128 v[224:227], v155 offset:3072
	ds_read_b128 v[228:231], v155 offset:4096
	ds_read_b128 v[232:235], v155 offset:5120
	ds_read_b128 v[236:239], v155 offset:6144
	ds_read_b128 v[240:243], v155 offset:7168
	global_load_lds_dwordx4 v[210:211], off
	v_lshl_add_u64 v[210:211], v[152:153], 0, s[16:17]
	s_add_i32 m0, s20, 0xe000
	s_nop 0
	global_load_lds_dwordx4 v[210:211], off
	s_waitcnt vmcnt(8)
	s_waitcnt lgkmcnt(0)
	s_barrier
	s_setprio 0
	s_waitcnt lgkmcnt(0)
	v_mfma_f32_16x16x32_bf16 v[124:127], v[156:159], v[198:201], v[124:127]
	v_mfma_f32_16x16x32_bf16 v[120:123], v[164:167], v[198:201], v[120:123]
	v_mfma_f32_16x16x32_bf16 v[116:119], v[156:159], v[206:209], v[116:119]
	v_mfma_f32_16x16x32_bf16 v[108:111], v[164:167], v[206:209], v[108:111]
	v_mfma_f32_16x16x32_bf16 v[100:103], v[156:159], v[228:231], v[100:103]
	v_mfma_f32_16x16x32_bf16 v[92:95], v[164:167], v[228:231], v[92:95]
	v_mfma_f32_16x16x32_bf16 v[84:87], v[156:159], v[236:239], v[84:87]
	v_mfma_f32_16x16x32_bf16 v[76:79], v[164:167], v[236:239], v[76:79]
	v_mfma_f32_16x16x32_bf16 v[124:127], v[160:163], v[202:205], v[124:127]
	v_mfma_f32_16x16x32_bf16 v[120:123], v[168:171], v[202:205], v[120:123]
	v_mfma_f32_16x16x32_bf16 v[116:119], v[160:163], v[224:227], v[116:119]
	v_mfma_f32_16x16x32_bf16 v[108:111], v[168:171], v[224:227], v[108:111]
	v_mfma_f32_16x16x32_bf16 v[100:103], v[160:163], v[232:235], v[100:103]
	v_mfma_f32_16x16x32_bf16 v[92:95], v[168:171], v[232:235], v[92:95]
	v_mfma_f32_16x16x32_bf16 v[84:87], v[160:163], v[240:243], v[84:87]
	v_mfma_f32_16x16x32_bf16 v[76:79], v[168:171], v[240:243], v[76:79]
	s_setprio 1
	s_setprio 0
	v_mfma_f32_16x16x32_bf16 v[112:115], v[172:175], v[198:201], v[112:115]
	v_mfma_f32_16x16x32_bf16 v[104:107], v[180:183], v[198:201], v[104:107]
	v_mfma_f32_16x16x32_bf16 v[96:99], v[172:175], v[206:209], v[96:99]
	v_mfma_f32_16x16x32_bf16 v[88:91], v[180:183], v[206:209], v[88:91]
	v_mfma_f32_16x16x32_bf16 v[80:83], v[172:175], v[228:231], v[80:83]
	v_mfma_f32_16x16x32_bf16 v[72:75], v[180:183], v[228:231], v[72:75]
	v_mfma_f32_16x16x32_bf16 v[68:71], v[172:175], v[236:239], v[68:71]
	v_mfma_f32_16x16x32_bf16 v[64:67], v[180:183], v[236:239], v[64:67]
	v_mfma_f32_16x16x32_bf16 v[112:115], v[176:179], v[202:205], v[112:115]
	v_mfma_f32_16x16x32_bf16 v[104:107], v[194:197], v[202:205], v[104:107]
	v_mfma_f32_16x16x32_bf16 v[96:99], v[176:179], v[224:227], v[96:99]
	v_mfma_f32_16x16x32_bf16 v[88:91], v[194:197], v[224:227], v[88:91]
	v_mfma_f32_16x16x32_bf16 v[80:83], v[176:179], v[232:235], v[80:83]
	v_mfma_f32_16x16x32_bf16 v[72:75], v[194:197], v[232:235], v[72:75]
	v_mfma_f32_16x16x32_bf16 v[68:71], v[176:179], v[240:243], v[68:71]
	v_mfma_f32_16x16x32_bf16 v[64:67], v[194:197], v[240:243], v[64:67]
	s_setprio 1
	s_barrier
	s_add_i32 s16, s28, s4
	v_lshl_add_u64 v[210:211], s[30:31], 0, v[184:185]
	s_mov_b32 m0, s16
	ds_read_b128 v[198:201], v155 offset:16384
	ds_read_b128 v[202:205], v155 offset:17408
	ds_read_b128 v[206:209], v155 offset:18432
	ds_read_b128 v[224:227], v155 offset:19456
	ds_read_b128 v[228:231], v155 offset:20480
	ds_read_b128 v[232:235], v155 offset:21504
	ds_read_b128 v[236:239], v155 offset:22528
	ds_read_b128 v[240:243], v155 offset:23552
	global_load_lds_dwordx4 v[210:211], off
	s_add_i32 m0, s16, 0x2000
	s_add_u32 s16, s30, 0x20000
	v_lshl_add_u64 v[244:245], s[30:31], 0, v[128:129]
	s_addc_u32 s17, s31, 0
	s_add_i32 s28, s29, s4
	global_load_lds_dwordx4 v[244:245], off
	v_lshl_add_u64 v[246:247], s[16:17], 0, v[184:185]
	s_mov_b32 m0, s28
	v_lshl_add_u64 v[218:219], s[36:37], 0, v[130:131]
	global_load_lds_dwordx4 v[246:247], off
	v_lshl_add_u64 v[246:247], s[16:17], 0, v[128:129]
	s_add_i32 m0, s28, 0x2000
	s_nop 0
	global_load_lds_dwordx4 v[246:247], off
	v_lshl_add_u64 v[246:247], s[36:37], 0, v[132:133]
	s_waitcnt vmcnt(6)
	s_waitcnt lgkmcnt(0)
	s_barrier
	s_setprio 0
	s_waitcnt lgkmcnt(0)
	v_mfma_f32_16x16x32_bf16 v[60:63], v[156:159], v[198:201], v[60:63]
	v_mfma_f32_16x16x32_bf16 v[56:59], v[164:167], v[198:201], v[56:59]
	v_mfma_f32_16x16x32_bf16 v[52:55], v[156:159], v[206:209], v[52:55]
	v_mfma_f32_16x16x32_bf16 v[44:47], v[164:167], v[206:209], v[44:47]
	v_mfma_f32_16x16x32_bf16 v[36:39], v[156:159], v[228:231], v[36:39]
	v_mfma_f32_16x16x32_bf16 v[28:31], v[164:167], v[228:231], v[28:31]
	v_mfma_f32_16x16x32_bf16 v[20:23], v[156:159], v[236:239], v[20:23]
	v_mfma_f32_16x16x32_bf16 v[12:15], v[164:167], v[236:239], v[12:15]
	v_mfma_f32_16x16x32_bf16 v[60:63], v[160:163], v[202:205], v[60:63]
	v_mfma_f32_16x16x32_bf16 v[56:59], v[168:171], v[202:205], v[56:59]
	v_mfma_f32_16x16x32_bf16 v[52:55], v[160:163], v[224:227], v[52:55]
	v_mfma_f32_16x16x32_bf16 v[44:47], v[168:171], v[224:227], v[44:47]
	v_mfma_f32_16x16x32_bf16 v[36:39], v[160:163], v[232:235], v[36:39]
	v_mfma_f32_16x16x32_bf16 v[28:31], v[168:171], v[232:235], v[28:31]
	v_mfma_f32_16x16x32_bf16 v[20:23], v[160:163], v[240:243], v[20:23]
	v_mfma_f32_16x16x32_bf16 v[12:15], v[168:171], v[240:243], v[12:15]
	s_setprio 1
	s_setprio 0
	v_mfma_f32_16x16x32_bf16 v[48:51], v[172:175], v[198:201], v[48:51]
	v_mfma_f32_16x16x32_bf16 v[40:43], v[180:183], v[198:201], v[40:43]
	v_mfma_f32_16x16x32_bf16 v[32:35], v[172:175], v[206:209], v[32:35]
	v_mfma_f32_16x16x32_bf16 v[24:27], v[180:183], v[206:209], v[24:27]
	v_mfma_f32_16x16x32_bf16 v[16:19], v[172:175], v[228:231], v[16:19]
	v_mfma_f32_16x16x32_bf16 v[8:11], v[180:183], v[228:231], v[8:11]
	v_mfma_f32_16x16x32_bf16 v[4:7], v[172:175], v[236:239], v[4:7]
	v_mfma_f32_16x16x32_bf16 v[0:3], v[180:183], v[236:239], v[0:3]
	v_mfma_f32_16x16x32_bf16 v[48:51], v[176:179], v[202:205], v[48:51]
	v_mfma_f32_16x16x32_bf16 v[40:43], v[194:197], v[202:205], v[40:43]
	v_mfma_f32_16x16x32_bf16 v[32:35], v[176:179], v[224:227], v[32:35]
	v_mfma_f32_16x16x32_bf16 v[24:27], v[194:197], v[224:227], v[24:27]
	v_mfma_f32_16x16x32_bf16 v[16:19], v[176:179], v[232:235], v[16:19]
	v_mfma_f32_16x16x32_bf16 v[8:11], v[194:197], v[232:235], v[8:11]
	v_mfma_f32_16x16x32_bf16 v[4:7], v[176:179], v[240:243], v[4:7]
	v_mfma_f32_16x16x32_bf16 v[0:3], v[194:197], v[240:243], v[0:3]
	s_setprio 1
	s_barrier
	s_add_i32 s28, 0, 0x18000
	s_add_i32 s29, 0, 0x1c000
	v_add_u32_e32 v168, s28, v154
	v_add_u32_e32 v194, s29, v154
	ds_read_b128 v[156:159], v168
	ds_read_b128 v[160:163], v168 offset:1024
	ds_read_b128 v[164:167], v168 offset:2048
	ds_read_b128 v[168:171], v168 offset:3072
	ds_read_b128 v[172:175], v194
	ds_read_b128 v[176:179], v194 offset:1024
	ds_read_b128 v[180:183], v194 offset:2048
	ds_read_b128 v[194:197], v194 offset:3072
	s_add_u32 s16, s36, 0x20000
	s_addc_u32 s17, s37, 0
	s_mov_b32 m0, s26
	v_lshl_add_u64 v[216:217], s[16:17], 0, v[132:133]
	ds_read_b128 v[198:201], v155 offset:32768
	ds_read_b128 v[202:205], v155 offset:33792
	ds_read_b128 v[206:209], v155 offset:34816
	ds_read_b128 v[224:227], v155 offset:35840
	ds_read_b128 v[228:231], v155 offset:36864
	ds_read_b128 v[232:235], v155 offset:37888
	ds_read_b128 v[236:239], v155 offset:38912
	ds_read_b128 v[240:243], v155 offset:39936
	global_load_lds_dwordx4 v[216:217], off
	v_lshl_add_u64 v[216:217], s[16:17], 0, v[130:131]
	s_mov_b32 m0, s27
	s_nop 0
	global_load_lds_dwordx4 v[216:217], off
	s_mov_b32 m0, s20
	s_nop 0
	global_load_lds_dwordx4 v[246:247], off
	s_mov_b32 m0, s21
	s_nop 0
	global_load_lds_dwordx4 v[218:219], off
	s_waitcnt vmcnt(8)
	s_waitcnt lgkmcnt(0)
	s_barrier
	s_setprio 0
	s_waitcnt lgkmcnt(0)
	v_mfma_f32_16x16x32_bf16 v[124:127], v[156:159], v[198:201], v[124:127]
	v_mfma_f32_16x16x32_bf16 v[120:123], v[164:167], v[198:201], v[120:123]
	v_mfma_f32_16x16x32_bf16 v[116:119], v[156:159], v[206:209], v[116:119]
	v_mfma_f32_16x16x32_bf16 v[108:111], v[164:167], v[206:209], v[108:111]
	v_mfma_f32_16x16x32_bf16 v[100:103], v[156:159], v[228:231], v[100:103]
	v_mfma_f32_16x16x32_bf16 v[92:95], v[164:167], v[228:231], v[92:95]
	v_mfma_f32_16x16x32_bf16 v[84:87], v[156:159], v[236:239], v[84:87]
	v_mfma_f32_16x16x32_bf16 v[76:79], v[164:167], v[236:239], v[76:79]
	v_mfma_f32_16x16x32_bf16 v[124:127], v[160:163], v[202:205], v[124:127]
	v_mfma_f32_16x16x32_bf16 v[120:123], v[168:171], v[202:205], v[120:123]
	v_mfma_f32_16x16x32_bf16 v[116:119], v[160:163], v[224:227], v[116:119]
	v_mfma_f32_16x16x32_bf16 v[108:111], v[168:171], v[224:227], v[108:111]
	v_mfma_f32_16x16x32_bf16 v[100:103], v[160:163], v[232:235], v[100:103]
	v_mfma_f32_16x16x32_bf16 v[92:95], v[168:171], v[232:235], v[92:95]
	v_mfma_f32_16x16x32_bf16 v[84:87], v[160:163], v[240:243], v[84:87]
	v_mfma_f32_16x16x32_bf16 v[76:79], v[168:171], v[240:243], v[76:79]
	s_setprio 1
	s_setprio 0
	v_mfma_f32_16x16x32_bf16 v[112:115], v[172:175], v[198:201], v[112:115]
	v_mfma_f32_16x16x32_bf16 v[104:107], v[180:183], v[198:201], v[104:107]
	v_mfma_f32_16x16x32_bf16 v[96:99], v[172:175], v[206:209], v[96:99]
	v_mfma_f32_16x16x32_bf16 v[88:91], v[180:183], v[206:209], v[88:91]
	v_mfma_f32_16x16x32_bf16 v[80:83], v[172:175], v[228:231], v[80:83]
	v_mfma_f32_16x16x32_bf16 v[72:75], v[180:183], v[228:231], v[72:75]
	v_mfma_f32_16x16x32_bf16 v[68:71], v[172:175], v[236:239], v[68:71]
	v_mfma_f32_16x16x32_bf16 v[64:67], v[180:183], v[236:239], v[64:67]
	v_mfma_f32_16x16x32_bf16 v[112:115], v[176:179], v[202:205], v[112:115]
	v_mfma_f32_16x16x32_bf16 v[104:107], v[194:197], v[202:205], v[104:107]
	v_mfma_f32_16x16x32_bf16 v[96:99], v[176:179], v[224:227], v[96:99]
	v_mfma_f32_16x16x32_bf16 v[88:91], v[194:197], v[224:227], v[88:91]
	v_mfma_f32_16x16x32_bf16 v[80:83], v[176:179], v[232:235], v[80:83]
	v_mfma_f32_16x16x32_bf16 v[72:75], v[194:197], v[232:235], v[72:75]
	v_mfma_f32_16x16x32_bf16 v[68:71], v[176:179], v[240:243], v[68:71]
	v_mfma_f32_16x16x32_bf16 v[64:67], v[194:197], v[240:243], v[64:67]
	s_setprio 1
	s_barrier
	s_add_i32 s16, s28, s4
	v_lshl_add_u64 v[210:211], v[210:211], 0, s[68:69]
	s_mov_b32 m0, s16
	ds_read_b128 v[198:201], v155 offset:49152
	ds_read_b128 v[202:205], v155 offset:50176
	ds_read_b128 v[206:209], v155 offset:51200
	ds_read_b128 v[224:227], v155 offset:52224
	ds_read_b128 v[228:231], v155 offset:53248
	ds_read_b128 v[232:235], v155 offset:54272
	ds_read_b128 v[236:239], v155 offset:55296
	ds_read_b128 v[240:243], v155 offset:56320
	global_load_lds_dwordx4 v[210:211], off
	s_add_i32 m0, s16, 0x2000
	s_add_u32 s16, s30, 0x20080
	v_lshl_add_u64 v[210:211], v[244:245], 0, s[68:69]
	s_addc_u32 s17, s31, 0
	s_add_i32 s28, s29, s4
	global_load_lds_dwordx4 v[210:211], off
	v_lshl_add_u64 v[210:211], s[16:17], 0, v[184:185]
	s_mov_b32 m0, s28
	s_nop 0
	global_load_lds_dwordx4 v[210:211], off
	v_lshl_add_u64 v[210:211], s[16:17], 0, v[128:129]
	s_add_i32 m0, s28, 0x2000
	s_nop 0
	global_load_lds_dwordx4 v[210:211], off
	v_lshl_add_u64 v[210:211], v[246:247], 0, s[68:69]
	s_mov_b32 m0, s38
	s_nop 0
	global_load_lds_dwordx4 v[210:211], off
	v_lshl_add_u64 v[210:211], v[218:219], 0, s[68:69]
	s_mov_b32 m0, s39
	s_nop 0
	global_load_lds_dwordx4 v[210:211], off
	s_waitcnt vmcnt(6)
	s_waitcnt lgkmcnt(0)
	s_barrier
	s_setprio 0
	s_waitcnt lgkmcnt(0)
	v_mfma_f32_16x16x32_bf16 v[60:63], v[156:159], v[198:201], v[60:63]
	v_mfma_f32_16x16x32_bf16 v[56:59], v[164:167], v[198:201], v[56:59]
	v_mfma_f32_16x16x32_bf16 v[52:55], v[156:159], v[206:209], v[52:55]
	v_mfma_f32_16x16x32_bf16 v[44:47], v[164:167], v[206:209], v[44:47]
	v_mfma_f32_16x16x32_bf16 v[36:39], v[156:159], v[228:231], v[36:39]
	v_mfma_f32_16x16x32_bf16 v[28:31], v[164:167], v[228:231], v[28:31]
	v_mfma_f32_16x16x32_bf16 v[20:23], v[156:159], v[236:239], v[20:23]
	v_mfma_f32_16x16x32_bf16 v[12:15], v[164:167], v[236:239], v[12:15]
	v_mfma_f32_16x16x32_bf16 v[60:63], v[160:163], v[202:205], v[60:63]
	v_mfma_f32_16x16x32_bf16 v[56:59], v[168:171], v[202:205], v[56:59]
	v_mfma_f32_16x16x32_bf16 v[52:55], v[160:163], v[224:227], v[52:55]
	v_mfma_f32_16x16x32_bf16 v[44:47], v[168:171], v[224:227], v[44:47]
	v_mfma_f32_16x16x32_bf16 v[36:39], v[160:163], v[232:235], v[36:39]
	v_mfma_f32_16x16x32_bf16 v[28:31], v[168:171], v[232:235], v[28:31]
	v_mfma_f32_16x16x32_bf16 v[20:23], v[160:163], v[240:243], v[20:23]
	v_mfma_f32_16x16x32_bf16 v[12:15], v[168:171], v[240:243], v[12:15]
	s_setprio 1
	s_setprio 0
	v_mfma_f32_16x16x32_bf16 v[48:51], v[172:175], v[198:201], v[48:51]
	v_mfma_f32_16x16x32_bf16 v[40:43], v[180:183], v[198:201], v[40:43]
	v_mfma_f32_16x16x32_bf16 v[32:35], v[172:175], v[206:209], v[32:35]
	v_mfma_f32_16x16x32_bf16 v[24:27], v[180:183], v[206:209], v[24:27]
	v_mfma_f32_16x16x32_bf16 v[16:19], v[172:175], v[228:231], v[16:19]
	v_mfma_f32_16x16x32_bf16 v[8:11], v[180:183], v[228:231], v[8:11]
	v_mfma_f32_16x16x32_bf16 v[4:7], v[172:175], v[236:239], v[4:7]
	v_mfma_f32_16x16x32_bf16 v[0:3], v[180:183], v[236:239], v[0:3]
	v_mfma_f32_16x16x32_bf16 v[48:51], v[176:179], v[202:205], v[48:51]
	v_mfma_f32_16x16x32_bf16 v[40:43], v[194:197], v[202:205], v[40:43]
	v_mfma_f32_16x16x32_bf16 v[32:35], v[176:179], v[224:227], v[32:35]
	v_mfma_f32_16x16x32_bf16 v[24:27], v[194:197], v[224:227], v[24:27]
	v_mfma_f32_16x16x32_bf16 v[16:19], v[176:179], v[232:235], v[16:19]
	v_mfma_f32_16x16x32_bf16 v[8:11], v[194:197], v[232:235], v[8:11]
	v_mfma_f32_16x16x32_bf16 v[4:7], v[176:179], v[240:243], v[4:7]
	v_mfma_f32_16x16x32_bf16 v[0:3], v[194:197], v[240:243], v[0:3]
	s_setprio 1
	s_barrier
	s_add_i32 s47, s47, 2
	s_cmp_gt_u32 s47, 5
	s_mov_b64 s[16:17], s[18:19]
	s_cbranch_scc0 .LBB0_682
	s_and_b64 vcc, exec, s[6:7]
	s_cbranch_vccz .LBB0_685
	s_barrier

.LBB0_805:
	s_add_u32 s28, s30, 0xfff80080
	s_addc_u32 s29, s31, -1
	s_add_i32 s38, 0, 0x10000
	s_cmp_eq_u32 s78, 28
	s_cselect_b32 s45, s9, s29
	s_cselect_b32 s44, s11, s28
	s_cselect_b32 s41, s60, s63
	s_cselect_b32 s40, s61, s62
	s_add_i32 s39, 0, 0x14000
	v_add_u32_e32 v154, s38, v143
	v_add_u32_e32 v170, s39, v143
	ds_read_b128 v[138:141], v154
	ds_read_b128 v[146:149], v154 offset:1024
	ds_read_b128 v[150:153], v154 offset:2048
	ds_read_b128 v[154:157], v154 offset:3072
	ds_read_b128 v[158:161], v170
	ds_read_b128 v[162:165], v170 offset:1024
	ds_read_b128 v[166:169], v170 offset:2048
	ds_read_b128 v[170:173], v170 offset:3072
	v_lshl_add_u64 v[182:183], s[30:31], 0, v[134:135]
	s_add_i32 m0, s21, 0xc000
	ds_read_b128 v[174:177], v145
	ds_read_b128 v[178:181], v145 offset:1024
	ds_read_b128 v[194:197], v145 offset:2048
	ds_read_b128 v[198:201], v145 offset:3072
	ds_read_b128 v[202:205], v145 offset:4096
	ds_read_b128 v[206:209], v145 offset:5120
	ds_read_b128 v[224:227], v145 offset:6144
	ds_read_b128 v[228:231], v145 offset:7168
	global_load_lds_dwordx4 v[182:183], off
	v_lshl_add_u64 v[182:183], s[30:31], 0, v[136:137]
	s_add_i32 m0, s21, 0xe000
	s_nop 0
	global_load_lds_dwordx4 v[182:183], off
	s_waitcnt vmcnt(8)
	s_waitcnt lgkmcnt(0)
	s_barrier
	s_setprio 0
	s_waitcnt lgkmcnt(0)
	v_mfma_f32_16x16x32_bf16 v[124:127], v[138:141], v[174:177], v[124:127]
	v_mfma_f32_16x16x32_bf16 v[120:123], v[150:153], v[174:177], v[120:123]
	v_mfma_f32_16x16x32_bf16 v[116:119], v[138:141], v[194:197], v[116:119]
	v_mfma_f32_16x16x32_bf16 v[104:107], v[150:153], v[194:197], v[104:107]
	v_mfma_f32_16x16x32_bf16 v[100:103], v[138:141], v[202:205], v[100:103]
	v_mfma_f32_16x16x32_bf16 v[88:91], v[150:153], v[202:205], v[88:91]
	v_mfma_f32_16x16x32_bf16 v[84:87], v[138:141], v[224:227], v[84:87]
	v_mfma_f32_16x16x32_bf16 v[72:75], v[150:153], v[224:227], v[72:75]
	v_mfma_f32_16x16x32_bf16 v[124:127], v[146:149], v[178:181], v[124:127]
	v_mfma_f32_16x16x32_bf16 v[120:123], v[154:157], v[178:181], v[120:123]
	v_mfma_f32_16x16x32_bf16 v[116:119], v[146:149], v[198:201], v[116:119]
	v_mfma_f32_16x16x32_bf16 v[104:107], v[154:157], v[198:201], v[104:107]
	v_mfma_f32_16x16x32_bf16 v[100:103], v[146:149], v[206:209], v[100:103]
	v_mfma_f32_16x16x32_bf16 v[88:91], v[154:157], v[206:209], v[88:91]
	v_mfma_f32_16x16x32_bf16 v[84:87], v[146:149], v[228:231], v[84:87]
	v_mfma_f32_16x16x32_bf16 v[72:75], v[154:157], v[228:231], v[72:75]
	s_setprio 1
	s_setprio 0
	v_mfma_f32_16x16x32_bf16 v[112:115], v[158:161], v[174:177], v[112:115]
	v_mfma_f32_16x16x32_bf16 v[108:111], v[166:169], v[174:177], v[108:111]
	v_mfma_f32_16x16x32_bf16 v[96:99], v[158:161], v[194:197], v[96:99]
	v_mfma_f32_16x16x32_bf16 v[92:95], v[166:169], v[194:197], v[92:95]
	v_mfma_f32_16x16x32_bf16 v[80:83], v[158:161], v[202:205], v[80:83]
	v_mfma_f32_16x16x32_bf16 v[76:79], v[166:169], v[202:205], v[76:79]
	v_mfma_f32_16x16x32_bf16 v[68:71], v[158:161], v[224:227], v[68:71]
	v_mfma_f32_16x16x32_bf16 v[64:67], v[166:169], v[224:227], v[64:67]
	v_mfma_f32_16x16x32_bf16 v[112:115], v[162:165], v[178:181], v[112:115]
	v_mfma_f32_16x16x32_bf16 v[108:111], v[170:173], v[178:181], v[108:111]
	v_mfma_f32_16x16x32_bf16 v[96:99], v[162:165], v[198:201], v[96:99]
	v_mfma_f32_16x16x32_bf16 v[92:95], v[170:173], v[198:201], v[92:95]
	v_mfma_f32_16x16x32_bf16 v[80:83], v[162:165], v[206:209], v[80:83]
	v_mfma_f32_16x16x32_bf16 v[76:79], v[170:173], v[206:209], v[76:79]
	v_mfma_f32_16x16x32_bf16 v[68:71], v[162:165], v[228:231], v[68:71]
	v_mfma_f32_16x16x32_bf16 v[64:67], v[170:173], v[228:231], v[64:67]
	s_setprio 1
	s_barrier
	s_add_i32 s28, s38, s20
	v_lshl_add_u64 v[182:183], s[40:41], 0, v[184:185]
	s_mov_b32 m0, s28
	ds_read_b128 v[174:177], v145 offset:16384
	ds_read_b128 v[178:181], v145 offset:17408
	ds_read_b128 v[194:197], v145 offset:18432
	ds_read_b128 v[198:201], v145 offset:19456
	ds_read_b128 v[202:205], v145 offset:20480
	ds_read_b128 v[206:209], v145 offset:21504
	ds_read_b128 v[224:227], v145 offset:22528
	ds_read_b128 v[228:231], v145 offset:23552
	global_load_lds_dwordx4 v[182:183], off
	s_add_i32 m0, s28, 0x2000
	s_add_u32 s28, s40, 0x80000
	v_lshl_add_u64 v[210:211], s[40:41], 0, v[128:129]
	s_addc_u32 s29, s41, 0
	s_add_i32 s38, s39, s20
	global_load_lds_dwordx4 v[210:211], off
	v_lshl_add_u64 v[216:217], s[28:29], 0, v[184:185]
	s_mov_b32 m0, s38
	v_lshl_add_u64 v[218:219], s[44:45], 0, v[130:131]
	global_load_lds_dwordx4 v[216:217], off
	v_lshl_add_u64 v[216:217], s[28:29], 0, v[128:129]
	s_add_i32 m0, s38, 0x2000
	s_nop 0
	global_load_lds_dwordx4 v[216:217], off
	v_lshl_add_u64 v[216:217], s[44:45], 0, v[132:133]
	s_waitcnt vmcnt(6)
	s_waitcnt lgkmcnt(0)
	s_barrier
	s_setprio 0
	s_waitcnt lgkmcnt(0)
	v_mfma_f32_16x16x32_bf16 v[60:63], v[138:141], v[174:177], v[60:63]
	v_mfma_f32_16x16x32_bf16 v[56:59], v[150:153], v[174:177], v[56:59]
	v_mfma_f32_16x16x32_bf16 v[52:55], v[138:141], v[194:197], v[52:55]
	v_mfma_f32_16x16x32_bf16 v[40:43], v[150:153], v[194:197], v[40:43]
	v_mfma_f32_16x16x32_bf16 v[36:39], v[138:141], v[202:205], v[36:39]
	v_mfma_f32_16x16x32_bf16 v[24:27], v[150:153], v[202:205], v[24:27]
	v_mfma_f32_16x16x32_bf16 v[20:23], v[138:141], v[224:227], v[20:23]
	v_mfma_f32_16x16x32_bf16 v[8:11], v[150:153], v[224:227], v[8:11]
	v_mfma_f32_16x16x32_bf16 v[60:63], v[146:149], v[178:181], v[60:63]
	v_mfma_f32_16x16x32_bf16 v[56:59], v[154:157], v[178:181], v[56:59]
	v_mfma_f32_16x16x32_bf16 v[52:55], v[146:149], v[198:201], v[52:55]
	v_mfma_f32_16x16x32_bf16 v[40:43], v[154:157], v[198:201], v[40:43]
	v_mfma_f32_16x16x32_bf16 v[36:39], v[146:149], v[206:209], v[36:39]
	v_mfma_f32_16x16x32_bf16 v[24:27], v[154:157], v[206:209], v[24:27]
	v_mfma_f32_16x16x32_bf16 v[20:23], v[146:149], v[228:231], v[20:23]
	v_mfma_f32_16x16x32_bf16 v[8:11], v[154:157], v[228:231], v[8:11]
	s_setprio 1
	s_setprio 0
	v_mfma_f32_16x16x32_bf16 v[48:51], v[158:161], v[174:177], v[48:51]
	v_mfma_f32_16x16x32_bf16 v[44:47], v[166:169], v[174:177], v[44:47]
	v_mfma_f32_16x16x32_bf16 v[32:35], v[158:161], v[194:197], v[32:35]
	v_mfma_f32_16x16x32_bf16 v[28:31], v[166:169], v[194:197], v[28:31]
	v_mfma_f32_16x16x32_bf16 v[16:19], v[158:161], v[202:205], v[16:19]
	v_mfma_f32_16x16x32_bf16 v[12:15], v[166:169], v[202:205], v[12:15]
	v_mfma_f32_16x16x32_bf16 v[4:7], v[158:161], v[224:227], v[4:7]
	v_mfma_f32_16x16x32_bf16 v[0:3], v[166:169], v[224:227], v[0:3]
	v_mfma_f32_16x16x32_bf16 v[48:51], v[162:165], v[178:181], v[48:51]
	v_mfma_f32_16x16x32_bf16 v[44:47], v[170:173], v[178:181], v[44:47]
	v_mfma_f32_16x16x32_bf16 v[32:35], v[162:165], v[198:201], v[32:35]
	v_mfma_f32_16x16x32_bf16 v[28:31], v[170:173], v[198:201], v[28:31]
	v_mfma_f32_16x16x32_bf16 v[16:19], v[162:165], v[206:209], v[16:19]
	v_mfma_f32_16x16x32_bf16 v[12:15], v[170:173], v[206:209], v[12:15]
	v_mfma_f32_16x16x32_bf16 v[4:7], v[162:165], v[228:231], v[4:7]
	v_mfma_f32_16x16x32_bf16 v[0:3], v[170:173], v[228:231], v[0:3]
	s_setprio 1
	s_barrier
	s_add_i32 s38, 0, 0x18000
	s_add_i32 s39, 0, 0x1c000
	v_add_u32_e32 v154, s38, v143
	v_add_u32_e32 v170, s39, v143
	ds_read_b128 v[138:141], v154
	ds_read_b128 v[146:149], v154 offset:1024
	ds_read_b128 v[150:153], v154 offset:2048
	ds_read_b128 v[154:157], v154 offset:3072
	ds_read_b128 v[158:161], v170
	ds_read_b128 v[162:165], v170 offset:1024
	ds_read_b128 v[166:169], v170 offset:2048
	ds_read_b128 v[170:173], v170 offset:3072
	s_add_u32 s28, s44, 0x80000
	s_addc_u32 s29, s45, 0
	s_mov_b32 m0, s47
	v_lshl_add_u64 v[232:233], s[28:29], 0, v[132:133]
	ds_read_b128 v[174:177], v145 offset:32768
	ds_read_b128 v[178:181], v145 offset:33792
	ds_read_b128 v[194:197], v145 offset:34816
	ds_read_b128 v[198:201], v145 offset:35840
	ds_read_b128 v[202:205], v145 offset:36864
	ds_read_b128 v[206:209], v145 offset:37888
	ds_read_b128 v[224:227], v145 offset:38912
	ds_read_b128 v[228:231], v145 offset:39936
	global_load_lds_dwordx4 v[232:233], off
	v_lshl_add_u64 v[232:233], s[28:29], 0, v[130:131]
	s_mov_b32 m0, s50
	s_nop 0
	global_load_lds_dwordx4 v[232:233], off
	s_mov_b32 m0, s21
	s_nop 0
	global_load_lds_dwordx4 v[216:217], off
	s_mov_b32 m0, s46
	s_nop 0
	global_load_lds_dwordx4 v[218:219], off
	s_waitcnt vmcnt(8)
	s_waitcnt lgkmcnt(0)
	s_barrier
	s_setprio 0
	s_waitcnt lgkmcnt(0)
	v_mfma_f32_16x16x32_bf16 v[124:127], v[138:141], v[174:177], v[124:127]
	v_mfma_f32_16x16x32_bf16 v[120:123], v[150:153], v[174:177], v[120:123]
	v_mfma_f32_16x16x32_bf16 v[116:119], v[138:141], v[194:197], v[116:119]
	v_mfma_f32_16x16x32_bf16 v[104:107], v[150:153], v[194:197], v[104:107]
	v_mfma_f32_16x16x32_bf16 v[100:103], v[138:141], v[202:205], v[100:103]
	v_mfma_f32_16x16x32_bf16 v[88:91], v[150:153], v[202:205], v[88:91]
	v_mfma_f32_16x16x32_bf16 v[84:87], v[138:141], v[224:227], v[84:87]
	v_mfma_f32_16x16x32_bf16 v[72:75], v[150:153], v[224:227], v[72:75]
	v_mfma_f32_16x16x32_bf16 v[124:127], v[146:149], v[178:181], v[124:127]
	v_mfma_f32_16x16x32_bf16 v[120:123], v[154:157], v[178:181], v[120:123]
	v_mfma_f32_16x16x32_bf16 v[116:119], v[146:149], v[198:201], v[116:119]
	v_mfma_f32_16x16x32_bf16 v[104:107], v[154:157], v[198:201], v[104:107]
	v_mfma_f32_16x16x32_bf16 v[100:103], v[146:149], v[206:209], v[100:103]
	v_mfma_f32_16x16x32_bf16 v[88:91], v[154:157], v[206:209], v[88:91]
	v_mfma_f32_16x16x32_bf16 v[84:87], v[146:149], v[228:231], v[84:87]
	v_mfma_f32_16x16x32_bf16 v[72:75], v[154:157], v[228:231], v[72:75]
	s_setprio 1
	s_setprio 0
	v_mfma_f32_16x16x32_bf16 v[112:115], v[158:161], v[174:177], v[112:115]
	v_mfma_f32_16x16x32_bf16 v[108:111], v[166:169], v[174:177], v[108:111]
	v_mfma_f32_16x16x32_bf16 v[96:99], v[158:161], v[194:197], v[96:99]
	v_mfma_f32_16x16x32_bf16 v[92:95], v[166:169], v[194:197], v[92:95]
	v_mfma_f32_16x16x32_bf16 v[80:83], v[158:161], v[202:205], v[80:83]
	v_mfma_f32_16x16x32_bf16 v[76:79], v[166:169], v[202:205], v[76:79]
	v_mfma_f32_16x16x32_bf16 v[68:71], v[158:161], v[224:227], v[68:71]
	v_mfma_f32_16x16x32_bf16 v[64:67], v[166:169], v[224:227], v[64:67]
	v_mfma_f32_16x16x32_bf16 v[112:115], v[162:165], v[178:181], v[112:115]
	v_mfma_f32_16x16x32_bf16 v[108:111], v[170:173], v[178:181], v[108:111]
	v_mfma_f32_16x16x32_bf16 v[96:99], v[162:165], v[198:201], v[96:99]
	v_mfma_f32_16x16x32_bf16 v[92:95], v[170:173], v[198:201], v[92:95]
	v_mfma_f32_16x16x32_bf16 v[80:83], v[162:165], v[206:209], v[80:83]
	v_mfma_f32_16x16x32_bf16 v[76:79], v[170:173], v[206:209], v[76:79]
	v_mfma_f32_16x16x32_bf16 v[68:71], v[162:165], v[228:231], v[68:71]
	v_mfma_f32_16x16x32_bf16 v[64:67], v[170:173], v[228:231], v[64:67]
	s_setprio 1
	s_barrier
	s_add_i32 s28, s38, s20
	v_lshl_add_u64 v[182:183], v[182:183], 0, s[68:69]
	s_mov_b32 m0, s28
	ds_read_b128 v[174:177], v145 offset:49152
	ds_read_b128 v[178:181], v145 offset:50176
	ds_read_b128 v[194:197], v145 offset:51200
	ds_read_b128 v[198:201], v145 offset:52224
	ds_read_b128 v[202:205], v145 offset:53248
	ds_read_b128 v[206:209], v145 offset:54272
	ds_read_b128 v[224:227], v145 offset:55296
	ds_read_b128 v[228:231], v145 offset:56320
	global_load_lds_dwordx4 v[182:183], off
	s_add_i32 m0, s28, 0x2000
	s_add_u32 s28, s40, 0x80080
	v_lshl_add_u64 v[182:183], v[210:211], 0, s[68:69]
	s_addc_u32 s29, s41, 0
	s_add_i32 s38, s39, s20
	global_load_lds_dwordx4 v[182:183], off
	v_lshl_add_u64 v[182:183], s[28:29], 0, v[184:185]
	s_mov_b32 m0, s38
	s_nop 0
	global_load_lds_dwordx4 v[182:183], off
	v_lshl_add_u64 v[182:183], s[28:29], 0, v[128:129]
	s_add_i32 m0, s38, 0x2000
	s_nop 0
	global_load_lds_dwordx4 v[182:183], off
	v_lshl_add_u64 v[182:183], v[216:217], 0, s[68:69]
	s_mov_b32 m0, s51
	s_nop 0
	global_load_lds_dwordx4 v[182:183], off
	v_lshl_add_u64 v[182:183], v[218:219], 0, s[68:69]
	s_mov_b32 m0, s52
	s_nop 0
	global_load_lds_dwordx4 v[182:183], off
	s_waitcnt vmcnt(6)
	s_waitcnt lgkmcnt(0)
	s_barrier
	s_setprio 0
	s_waitcnt lgkmcnt(0)
	v_mfma_f32_16x16x32_bf16 v[60:63], v[138:141], v[174:177], v[60:63]
	v_mfma_f32_16x16x32_bf16 v[56:59], v[150:153], v[174:177], v[56:59]
	v_mfma_f32_16x16x32_bf16 v[52:55], v[138:141], v[194:197], v[52:55]
	v_mfma_f32_16x16x32_bf16 v[40:43], v[150:153], v[194:197], v[40:43]
	v_mfma_f32_16x16x32_bf16 v[36:39], v[138:141], v[202:205], v[36:39]
	v_mfma_f32_16x16x32_bf16 v[24:27], v[150:153], v[202:205], v[24:27]
	v_mfma_f32_16x16x32_bf16 v[20:23], v[138:141], v[224:227], v[20:23]
	v_mfma_f32_16x16x32_bf16 v[8:11], v[150:153], v[224:227], v[8:11]
	v_mfma_f32_16x16x32_bf16 v[60:63], v[146:149], v[178:181], v[60:63]
	v_mfma_f32_16x16x32_bf16 v[56:59], v[154:157], v[178:181], v[56:59]
	v_mfma_f32_16x16x32_bf16 v[52:55], v[146:149], v[198:201], v[52:55]
	v_mfma_f32_16x16x32_bf16 v[40:43], v[154:157], v[198:201], v[40:43]
	v_mfma_f32_16x16x32_bf16 v[36:39], v[146:149], v[206:209], v[36:39]
	v_mfma_f32_16x16x32_bf16 v[24:27], v[154:157], v[206:209], v[24:27]
	v_mfma_f32_16x16x32_bf16 v[20:23], v[146:149], v[228:231], v[20:23]
	v_mfma_f32_16x16x32_bf16 v[8:11], v[154:157], v[228:231], v[8:11]
	s_setprio 1
	s_setprio 0
	v_mfma_f32_16x16x32_bf16 v[48:51], v[158:161], v[174:177], v[48:51]
	v_mfma_f32_16x16x32_bf16 v[44:47], v[166:169], v[174:177], v[44:47]
	v_mfma_f32_16x16x32_bf16 v[32:35], v[158:161], v[194:197], v[32:35]
	v_mfma_f32_16x16x32_bf16 v[28:31], v[166:169], v[194:197], v[28:31]
	v_mfma_f32_16x16x32_bf16 v[16:19], v[158:161], v[202:205], v[16:19]
	v_mfma_f32_16x16x32_bf16 v[12:15], v[166:169], v[202:205], v[12:15]
	v_mfma_f32_16x16x32_bf16 v[4:7], v[158:161], v[224:227], v[4:7]
	v_mfma_f32_16x16x32_bf16 v[0:3], v[166:169], v[224:227], v[0:3]
	v_mfma_f32_16x16x32_bf16 v[48:51], v[162:165], v[178:181], v[48:51]
	v_mfma_f32_16x16x32_bf16 v[44:47], v[170:173], v[178:181], v[44:47]
	v_mfma_f32_16x16x32_bf16 v[32:35], v[162:165], v[198:201], v[32:35]
	v_mfma_f32_16x16x32_bf16 v[28:31], v[170:173], v[198:201], v[28:31]
	v_mfma_f32_16x16x32_bf16 v[16:19], v[162:165], v[206:209], v[16:19]
	v_mfma_f32_16x16x32_bf16 v[12:15], v[170:173], v[206:209], v[12:15]
	v_mfma_f32_16x16x32_bf16 v[4:7], v[162:165], v[228:231], v[4:7]
	v_mfma_f32_16x16x32_bf16 v[0:3], v[170:173], v[228:231], v[0:3]
	s_setprio 1
	s_barrier
	s_add_i32 s78, s78, 2
	s_add_u32 s30, s30, 0x100
	s_addc_u32 s31, s31, 0
	s_add_u32 s62, s62, 0x100
	s_addc_u32 s63, s63, 0
	s_cmp_gt_u32 s78, 29
	s_cbranch_scc0 .LBB0_805
	s_and_b64 vcc, exec, s[6:7]
	s_cbranch_vccz .LBB0_808
	s_barrier

.LBB0_842:
	s_add_u32 s28, s30, 0xfffc0080
	s_addc_u32 s29, s31, -1
	s_add_i32 s42, 0, 0x10000
	s_cmp_eq_u32 s60, 12
	s_cselect_b32 s45, s9, s29
	s_cselect_b32 s44, s11, s28
	s_cselect_b32 s41, s36, s59
	s_cselect_b32 s40, s37, s58
	s_add_i32 s43, 0, 0x14000
	v_add_u32_e32 v154, s42, v147
	v_add_u32_e32 v170, s43, v147
	ds_read_b128 v[138:141], v154
	ds_read_b128 v[142:145], v154 offset:1024
	ds_read_b128 v[150:153], v154 offset:2048
	ds_read_b128 v[154:157], v154 offset:3072
	ds_read_b128 v[158:161], v170
	ds_read_b128 v[162:165], v170 offset:1024
	ds_read_b128 v[166:169], v170 offset:2048
	ds_read_b128 v[170:173], v170 offset:3072
	v_lshl_add_u64 v[182:183], s[30:31], 0, v[134:135]
	s_add_i32 m0, s21, 0xc000
	ds_read_b128 v[174:177], v149
	ds_read_b128 v[178:181], v149 offset:1024
	ds_read_b128 v[194:197], v149 offset:2048
	ds_read_b128 v[198:201], v149 offset:3072
	ds_read_b128 v[202:205], v149 offset:4096
	ds_read_b128 v[206:209], v149 offset:5120
	ds_read_b128 v[224:227], v149 offset:6144
	ds_read_b128 v[228:231], v149 offset:7168
	global_load_lds_dwordx4 v[182:183], off
	v_lshl_add_u64 v[182:183], s[30:31], 0, v[136:137]
	s_add_i32 m0, s21, 0xe000
	s_nop 0
	global_load_lds_dwordx4 v[182:183], off
	s_waitcnt vmcnt(8)
	s_waitcnt lgkmcnt(0)
	s_barrier
	s_setprio 0
	s_waitcnt lgkmcnt(0)
	v_mfma_f32_16x16x32_bf16 v[124:127], v[138:141], v[174:177], v[124:127]
	v_mfma_f32_16x16x32_bf16 v[120:123], v[150:153], v[174:177], v[120:123]
	v_mfma_f32_16x16x32_bf16 v[108:111], v[138:141], v[194:197], v[108:111]
	v_mfma_f32_16x16x32_bf16 v[104:107], v[150:153], v[194:197], v[104:107]
	v_mfma_f32_16x16x32_bf16 v[92:95], v[138:141], v[202:205], v[92:95]
	v_mfma_f32_16x16x32_bf16 v[88:91], v[150:153], v[202:205], v[88:91]
	v_mfma_f32_16x16x32_bf16 v[76:79], v[138:141], v[224:227], v[76:79]
	v_mfma_f32_16x16x32_bf16 v[72:75], v[150:153], v[224:227], v[72:75]
	v_mfma_f32_16x16x32_bf16 v[124:127], v[142:145], v[178:181], v[124:127]
	v_mfma_f32_16x16x32_bf16 v[120:123], v[154:157], v[178:181], v[120:123]
	v_mfma_f32_16x16x32_bf16 v[108:111], v[142:145], v[198:201], v[108:111]
	v_mfma_f32_16x16x32_bf16 v[104:107], v[154:157], v[198:201], v[104:107]
	v_mfma_f32_16x16x32_bf16 v[92:95], v[142:145], v[206:209], v[92:95]
	v_mfma_f32_16x16x32_bf16 v[88:91], v[154:157], v[206:209], v[88:91]
	v_mfma_f32_16x16x32_bf16 v[76:79], v[142:145], v[228:231], v[76:79]
	v_mfma_f32_16x16x32_bf16 v[72:75], v[154:157], v[228:231], v[72:75]
	s_setprio 1
	s_setprio 0
	v_mfma_f32_16x16x32_bf16 v[116:119], v[158:161], v[174:177], v[116:119]
	v_mfma_f32_16x16x32_bf16 v[112:115], v[166:169], v[174:177], v[112:115]
	v_mfma_f32_16x16x32_bf16 v[100:103], v[158:161], v[194:197], v[100:103]
	v_mfma_f32_16x16x32_bf16 v[96:99], v[166:169], v[194:197], v[96:99]
	v_mfma_f32_16x16x32_bf16 v[84:87], v[158:161], v[202:205], v[84:87]
	v_mfma_f32_16x16x32_bf16 v[80:83], v[166:169], v[202:205], v[80:83]
	v_mfma_f32_16x16x32_bf16 v[68:71], v[158:161], v[224:227], v[68:71]
	v_mfma_f32_16x16x32_bf16 v[64:67], v[166:169], v[224:227], v[64:67]
	v_mfma_f32_16x16x32_bf16 v[116:119], v[162:165], v[178:181], v[116:119]
	v_mfma_f32_16x16x32_bf16 v[112:115], v[170:173], v[178:181], v[112:115]
	v_mfma_f32_16x16x32_bf16 v[100:103], v[162:165], v[198:201], v[100:103]
	v_mfma_f32_16x16x32_bf16 v[96:99], v[170:173], v[198:201], v[96:99]
	v_mfma_f32_16x16x32_bf16 v[84:87], v[162:165], v[206:209], v[84:87]
	v_mfma_f32_16x16x32_bf16 v[80:83], v[170:173], v[206:209], v[80:83]
	v_mfma_f32_16x16x32_bf16 v[68:71], v[162:165], v[228:231], v[68:71]
	v_mfma_f32_16x16x32_bf16 v[64:67], v[170:173], v[228:231], v[64:67]
	s_setprio 1
	s_barrier
	s_add_i32 s28, s42, s20
	v_lshl_add_u64 v[182:183], s[40:41], 0, v[184:185]
	s_mov_b32 m0, s28
	ds_read_b128 v[174:177], v149 offset:16384
	ds_read_b128 v[178:181], v149 offset:17408
	ds_read_b128 v[194:197], v149 offset:18432
	ds_read_b128 v[198:201], v149 offset:19456
	ds_read_b128 v[202:205], v149 offset:20480
	ds_read_b128 v[206:209], v149 offset:21504
	ds_read_b128 v[224:227], v149 offset:22528
	ds_read_b128 v[228:231], v149 offset:23552
	global_load_lds_dwordx4 v[182:183], off
	s_add_i32 m0, s28, 0x2000
	s_add_u32 s28, s40, 0x40000
	v_lshl_add_u64 v[210:211], s[40:41], 0, v[128:129]
	s_addc_u32 s29, s41, 0
	s_add_i32 s42, s43, s20
	global_load_lds_dwordx4 v[210:211], off
	v_lshl_add_u64 v[216:217], s[28:29], 0, v[184:185]
	s_mov_b32 m0, s42
	v_lshl_add_u64 v[218:219], s[44:45], 0, v[130:131]
	global_load_lds_dwordx4 v[216:217], off
	v_lshl_add_u64 v[216:217], s[28:29], 0, v[128:129]
	s_add_i32 m0, s42, 0x2000
	s_nop 0
	global_load_lds_dwordx4 v[216:217], off
	v_lshl_add_u64 v[216:217], s[44:45], 0, v[132:133]
	s_waitcnt vmcnt(6)
	s_waitcnt lgkmcnt(0)
	s_barrier
	s_setprio 0
	s_waitcnt lgkmcnt(0)
	v_mfma_f32_16x16x32_bf16 v[60:63], v[138:141], v[174:177], v[60:63]
	v_mfma_f32_16x16x32_bf16 v[56:59], v[150:153], v[174:177], v[56:59]
	v_mfma_f32_16x16x32_bf16 v[44:47], v[138:141], v[194:197], v[44:47]
	v_mfma_f32_16x16x32_bf16 v[40:43], v[150:153], v[194:197], v[40:43]
	v_mfma_f32_16x16x32_bf16 v[28:31], v[138:141], v[202:205], v[28:31]
	v_mfma_f32_16x16x32_bf16 v[24:27], v[150:153], v[202:205], v[24:27]
	v_mfma_f32_16x16x32_bf16 v[12:15], v[138:141], v[224:227], v[12:15]
	v_mfma_f32_16x16x32_bf16 v[8:11], v[150:153], v[224:227], v[8:11]
	v_mfma_f32_16x16x32_bf16 v[60:63], v[142:145], v[178:181], v[60:63]
	v_mfma_f32_16x16x32_bf16 v[56:59], v[154:157], v[178:181], v[56:59]
	v_mfma_f32_16x16x32_bf16 v[44:47], v[142:145], v[198:201], v[44:47]
	v_mfma_f32_16x16x32_bf16 v[40:43], v[154:157], v[198:201], v[40:43]
	v_mfma_f32_16x16x32_bf16 v[28:31], v[142:145], v[206:209], v[28:31]
	v_mfma_f32_16x16x32_bf16 v[24:27], v[154:157], v[206:209], v[24:27]
	v_mfma_f32_16x16x32_bf16 v[12:15], v[142:145], v[228:231], v[12:15]
	v_mfma_f32_16x16x32_bf16 v[8:11], v[154:157], v[228:231], v[8:11]
	s_setprio 1
	s_setprio 0
	v_mfma_f32_16x16x32_bf16 v[52:55], v[158:161], v[174:177], v[52:55]
	v_mfma_f32_16x16x32_bf16 v[48:51], v[166:169], v[174:177], v[48:51]
	v_mfma_f32_16x16x32_bf16 v[36:39], v[158:161], v[194:197], v[36:39]
	v_mfma_f32_16x16x32_bf16 v[32:35], v[166:169], v[194:197], v[32:35]
	v_mfma_f32_16x16x32_bf16 v[20:23], v[158:161], v[202:205], v[20:23]
	v_mfma_f32_16x16x32_bf16 v[16:19], v[166:169], v[202:205], v[16:19]
	v_mfma_f32_16x16x32_bf16 v[4:7], v[158:161], v[224:227], v[4:7]
	v_mfma_f32_16x16x32_bf16 v[0:3], v[166:169], v[224:227], v[0:3]
	v_mfma_f32_16x16x32_bf16 v[52:55], v[162:165], v[178:181], v[52:55]
	v_mfma_f32_16x16x32_bf16 v[48:51], v[170:173], v[178:181], v[48:51]
	v_mfma_f32_16x16x32_bf16 v[36:39], v[162:165], v[198:201], v[36:39]
	v_mfma_f32_16x16x32_bf16 v[32:35], v[170:173], v[198:201], v[32:35]
	v_mfma_f32_16x16x32_bf16 v[20:23], v[162:165], v[206:209], v[20:23]
	v_mfma_f32_16x16x32_bf16 v[16:19], v[170:173], v[206:209], v[16:19]
	v_mfma_f32_16x16x32_bf16 v[4:7], v[162:165], v[228:231], v[4:7]
	v_mfma_f32_16x16x32_bf16 v[0:3], v[170:173], v[228:231], v[0:3]
	s_setprio 1
	s_barrier
	s_add_i32 s42, 0, 0x18000
	s_add_i32 s43, 0, 0x1c000
	v_add_u32_e32 v154, s42, v147
	v_add_u32_e32 v170, s43, v147
	ds_read_b128 v[138:141], v154
	ds_read_b128 v[142:145], v154 offset:1024
	ds_read_b128 v[150:153], v154 offset:2048
	ds_read_b128 v[154:157], v154 offset:3072
	ds_read_b128 v[158:161], v170
	ds_read_b128 v[162:165], v170 offset:1024
	ds_read_b128 v[166:169], v170 offset:2048
	ds_read_b128 v[170:173], v170 offset:3072
	s_add_u32 s28, s44, 0x40000
	s_addc_u32 s29, s45, 0
	s_mov_b32 m0, s27
	v_lshl_add_u64 v[232:233], s[28:29], 0, v[132:133]
	ds_read_b128 v[174:177], v149 offset:32768
	ds_read_b128 v[178:181], v149 offset:33792
	ds_read_b128 v[194:197], v149 offset:34816
	ds_read_b128 v[198:201], v149 offset:35840
	ds_read_b128 v[202:205], v149 offset:36864
	ds_read_b128 v[206:209], v149 offset:37888
	ds_read_b128 v[224:227], v149 offset:38912
	ds_read_b128 v[228:231], v149 offset:39936
	global_load_lds_dwordx4 v[232:233], off
	v_lshl_add_u64 v[232:233], s[28:29], 0, v[130:131]
	s_mov_b32 m0, s46
	s_nop 0
	global_load_lds_dwordx4 v[232:233], off
	s_mov_b32 m0, s21
	s_nop 0
	global_load_lds_dwordx4 v[216:217], off
	s_mov_b32 m0, s26
	s_nop 0
	global_load_lds_dwordx4 v[218:219], off
	s_waitcnt vmcnt(8)
	s_waitcnt lgkmcnt(0)
	s_barrier
	s_setprio 0
	s_waitcnt lgkmcnt(0)
	v_mfma_f32_16x16x32_bf16 v[124:127], v[138:141], v[174:177], v[124:127]
	v_mfma_f32_16x16x32_bf16 v[120:123], v[150:153], v[174:177], v[120:123]
	v_mfma_f32_16x16x32_bf16 v[108:111], v[138:141], v[194:197], v[108:111]
	v_mfma_f32_16x16x32_bf16 v[104:107], v[150:153], v[194:197], v[104:107]
	v_mfma_f32_16x16x32_bf16 v[92:95], v[138:141], v[202:205], v[92:95]
	v_mfma_f32_16x16x32_bf16 v[88:91], v[150:153], v[202:205], v[88:91]
	v_mfma_f32_16x16x32_bf16 v[76:79], v[138:141], v[224:227], v[76:79]
	v_mfma_f32_16x16x32_bf16 v[72:75], v[150:153], v[224:227], v[72:75]
	v_mfma_f32_16x16x32_bf16 v[124:127], v[142:145], v[178:181], v[124:127]
	v_mfma_f32_16x16x32_bf16 v[120:123], v[154:157], v[178:181], v[120:123]
	v_mfma_f32_16x16x32_bf16 v[108:111], v[142:145], v[198:201], v[108:111]
	v_mfma_f32_16x16x32_bf16 v[104:107], v[154:157], v[198:201], v[104:107]
	v_mfma_f32_16x16x32_bf16 v[92:95], v[142:145], v[206:209], v[92:95]
	v_mfma_f32_16x16x32_bf16 v[88:91], v[154:157], v[206:209], v[88:91]
	v_mfma_f32_16x16x32_bf16 v[76:79], v[142:145], v[228:231], v[76:79]
	v_mfma_f32_16x16x32_bf16 v[72:75], v[154:157], v[228:231], v[72:75]
	s_setprio 1
	s_setprio 0
	v_mfma_f32_16x16x32_bf16 v[116:119], v[158:161], v[174:177], v[116:119]
	v_mfma_f32_16x16x32_bf16 v[112:115], v[166:169], v[174:177], v[112:115]
	v_mfma_f32_16x16x32_bf16 v[100:103], v[158:161], v[194:197], v[100:103]
	v_mfma_f32_16x16x32_bf16 v[96:99], v[166:169], v[194:197], v[96:99]
	v_mfma_f32_16x16x32_bf16 v[84:87], v[158:161], v[202:205], v[84:87]
	v_mfma_f32_16x16x32_bf16 v[80:83], v[166:169], v[202:205], v[80:83]
	v_mfma_f32_16x16x32_bf16 v[68:71], v[158:161], v[224:227], v[68:71]
	v_mfma_f32_16x16x32_bf16 v[64:67], v[166:169], v[224:227], v[64:67]
	v_mfma_f32_16x16x32_bf16 v[116:119], v[162:165], v[178:181], v[116:119]
	v_mfma_f32_16x16x32_bf16 v[112:115], v[170:173], v[178:181], v[112:115]
	v_mfma_f32_16x16x32_bf16 v[100:103], v[162:165], v[198:201], v[100:103]
	v_mfma_f32_16x16x32_bf16 v[96:99], v[170:173], v[198:201], v[96:99]
	v_mfma_f32_16x16x32_bf16 v[84:87], v[162:165], v[206:209], v[84:87]
	v_mfma_f32_16x16x32_bf16 v[80:83], v[170:173], v[206:209], v[80:83]
	v_mfma_f32_16x16x32_bf16 v[68:71], v[162:165], v[228:231], v[68:71]
	v_mfma_f32_16x16x32_bf16 v[64:67], v[170:173], v[228:231], v[64:67]
	s_setprio 1
	s_barrier
	s_add_i32 s28, s42, s20
	v_lshl_add_u64 v[182:183], v[182:183], 0, s[68:69]
	s_mov_b32 m0, s28
	ds_read_b128 v[174:177], v149 offset:49152
	ds_read_b128 v[178:181], v149 offset:50176
	ds_read_b128 v[194:197], v149 offset:51200
	ds_read_b128 v[198:201], v149 offset:52224
	ds_read_b128 v[202:205], v149 offset:53248
	ds_read_b128 v[206:209], v149 offset:54272
	ds_read_b128 v[224:227], v149 offset:55296
	ds_read_b128 v[228:231], v149 offset:56320
	global_load_lds_dwordx4 v[182:183], off
	s_add_i32 m0, s28, 0x2000
	s_add_u32 s28, s40, 0x40080
	v_lshl_add_u64 v[182:183], v[210:211], 0, s[68:69]
	s_addc_u32 s29, s41, 0
	s_add_i32 s40, s43, s20
	global_load_lds_dwordx4 v[182:183], off
	v_lshl_add_u64 v[182:183], s[28:29], 0, v[184:185]
	s_mov_b32 m0, s40
	s_nop 0
	global_load_lds_dwordx4 v[182:183], off
	v_lshl_add_u64 v[182:183], s[28:29], 0, v[128:129]
	s_add_i32 m0, s40, 0x2000
	s_nop 0
	global_load_lds_dwordx4 v[182:183], off
	v_lshl_add_u64 v[182:183], v[216:217], 0, s[68:69]
	s_mov_b32 m0, s47
	s_nop 0
	global_load_lds_dwordx4 v[182:183], off
	v_lshl_add_u64 v[182:183], v[218:219], 0, s[68:69]
	s_mov_b32 m0, s50
	s_nop 0
	global_load_lds_dwordx4 v[182:183], off
	s_waitcnt vmcnt(6)
	s_waitcnt lgkmcnt(0)
	s_barrier
	s_setprio 0
	s_waitcnt lgkmcnt(0)
	v_mfma_f32_16x16x32_bf16 v[60:63], v[138:141], v[174:177], v[60:63]
	v_mfma_f32_16x16x32_bf16 v[56:59], v[150:153], v[174:177], v[56:59]
	v_mfma_f32_16x16x32_bf16 v[44:47], v[138:141], v[194:197], v[44:47]
	v_mfma_f32_16x16x32_bf16 v[40:43], v[150:153], v[194:197], v[40:43]
	v_mfma_f32_16x16x32_bf16 v[28:31], v[138:141], v[202:205], v[28:31]
	v_mfma_f32_16x16x32_bf16 v[24:27], v[150:153], v[202:205], v[24:27]
	v_mfma_f32_16x16x32_bf16 v[12:15], v[138:141], v[224:227], v[12:15]
	v_mfma_f32_16x16x32_bf16 v[8:11], v[150:153], v[224:227], v[8:11]
	v_mfma_f32_16x16x32_bf16 v[60:63], v[142:145], v[178:181], v[60:63]
	v_mfma_f32_16x16x32_bf16 v[56:59], v[154:157], v[178:181], v[56:59]
	v_mfma_f32_16x16x32_bf16 v[44:47], v[142:145], v[198:201], v[44:47]
	v_mfma_f32_16x16x32_bf16 v[40:43], v[154:157], v[198:201], v[40:43]
	v_mfma_f32_16x16x32_bf16 v[28:31], v[142:145], v[206:209], v[28:31]
	v_mfma_f32_16x16x32_bf16 v[24:27], v[154:157], v[206:209], v[24:27]
	v_mfma_f32_16x16x32_bf16 v[12:15], v[142:145], v[228:231], v[12:15]
	v_mfma_f32_16x16x32_bf16 v[8:11], v[154:157], v[228:231], v[8:11]
	s_setprio 1
	s_setprio 0
	v_mfma_f32_16x16x32_bf16 v[52:55], v[158:161], v[174:177], v[52:55]
	v_mfma_f32_16x16x32_bf16 v[48:51], v[166:169], v[174:177], v[48:51]
	v_mfma_f32_16x16x32_bf16 v[36:39], v[158:161], v[194:197], v[36:39]
	v_mfma_f32_16x16x32_bf16 v[32:35], v[166:169], v[194:197], v[32:35]
	v_mfma_f32_16x16x32_bf16 v[20:23], v[158:161], v[202:205], v[20:23]
	v_mfma_f32_16x16x32_bf16 v[16:19], v[166:169], v[202:205], v[16:19]
	v_mfma_f32_16x16x32_bf16 v[4:7], v[158:161], v[224:227], v[4:7]
	v_mfma_f32_16x16x32_bf16 v[0:3], v[166:169], v[224:227], v[0:3]
	v_mfma_f32_16x16x32_bf16 v[52:55], v[162:165], v[178:181], v[52:55]
	v_mfma_f32_16x16x32_bf16 v[48:51], v[170:173], v[178:181], v[48:51]
	v_mfma_f32_16x16x32_bf16 v[36:39], v[162:165], v[198:201], v[36:39]
	v_mfma_f32_16x16x32_bf16 v[32:35], v[170:173], v[198:201], v[32:35]
	v_mfma_f32_16x16x32_bf16 v[20:23], v[162:165], v[206:209], v[20:23]
	v_mfma_f32_16x16x32_bf16 v[16:19], v[170:173], v[206:209], v[16:19]
	v_mfma_f32_16x16x32_bf16 v[4:7], v[162:165], v[228:231], v[4:7]
	v_mfma_f32_16x16x32_bf16 v[0:3], v[170:173], v[228:231], v[0:3]
	s_setprio 1
	s_barrier
	s_add_i32 s60, s60, 2
	s_add_u32 s30, s30, 0x100
	s_addc_u32 s31, s31, 0
	s_add_u32 s58, s58, 0x100
	s_addc_u32 s59, s59, 0
	s_cmp_gt_u32 s60, 13
	s_cbranch_scc0 .LBB0_842
	s_and_b64 vcc, exec, s[6:7]
	s_cbranch_vccz .LBB0_845
	s_barrier

.LBB0_991:
	s_add_u32 s28, s40, 0xfff80080
	s_addc_u32 s29, s41, -1
	s_add_i32 s48, 0, 0x10000
	s_cmp_eq_u32 s79, 28
	s_cselect_b32 s45, s11, s29
	s_cselect_b32 s44, s13, s28
	s_cselect_b32 s43, s60, s63
	s_cselect_b32 s42, s61, s62
	s_add_i32 s49, 0, 0x14000
	s_waitcnt vmcnt(0)
	v_add_u32_e32 v60, s48, v169
	v_add_u32_e32 v166, s49, v169
	ds_read_b128 v[40:43], v60
	ds_read_b128 v[44:47], v60 offset:1024
	ds_read_b128 v[56:59], v60 offset:2048
	ds_read_b128 v[60:63], v60 offset:3072
	ds_read_b128 v[144:147], v166
	ds_read_b128 v[148:151], v166 offset:1024
	ds_read_b128 v[162:165], v166 offset:2048
	ds_read_b128 v[172:175], v166 offset:3072
	v_lshl_add_u64 v[166:167], s[40:41], 0, v[158:159]
	s_add_i32 m0, s26, 0xc000
	ds_read_b128 v[176:179], v171
	ds_read_b128 v[180:183], v171 offset:1024
	ds_read_b128 v[194:197], v171 offset:2048
	ds_read_b128 v[198:201], v171 offset:3072
	ds_read_b128 v[202:205], v171 offset:4096
	ds_read_b128 v[206:209], v171 offset:5120
	ds_read_b128 v[224:227], v171 offset:6144
	ds_read_b128 v[228:231], v171 offset:7168
	global_load_lds_dwordx4 v[166:167], off
	v_lshl_add_u64 v[166:167], s[40:41], 0, v[160:161]
	s_add_i32 m0, s26, 0xe000
	s_nop 0
	global_load_lds_dwordx4 v[166:167], off
	s_waitcnt vmcnt(8)
	s_waitcnt lgkmcnt(0)
	s_barrier
	s_setprio 0
	s_waitcnt lgkmcnt(0)
	v_mfma_f32_16x16x32_bf16 v[140:143], v[40:43], v[176:179], v[140:143]
	v_mfma_f32_16x16x32_bf16 v[136:139], v[56:59], v[176:179], v[136:139]
	v_mfma_f32_16x16x32_bf16 v[124:127], v[40:43], v[194:197], v[124:127]
	v_mfma_f32_16x16x32_bf16 v[120:123], v[56:59], v[194:197], v[120:123]
	v_mfma_f32_16x16x32_bf16 v[108:111], v[40:43], v[202:205], v[108:111]
	v_mfma_f32_16x16x32_bf16 v[104:107], v[56:59], v[202:205], v[104:107]
	v_mfma_f32_16x16x32_bf16 v[92:95], v[40:43], v[224:227], v[92:95]
	v_mfma_f32_16x16x32_bf16 v[88:91], v[56:59], v[224:227], v[88:91]
	v_mfma_f32_16x16x32_bf16 v[140:143], v[44:47], v[180:183], v[140:143]
	v_mfma_f32_16x16x32_bf16 v[136:139], v[60:63], v[180:183], v[136:139]
	v_mfma_f32_16x16x32_bf16 v[124:127], v[44:47], v[198:201], v[124:127]
	v_mfma_f32_16x16x32_bf16 v[120:123], v[60:63], v[198:201], v[120:123]
	v_mfma_f32_16x16x32_bf16 v[108:111], v[44:47], v[206:209], v[108:111]
	v_mfma_f32_16x16x32_bf16 v[104:107], v[60:63], v[206:209], v[104:107]
	v_mfma_f32_16x16x32_bf16 v[92:95], v[44:47], v[228:231], v[92:95]
	v_mfma_f32_16x16x32_bf16 v[88:91], v[60:63], v[228:231], v[88:91]
	s_setprio 1
	s_setprio 0
	v_mfma_f32_16x16x32_bf16 v[132:135], v[144:147], v[176:179], v[132:135]
	v_mfma_f32_16x16x32_bf16 v[128:131], v[162:165], v[176:179], v[128:131]
	v_mfma_f32_16x16x32_bf16 v[116:119], v[144:147], v[194:197], v[116:119]
	v_mfma_f32_16x16x32_bf16 v[112:115], v[162:165], v[194:197], v[112:115]
	v_mfma_f32_16x16x32_bf16 v[100:103], v[144:147], v[202:205], v[100:103]
	v_mfma_f32_16x16x32_bf16 v[96:99], v[162:165], v[202:205], v[96:99]
	v_mfma_f32_16x16x32_bf16 v[84:87], v[144:147], v[224:227], v[84:87]
	v_mfma_f32_16x16x32_bf16 v[80:83], v[162:165], v[224:227], v[80:83]
	v_mfma_f32_16x16x32_bf16 v[132:135], v[148:151], v[180:183], v[132:135]
	v_mfma_f32_16x16x32_bf16 v[128:131], v[172:175], v[180:183], v[128:131]
	v_mfma_f32_16x16x32_bf16 v[116:119], v[148:151], v[198:201], v[116:119]
	v_mfma_f32_16x16x32_bf16 v[112:115], v[172:175], v[198:201], v[112:115]
	v_mfma_f32_16x16x32_bf16 v[100:103], v[148:151], v[206:209], v[100:103]
	v_mfma_f32_16x16x32_bf16 v[96:99], v[172:175], v[206:209], v[96:99]
	v_mfma_f32_16x16x32_bf16 v[84:87], v[148:151], v[228:231], v[84:87]
	v_mfma_f32_16x16x32_bf16 v[80:83], v[172:175], v[228:231], v[80:83]
	s_setprio 1
	s_barrier
	s_add_i32 s28, s48, s46
	v_lshl_add_u64 v[166:167], s[42:43], 0, v[184:185]
	s_mov_b32 m0, s28
	ds_read_b128 v[176:179], v171 offset:16384
	ds_read_b128 v[180:183], v171 offset:17408
	ds_read_b128 v[194:197], v171 offset:18432
	ds_read_b128 v[198:201], v171 offset:19456
	ds_read_b128 v[202:205], v171 offset:20480
	ds_read_b128 v[206:209], v171 offset:21504
	ds_read_b128 v[224:227], v171 offset:22528
	ds_read_b128 v[228:231], v171 offset:23552
	global_load_lds_dwordx4 v[166:167], off
	s_add_i32 m0, s28, 0x2000
	s_add_u32 s28, s42, 0x80000
	v_lshl_add_u64 v[210:211], s[42:43], 0, v[152:153]
	s_addc_u32 s29, s43, 0
	s_add_i32 s48, s49, s46
	global_load_lds_dwordx4 v[210:211], off
	v_lshl_add_u64 v[216:217], s[28:29], 0, v[184:185]
	s_mov_b32 m0, s48
	v_lshl_add_u64 v[218:219], s[44:45], 0, v[154:155]
	global_load_lds_dwordx4 v[216:217], off
	v_lshl_add_u64 v[216:217], s[28:29], 0, v[152:153]
	s_add_i32 m0, s48, 0x2000
	s_nop 0
	global_load_lds_dwordx4 v[216:217], off
	v_lshl_add_u64 v[216:217], s[44:45], 0, v[156:157]
	s_waitcnt vmcnt(6)
	s_waitcnt lgkmcnt(0)
	s_barrier
	s_setprio 0
	s_waitcnt lgkmcnt(0)
	v_mfma_f32_16x16x32_bf16 v[76:79], v[40:43], v[176:179], v[76:79]
	v_mfma_f32_16x16x32_bf16 v[72:75], v[56:59], v[176:179], v[72:75]
	v_mfma_f32_16x16x32_bf16 v[52:55], v[40:43], v[194:197], v[52:55]
	v_mfma_f32_16x16x32_bf16 v[48:51], v[56:59], v[194:197], v[48:51]
	v_mfma_f32_16x16x32_bf16 v[28:31], v[40:43], v[202:205], v[28:31]
	v_mfma_f32_16x16x32_bf16 v[24:27], v[56:59], v[202:205], v[24:27]
	v_mfma_f32_16x16x32_bf16 v[12:15], v[40:43], v[224:227], v[12:15]
	v_mfma_f32_16x16x32_bf16 v[8:11], v[56:59], v[224:227], v[8:11]
	v_mfma_f32_16x16x32_bf16 v[76:79], v[44:47], v[180:183], v[76:79]
	v_mfma_f32_16x16x32_bf16 v[72:75], v[60:63], v[180:183], v[72:75]
	v_mfma_f32_16x16x32_bf16 v[52:55], v[44:47], v[198:201], v[52:55]
	v_mfma_f32_16x16x32_bf16 v[48:51], v[60:63], v[198:201], v[48:51]
	v_mfma_f32_16x16x32_bf16 v[28:31], v[44:47], v[206:209], v[28:31]
	v_mfma_f32_16x16x32_bf16 v[24:27], v[60:63], v[206:209], v[24:27]
	v_mfma_f32_16x16x32_bf16 v[12:15], v[44:47], v[228:231], v[12:15]
	v_mfma_f32_16x16x32_bf16 v[8:11], v[60:63], v[228:231], v[8:11]
	s_setprio 1
	s_setprio 0
	v_mfma_f32_16x16x32_bf16 v[36:39], v[144:147], v[194:197], v[36:39]
	v_mfma_f32_16x16x32_bf16 v[32:35], v[162:165], v[194:197], v[32:35]
	v_mfma_f32_16x16x32_bf16 v[20:23], v[144:147], v[202:205], v[20:23]
	v_mfma_f32_16x16x32_bf16 v[16:19], v[162:165], v[202:205], v[16:19]
	v_mfma_f32_16x16x32_bf16 v[4:7], v[144:147], v[224:227], v[4:7]
	v_mfma_f32_16x16x32_bf16 v[0:3], v[162:165], v[224:227], v[0:3]
	v_mfma_f32_16x16x32_bf16 v[40:43], v[144:147], v[176:179], v[68:71]
	v_mfma_f32_16x16x32_bf16 v[44:47], v[162:165], v[176:179], v[64:67]
	v_mfma_f32_16x16x32_bf16 v[36:39], v[148:151], v[198:201], v[36:39]
	v_mfma_f32_16x16x32_bf16 v[32:35], v[172:175], v[198:201], v[32:35]
	v_mfma_f32_16x16x32_bf16 v[20:23], v[148:151], v[206:209], v[20:23]
	v_mfma_f32_16x16x32_bf16 v[16:19], v[172:175], v[206:209], v[16:19]
	v_mfma_f32_16x16x32_bf16 v[4:7], v[148:151], v[228:231], v[4:7]
	v_mfma_f32_16x16x32_bf16 v[0:3], v[172:175], v[228:231], v[0:3]
	v_mfma_f32_16x16x32_bf16 v[40:43], v[148:151], v[180:183], v[40:43]
	v_mfma_f32_16x16x32_bf16 v[44:47], v[172:175], v[180:183], v[44:47]
	s_setprio 1
	s_barrier
	s_add_i32 s48, 0, 0x18000
	s_add_i32 s49, 0, 0x1c000
	v_add_u32_e32 v68, s48, v169
	v_add_u32_e32 v172, s49, v169
	ds_read_b128 v[56:59], v68
	ds_read_b128 v[60:63], v68 offset:1024
	ds_read_b128 v[64:67], v68 offset:2048
	ds_read_b128 v[68:71], v68 offset:3072
	ds_read_b128 v[144:147], v172
	ds_read_b128 v[148:151], v172 offset:1024
	ds_read_b128 v[162:165], v172 offset:2048
	ds_read_b128 v[172:175], v172 offset:3072
	s_add_u32 s28, s44, 0x80000
	s_addc_u32 s29, s45, 0
	s_mov_b32 m0, s47
	v_lshl_add_u64 v[232:233], s[28:29], 0, v[156:157]
	ds_read_b128 v[176:179], v171 offset:32768
	ds_read_b128 v[180:183], v171 offset:33792
	ds_read_b128 v[194:197], v171 offset:34816
	ds_read_b128 v[198:201], v171 offset:35840
	ds_read_b128 v[202:205], v171 offset:36864
	ds_read_b128 v[206:209], v171 offset:37888
	ds_read_b128 v[224:227], v171 offset:38912
	ds_read_b128 v[228:231], v171 offset:39936
	global_load_lds_dwordx4 v[232:233], off
	v_lshl_add_u64 v[232:233], s[28:29], 0, v[154:155]
	s_mov_b32 m0, s50
	s_nop 0
	global_load_lds_dwordx4 v[232:233], off
	s_mov_b32 m0, s26
	s_nop 0
	global_load_lds_dwordx4 v[216:217], off
	s_mov_b32 m0, s27
	s_nop 0
	global_load_lds_dwordx4 v[218:219], off
	s_waitcnt vmcnt(8)
	s_waitcnt lgkmcnt(0)
	s_barrier
	s_setprio 0
	s_waitcnt lgkmcnt(0)
	v_mfma_f32_16x16x32_bf16 v[140:143], v[56:59], v[176:179], v[140:143]
	v_mfma_f32_16x16x32_bf16 v[136:139], v[64:67], v[176:179], v[136:139]
	v_mfma_f32_16x16x32_bf16 v[124:127], v[56:59], v[194:197], v[124:127]
	v_mfma_f32_16x16x32_bf16 v[120:123], v[64:67], v[194:197], v[120:123]
	v_mfma_f32_16x16x32_bf16 v[108:111], v[56:59], v[202:205], v[108:111]
	v_mfma_f32_16x16x32_bf16 v[104:107], v[64:67], v[202:205], v[104:107]
	v_mfma_f32_16x16x32_bf16 v[92:95], v[56:59], v[224:227], v[92:95]
	v_mfma_f32_16x16x32_bf16 v[88:91], v[64:67], v[224:227], v[88:91]
	v_mfma_f32_16x16x32_bf16 v[140:143], v[60:63], v[180:183], v[140:143]
	v_mfma_f32_16x16x32_bf16 v[136:139], v[68:71], v[180:183], v[136:139]
	v_mfma_f32_16x16x32_bf16 v[124:127], v[60:63], v[198:201], v[124:127]
	v_mfma_f32_16x16x32_bf16 v[120:123], v[68:71], v[198:201], v[120:123]
	v_mfma_f32_16x16x32_bf16 v[108:111], v[60:63], v[206:209], v[108:111]
	v_mfma_f32_16x16x32_bf16 v[104:107], v[68:71], v[206:209], v[104:107]
	v_mfma_f32_16x16x32_bf16 v[92:95], v[60:63], v[228:231], v[92:95]
	v_mfma_f32_16x16x32_bf16 v[88:91], v[68:71], v[228:231], v[88:91]
	s_setprio 1
	s_setprio 0
	v_mfma_f32_16x16x32_bf16 v[132:135], v[144:147], v[176:179], v[132:135]
	v_mfma_f32_16x16x32_bf16 v[128:131], v[162:165], v[176:179], v[128:131]
	v_mfma_f32_16x16x32_bf16 v[116:119], v[144:147], v[194:197], v[116:119]
	v_mfma_f32_16x16x32_bf16 v[112:115], v[162:165], v[194:197], v[112:115]
	v_mfma_f32_16x16x32_bf16 v[100:103], v[144:147], v[202:205], v[100:103]
	v_mfma_f32_16x16x32_bf16 v[96:99], v[162:165], v[202:205], v[96:99]
	v_mfma_f32_16x16x32_bf16 v[84:87], v[144:147], v[224:227], v[84:87]
	v_mfma_f32_16x16x32_bf16 v[80:83], v[162:165], v[224:227], v[80:83]
	v_mfma_f32_16x16x32_bf16 v[132:135], v[148:151], v[180:183], v[132:135]
	v_mfma_f32_16x16x32_bf16 v[128:131], v[172:175], v[180:183], v[128:131]
	v_mfma_f32_16x16x32_bf16 v[116:119], v[148:151], v[198:201], v[116:119]
	v_mfma_f32_16x16x32_bf16 v[112:115], v[172:175], v[198:201], v[112:115]
	v_mfma_f32_16x16x32_bf16 v[100:103], v[148:151], v[206:209], v[100:103]
	v_mfma_f32_16x16x32_bf16 v[96:99], v[172:175], v[206:209], v[96:99]
	v_mfma_f32_16x16x32_bf16 v[84:87], v[148:151], v[228:231], v[84:87]
	v_mfma_f32_16x16x32_bf16 v[80:83], v[172:175], v[228:231], v[80:83]
	s_setprio 1
	s_barrier
	s_add_i32 s28, s48, s46
	v_lshl_add_u64 v[166:167], v[166:167], 0, s[68:69]
	s_mov_b32 m0, s28
	ds_read_b128 v[176:179], v171 offset:49152
	ds_read_b128 v[180:183], v171 offset:50176
	ds_read_b128 v[194:197], v171 offset:51200
	ds_read_b128 v[198:201], v171 offset:52224
	ds_read_b128 v[202:205], v171 offset:53248
	ds_read_b128 v[206:209], v171 offset:54272
	ds_read_b128 v[224:227], v171 offset:55296
	ds_read_b128 v[228:231], v171 offset:56320
	global_load_lds_dwordx4 v[166:167], off
	s_add_i32 m0, s28, 0x2000
	s_add_u32 s28, s42, 0x80080
	v_lshl_add_u64 v[166:167], v[210:211], 0, s[68:69]
	s_addc_u32 s29, s43, 0
	s_add_i32 s42, s49, s46
	global_load_lds_dwordx4 v[166:167], off
	v_lshl_add_u64 v[166:167], s[28:29], 0, v[184:185]
	s_mov_b32 m0, s42
	s_nop 0
	global_load_lds_dwordx4 v[166:167], off
	v_lshl_add_u64 v[166:167], s[28:29], 0, v[152:153]
	s_add_i32 m0, s42, 0x2000
	s_nop 0
	global_load_lds_dwordx4 v[166:167], off
	v_lshl_add_u64 v[166:167], v[216:217], 0, s[68:69]
	s_mov_b32 m0, s53
	s_nop 0
	global_load_lds_dwordx4 v[166:167], off
	v_lshl_add_u64 v[166:167], v[218:219], 0, s[68:69]
	s_mov_b32 m0, s58
	s_nop 0
	global_load_lds_dwordx4 v[166:167], off
	s_waitcnt vmcnt(6)
	s_waitcnt lgkmcnt(0)
	s_barrier
	s_setprio 0
	s_waitcnt lgkmcnt(0)
	v_mfma_f32_16x16x32_bf16 v[76:79], v[56:59], v[176:179], v[76:79]
	v_mfma_f32_16x16x32_bf16 v[72:75], v[64:67], v[176:179], v[72:75]
	v_mfma_f32_16x16x32_bf16 v[52:55], v[56:59], v[194:197], v[52:55]
	v_mfma_f32_16x16x32_bf16 v[48:51], v[64:67], v[194:197], v[48:51]
	v_mfma_f32_16x16x32_bf16 v[28:31], v[56:59], v[202:205], v[28:31]
	v_mfma_f32_16x16x32_bf16 v[24:27], v[64:67], v[202:205], v[24:27]
	v_mfma_f32_16x16x32_bf16 v[12:15], v[56:59], v[224:227], v[12:15]
	v_mfma_f32_16x16x32_bf16 v[8:11], v[64:67], v[224:227], v[8:11]
	v_mfma_f32_16x16x32_bf16 v[76:79], v[60:63], v[180:183], v[76:79]
	v_mfma_f32_16x16x32_bf16 v[72:75], v[68:71], v[180:183], v[72:75]
	v_mfma_f32_16x16x32_bf16 v[52:55], v[60:63], v[198:201], v[52:55]
	v_mfma_f32_16x16x32_bf16 v[48:51], v[68:71], v[198:201], v[48:51]
	v_mfma_f32_16x16x32_bf16 v[28:31], v[60:63], v[206:209], v[28:31]
	v_mfma_f32_16x16x32_bf16 v[24:27], v[68:71], v[206:209], v[24:27]
	v_mfma_f32_16x16x32_bf16 v[12:15], v[60:63], v[228:231], v[12:15]
	v_mfma_f32_16x16x32_bf16 v[8:11], v[68:71], v[228:231], v[8:11]
	s_setprio 1
	s_setprio 0
	v_mfma_f32_16x16x32_bf16 v[40:43], v[144:147], v[176:179], v[40:43]
	v_mfma_f32_16x16x32_bf16 v[68:71], v[148:151], v[180:183], v[40:43]
	v_mfma_f32_16x16x32_bf16 v[40:43], v[162:165], v[176:179], v[44:47]
	v_mfma_f32_16x16x32_bf16 v[36:39], v[144:147], v[194:197], v[36:39]
	v_mfma_f32_16x16x32_bf16 v[32:35], v[162:165], v[194:197], v[32:35]
	v_mfma_f32_16x16x32_bf16 v[20:23], v[144:147], v[202:205], v[20:23]
	v_mfma_f32_16x16x32_bf16 v[16:19], v[162:165], v[202:205], v[16:19]
	v_mfma_f32_16x16x32_bf16 v[4:7], v[144:147], v[224:227], v[4:7]
	v_mfma_f32_16x16x32_bf16 v[0:3], v[162:165], v[224:227], v[0:3]
	v_mfma_f32_16x16x32_bf16 v[64:67], v[172:175], v[180:183], v[40:43]
	v_mfma_f32_16x16x32_bf16 v[36:39], v[148:151], v[198:201], v[36:39]
	v_mfma_f32_16x16x32_bf16 v[32:35], v[172:175], v[198:201], v[32:35]
	v_mfma_f32_16x16x32_bf16 v[20:23], v[148:151], v[206:209], v[20:23]
	v_mfma_f32_16x16x32_bf16 v[16:19], v[172:175], v[206:209], v[16:19]
	v_mfma_f32_16x16x32_bf16 v[4:7], v[148:151], v[228:231], v[4:7]
	v_mfma_f32_16x16x32_bf16 v[0:3], v[172:175], v[228:231], v[0:3]
	s_setprio 1
	s_barrier
	s_add_i32 s79, s79, 2
	s_add_u32 s40, s40, 0x100
	s_addc_u32 s41, s41, 0
	s_add_u32 s62, s62, 0x100
	s_addc_u32 s63, s63, 0
	s_cmp_gt_u32 s79, 29
	s_cbranch_scc0 .LBB0_991
	s_and_b64 vcc, exec, s[8:9]
	s_cbranch_vccz .LBB0_994
	s_barrier

.LBB0_1419:
	s_add_u32 s28, s24, 0xfff80080
	s_addc_u32 s29, s25, -1
	s_add_i32 s48, 0, 0x10000
	s_cmp_eq_u32 s17, 28
	s_cselect_b32 s31, s9, s29
	s_cselect_b32 s30, s11, s28
	s_cselect_b64 vcc, -1, 0
	s_add_i32 s28, 0, 0x14000
	v_add_u32_e32 v164, s48, v147
	v_add_u32_e32 v180, s28, v147
	ds_read_b128 v[152:155], v164
	ds_read_b128 v[156:159], v164 offset:1024
	ds_read_b128 v[160:163], v164 offset:2048
	ds_read_b128 v[164:167], v164 offset:3072
	ds_read_b128 v[168:171], v180
	ds_read_b128 v[172:175], v180 offset:1024
	ds_read_b128 v[176:179], v180 offset:2048
	ds_read_b128 v[180:183], v180 offset:3072
	v_cndmask_b32_e32 v211, v145, v150, vcc
	v_cndmask_b32_e32 v210, v144, v151, vcc
	v_lshl_add_u64 v[216:217], s[24:25], 0, v[136:137]
	s_add_i32 m0, s19, 0xc000
	ds_read_b128 v[194:197], v149
	ds_read_b128 v[198:201], v149 offset:1024
	ds_read_b128 v[202:205], v149 offset:2048
	ds_read_b128 v[206:209], v149 offset:3072
	ds_read_b128 v[224:227], v149 offset:4096
	ds_read_b128 v[228:231], v149 offset:5120
	ds_read_b128 v[232:235], v149 offset:6144
	ds_read_b128 v[236:239], v149 offset:7168
	global_load_lds_dwordx4 v[216:217], off
	v_lshl_add_u64 v[216:217], s[24:25], 0, v[138:139]
	s_add_i32 m0, s19, 0xe000
	s_nop 0
	global_load_lds_dwordx4 v[216:217], off
	s_waitcnt vmcnt(8)
	s_waitcnt lgkmcnt(0)
	s_barrier
	s_setprio 0
	s_waitcnt lgkmcnt(0)
	v_mfma_f32_16x16x32_bf16 v[124:127], v[152:155], v[194:197], v[124:127]
	v_mfma_f32_16x16x32_bf16 v[116:119], v[160:163], v[194:197], v[116:119]
	v_mfma_f32_16x16x32_bf16 v[108:111], v[152:155], v[202:205], v[108:111]
	v_mfma_f32_16x16x32_bf16 v[100:103], v[160:163], v[202:205], v[100:103]
	v_mfma_f32_16x16x32_bf16 v[92:95], v[152:155], v[224:227], v[92:95]
	v_mfma_f32_16x16x32_bf16 v[84:87], v[160:163], v[224:227], v[84:87]
	v_mfma_f32_16x16x32_bf16 v[76:79], v[152:155], v[232:235], v[76:79]
	v_mfma_f32_16x16x32_bf16 v[68:71], v[160:163], v[232:235], v[68:71]
	v_mfma_f32_16x16x32_bf16 v[124:127], v[156:159], v[198:201], v[124:127]
	v_mfma_f32_16x16x32_bf16 v[116:119], v[164:167], v[198:201], v[116:119]
	v_mfma_f32_16x16x32_bf16 v[108:111], v[156:159], v[206:209], v[108:111]
	v_mfma_f32_16x16x32_bf16 v[100:103], v[164:167], v[206:209], v[100:103]
	v_mfma_f32_16x16x32_bf16 v[92:95], v[156:159], v[228:231], v[92:95]
	v_mfma_f32_16x16x32_bf16 v[84:87], v[164:167], v[228:231], v[84:87]
	v_mfma_f32_16x16x32_bf16 v[76:79], v[156:159], v[236:239], v[76:79]
	v_mfma_f32_16x16x32_bf16 v[68:71], v[164:167], v[236:239], v[68:71]
	s_setprio 1
	s_setprio 0
	v_mfma_f32_16x16x32_bf16 v[120:123], v[168:171], v[194:197], v[120:123]
	v_mfma_f32_16x16x32_bf16 v[112:115], v[176:179], v[194:197], v[112:115]
	v_mfma_f32_16x16x32_bf16 v[104:107], v[168:171], v[202:205], v[104:107]
	v_mfma_f32_16x16x32_bf16 v[96:99], v[176:179], v[202:205], v[96:99]
	v_mfma_f32_16x16x32_bf16 v[88:91], v[168:171], v[224:227], v[88:91]
	v_mfma_f32_16x16x32_bf16 v[80:83], v[176:179], v[224:227], v[80:83]
	v_mfma_f32_16x16x32_bf16 v[72:75], v[168:171], v[232:235], v[72:75]
	v_mfma_f32_16x16x32_bf16 v[64:67], v[176:179], v[232:235], v[64:67]
	v_mfma_f32_16x16x32_bf16 v[120:123], v[172:175], v[198:201], v[120:123]
	v_mfma_f32_16x16x32_bf16 v[112:115], v[180:183], v[198:201], v[112:115]
	v_mfma_f32_16x16x32_bf16 v[104:107], v[172:175], v[206:209], v[104:107]
	v_mfma_f32_16x16x32_bf16 v[96:99], v[180:183], v[206:209], v[96:99]
	v_mfma_f32_16x16x32_bf16 v[88:91], v[172:175], v[228:231], v[88:91]
	v_mfma_f32_16x16x32_bf16 v[80:83], v[180:183], v[228:231], v[80:83]
	v_mfma_f32_16x16x32_bf16 v[72:75], v[172:175], v[236:239], v[72:75]
	v_mfma_f32_16x16x32_bf16 v[64:67], v[180:183], v[236:239], v[64:67]
	s_setprio 1
	s_barrier
	s_add_i32 s29, s48, s50
	v_lshl_add_u64 v[216:217], v[210:211], 0, v[130:131]
	s_mov_b32 m0, s29
	ds_read_b128 v[194:197], v149 offset:16384
	ds_read_b128 v[198:201], v149 offset:17408
	ds_read_b128 v[202:205], v149 offset:18432
	ds_read_b128 v[206:209], v149 offset:19456
	ds_read_b128 v[224:227], v149 offset:20480
	ds_read_b128 v[228:231], v149 offset:21504
	ds_read_b128 v[232:235], v149 offset:22528
	ds_read_b128 v[236:239], v149 offset:23552
	global_load_lds_dwordx4 v[216:217], off
	v_lshl_add_u64 v[218:219], v[210:211], 0, v[134:135]
	s_add_i32 m0, s29, 0x2000
	v_lshl_add_u64 v[220:221], v[210:211], 0, s[72:73]
	s_add_i32 s28, s28, s50
	global_load_lds_dwordx4 v[218:219], off
	v_lshl_add_u64 v[240:241], v[220:221], 0, v[130:131]
	s_mov_b32 m0, s28
	v_lshl_add_u64 v[220:221], v[220:221], 0, v[134:135]
	global_load_lds_dwordx4 v[240:241], off
	s_add_i32 m0, s28, 0x2000
	v_lshl_add_u64 v[240:241], s[30:31], 0, v[132:133]
	global_load_lds_dwordx4 v[220:221], off
	v_lshl_add_u64 v[220:221], s[30:31], 0, v[128:129]
	s_waitcnt vmcnt(6)
	s_waitcnt lgkmcnt(0)
	s_barrier
	s_setprio 0
	s_waitcnt lgkmcnt(0)
	v_mfma_f32_16x16x32_bf16 v[60:63], v[152:155], v[194:197], v[60:63]
	v_mfma_f32_16x16x32_bf16 v[52:55], v[160:163], v[194:197], v[52:55]
	v_mfma_f32_16x16x32_bf16 v[44:47], v[152:155], v[202:205], v[44:47]
	v_mfma_f32_16x16x32_bf16 v[36:39], v[160:163], v[202:205], v[36:39]
	v_mfma_f32_16x16x32_bf16 v[28:31], v[152:155], v[224:227], v[28:31]
	v_mfma_f32_16x16x32_bf16 v[20:23], v[160:163], v[224:227], v[20:23]
	v_mfma_f32_16x16x32_bf16 v[12:15], v[152:155], v[232:235], v[12:15]
	v_mfma_f32_16x16x32_bf16 v[4:7], v[160:163], v[232:235], v[4:7]
	v_mfma_f32_16x16x32_bf16 v[60:63], v[156:159], v[198:201], v[60:63]
	v_mfma_f32_16x16x32_bf16 v[52:55], v[164:167], v[198:201], v[52:55]
	v_mfma_f32_16x16x32_bf16 v[44:47], v[156:159], v[206:209], v[44:47]
	v_mfma_f32_16x16x32_bf16 v[36:39], v[164:167], v[206:209], v[36:39]
	v_mfma_f32_16x16x32_bf16 v[28:31], v[156:159], v[228:231], v[28:31]
	v_mfma_f32_16x16x32_bf16 v[20:23], v[164:167], v[228:231], v[20:23]
	v_mfma_f32_16x16x32_bf16 v[12:15], v[156:159], v[236:239], v[12:15]
	v_mfma_f32_16x16x32_bf16 v[4:7], v[164:167], v[236:239], v[4:7]
	s_setprio 1
	s_setprio 0
	v_mfma_f32_16x16x32_bf16 v[56:59], v[168:171], v[194:197], v[56:59]
	v_mfma_f32_16x16x32_bf16 v[48:51], v[176:179], v[194:197], v[48:51]
	v_mfma_f32_16x16x32_bf16 v[40:43], v[168:171], v[202:205], v[40:43]
	v_mfma_f32_16x16x32_bf16 v[32:35], v[176:179], v[202:205], v[32:35]
	v_mfma_f32_16x16x32_bf16 v[24:27], v[168:171], v[224:227], v[24:27]
	v_mfma_f32_16x16x32_bf16 v[16:19], v[176:179], v[224:227], v[16:19]
	v_mfma_f32_16x16x32_bf16 v[8:11], v[168:171], v[232:235], v[8:11]
	v_mfma_f32_16x16x32_bf16 v[0:3], v[176:179], v[232:235], v[0:3]
	v_mfma_f32_16x16x32_bf16 v[56:59], v[172:175], v[198:201], v[56:59]
	v_mfma_f32_16x16x32_bf16 v[48:51], v[180:183], v[198:201], v[48:51]
	v_mfma_f32_16x16x32_bf16 v[40:43], v[172:175], v[206:209], v[40:43]
	v_mfma_f32_16x16x32_bf16 v[32:35], v[180:183], v[206:209], v[32:35]
	v_mfma_f32_16x16x32_bf16 v[24:27], v[172:175], v[228:231], v[24:27]
	v_mfma_f32_16x16x32_bf16 v[16:19], v[180:183], v[228:231], v[16:19]
	v_mfma_f32_16x16x32_bf16 v[8:11], v[172:175], v[236:239], v[8:11]
	v_mfma_f32_16x16x32_bf16 v[0:3], v[180:183], v[236:239], v[0:3]
	s_setprio 1
	s_barrier
	s_add_i32 s48, 0, 0x18000
	s_add_i32 s49, 0, 0x1c000
	v_add_u32_e32 v164, s48, v147
	v_add_u32_e32 v180, s49, v147
	ds_read_b128 v[152:155], v164
	ds_read_b128 v[156:159], v164 offset:1024
	ds_read_b128 v[160:163], v164 offset:2048
	ds_read_b128 v[164:167], v164 offset:3072
	ds_read_b128 v[168:171], v180
	ds_read_b128 v[172:175], v180 offset:1024
	ds_read_b128 v[176:179], v180 offset:2048
	ds_read_b128 v[180:183], v180 offset:3072
	s_add_u32 s28, s30, 0x80000
	s_addc_u32 s29, s31, 0
	s_mov_b32 m0, s52
	v_lshl_add_u64 v[242:243], s[28:29], 0, v[128:129]
	ds_read_b128 v[194:197], v149 offset:32768
	ds_read_b128 v[198:201], v149 offset:33792
	ds_read_b128 v[202:205], v149 offset:34816
	ds_read_b128 v[206:209], v149 offset:35840
	ds_read_b128 v[224:227], v149 offset:36864
	ds_read_b128 v[228:231], v149 offset:37888
	ds_read_b128 v[232:235], v149 offset:38912
	ds_read_b128 v[236:239], v149 offset:39936
	global_load_lds_dwordx4 v[242:243], off
	v_lshl_add_u64 v[242:243], s[28:29], 0, v[132:133]
	s_mov_b32 m0, s53
	s_nop 0
	global_load_lds_dwordx4 v[242:243], off
	s_mov_b32 m0, s19
	s_nop 0
	global_load_lds_dwordx4 v[220:221], off
	s_mov_b32 m0, s51
	s_nop 0
	global_load_lds_dwordx4 v[240:241], off
	s_waitcnt vmcnt(8)
	s_waitcnt lgkmcnt(0)
	s_barrier
	s_setprio 0
	s_waitcnt lgkmcnt(0)
	v_mfma_f32_16x16x32_bf16 v[124:127], v[152:155], v[194:197], v[124:127]
	v_mfma_f32_16x16x32_bf16 v[116:119], v[160:163], v[194:197], v[116:119]
	v_mfma_f32_16x16x32_bf16 v[108:111], v[152:155], v[202:205], v[108:111]
	v_mfma_f32_16x16x32_bf16 v[100:103], v[160:163], v[202:205], v[100:103]
	v_mfma_f32_16x16x32_bf16 v[92:95], v[152:155], v[224:227], v[92:95]
	v_mfma_f32_16x16x32_bf16 v[84:87], v[160:163], v[224:227], v[84:87]
	v_mfma_f32_16x16x32_bf16 v[76:79], v[152:155], v[232:235], v[76:79]
	v_mfma_f32_16x16x32_bf16 v[68:71], v[160:163], v[232:235], v[68:71]
	v_mfma_f32_16x16x32_bf16 v[124:127], v[156:159], v[198:201], v[124:127]
	v_mfma_f32_16x16x32_bf16 v[116:119], v[164:167], v[198:201], v[116:119]
	v_mfma_f32_16x16x32_bf16 v[108:111], v[156:159], v[206:209], v[108:111]
	v_mfma_f32_16x16x32_bf16 v[100:103], v[164:167], v[206:209], v[100:103]
	v_mfma_f32_16x16x32_bf16 v[92:95], v[156:159], v[228:231], v[92:95]
	v_mfma_f32_16x16x32_bf16 v[84:87], v[164:167], v[228:231], v[84:87]
	v_mfma_f32_16x16x32_bf16 v[76:79], v[156:159], v[236:239], v[76:79]
	v_mfma_f32_16x16x32_bf16 v[68:71], v[164:167], v[236:239], v[68:71]
	s_setprio 1
	s_setprio 0
	v_mfma_f32_16x16x32_bf16 v[120:123], v[168:171], v[194:197], v[120:123]
	v_mfma_f32_16x16x32_bf16 v[112:115], v[176:179], v[194:197], v[112:115]
	v_mfma_f32_16x16x32_bf16 v[104:107], v[168:171], v[202:205], v[104:107]
	v_mfma_f32_16x16x32_bf16 v[96:99], v[176:179], v[202:205], v[96:99]
	v_mfma_f32_16x16x32_bf16 v[88:91], v[168:171], v[224:227], v[88:91]
	v_mfma_f32_16x16x32_bf16 v[80:83], v[176:179], v[224:227], v[80:83]
	v_mfma_f32_16x16x32_bf16 v[72:75], v[168:171], v[232:235], v[72:75]
	v_mfma_f32_16x16x32_bf16 v[64:67], v[176:179], v[232:235], v[64:67]
	v_mfma_f32_16x16x32_bf16 v[120:123], v[172:175], v[198:201], v[120:123]
	v_mfma_f32_16x16x32_bf16 v[112:115], v[180:183], v[198:201], v[112:115]
	v_mfma_f32_16x16x32_bf16 v[104:107], v[172:175], v[206:209], v[104:107]
	v_mfma_f32_16x16x32_bf16 v[96:99], v[180:183], v[206:209], v[96:99]
	v_mfma_f32_16x16x32_bf16 v[88:91], v[172:175], v[228:231], v[88:91]
	v_mfma_f32_16x16x32_bf16 v[80:83], v[180:183], v[228:231], v[80:83]
	v_mfma_f32_16x16x32_bf16 v[72:75], v[172:175], v[236:239], v[72:75]
	v_mfma_f32_16x16x32_bf16 v[64:67], v[180:183], v[236:239], v[64:67]
	s_setprio 1
	s_barrier
	s_add_i32 s28, s48, s50
	v_lshl_add_u64 v[216:217], v[216:217], 0, s[68:69]
	s_mov_b32 m0, s28
	ds_read_b128 v[194:197], v149 offset:49152
	ds_read_b128 v[198:201], v149 offset:50176
	ds_read_b128 v[202:205], v149 offset:51200
	ds_read_b128 v[206:209], v149 offset:52224
	ds_read_b128 v[224:227], v149 offset:53248
	ds_read_b128 v[228:231], v149 offset:54272
	ds_read_b128 v[232:235], v149 offset:55296
	ds_read_b128 v[236:239], v149 offset:56320
	global_load_lds_dwordx4 v[216:217], off
	v_lshl_add_u64 v[216:217], v[218:219], 0, s[68:69]
	s_add_i32 m0, s28, 0x2000
	v_lshl_add_u64 v[210:211], v[210:211], 0, s[74:75]
	s_add_i32 s28, s49, s50
	global_load_lds_dwordx4 v[216:217], off
	v_lshl_add_u64 v[216:217], v[210:211], 0, v[130:131]
	s_mov_b32 m0, s28
	v_lshl_add_u64 v[210:211], v[210:211], 0, v[134:135]
	global_load_lds_dwordx4 v[216:217], off
	s_add_i32 m0, s28, 0x2000
	s_nop 0
	global_load_lds_dwordx4 v[210:211], off
	v_lshl_add_u64 v[210:211], v[220:221], 0, s[68:69]
	s_mov_b32 m0, s58
	s_nop 0
	global_load_lds_dwordx4 v[210:211], off
	v_lshl_add_u64 v[210:211], v[240:241], 0, s[68:69]
	s_mov_b32 m0, s59
	s_nop 0
	global_load_lds_dwordx4 v[210:211], off
	s_waitcnt vmcnt(6)
	s_waitcnt lgkmcnt(0)
	s_barrier
	s_setprio 0
	s_waitcnt lgkmcnt(0)
	v_mfma_f32_16x16x32_bf16 v[60:63], v[152:155], v[194:197], v[60:63]
	v_mfma_f32_16x16x32_bf16 v[52:55], v[160:163], v[194:197], v[52:55]
	v_mfma_f32_16x16x32_bf16 v[44:47], v[152:155], v[202:205], v[44:47]
	v_mfma_f32_16x16x32_bf16 v[36:39], v[160:163], v[202:205], v[36:39]
	v_mfma_f32_16x16x32_bf16 v[28:31], v[152:155], v[224:227], v[28:31]
	v_mfma_f32_16x16x32_bf16 v[20:23], v[160:163], v[224:227], v[20:23]
	v_mfma_f32_16x16x32_bf16 v[12:15], v[152:155], v[232:235], v[12:15]
	v_mfma_f32_16x16x32_bf16 v[4:7], v[160:163], v[232:235], v[4:7]
	v_mfma_f32_16x16x32_bf16 v[60:63], v[156:159], v[198:201], v[60:63]
	v_mfma_f32_16x16x32_bf16 v[52:55], v[164:167], v[198:201], v[52:55]
	v_mfma_f32_16x16x32_bf16 v[44:47], v[156:159], v[206:209], v[44:47]
	v_mfma_f32_16x16x32_bf16 v[36:39], v[164:167], v[206:209], v[36:39]
	v_mfma_f32_16x16x32_bf16 v[28:31], v[156:159], v[228:231], v[28:31]
	v_mfma_f32_16x16x32_bf16 v[20:23], v[164:167], v[228:231], v[20:23]
	v_mfma_f32_16x16x32_bf16 v[12:15], v[156:159], v[236:239], v[12:15]
	v_mfma_f32_16x16x32_bf16 v[4:7], v[164:167], v[236:239], v[4:7]
	s_setprio 1
	s_setprio 0
	v_mfma_f32_16x16x32_bf16 v[56:59], v[168:171], v[194:197], v[56:59]
	v_mfma_f32_16x16x32_bf16 v[48:51], v[176:179], v[194:197], v[48:51]
	v_mfma_f32_16x16x32_bf16 v[40:43], v[168:171], v[202:205], v[40:43]
	v_mfma_f32_16x16x32_bf16 v[32:35], v[176:179], v[202:205], v[32:35]
	v_mfma_f32_16x16x32_bf16 v[24:27], v[168:171], v[224:227], v[24:27]
	v_mfma_f32_16x16x32_bf16 v[16:19], v[176:179], v[224:227], v[16:19]
	v_mfma_f32_16x16x32_bf16 v[8:11], v[168:171], v[232:235], v[8:11]
	v_mfma_f32_16x16x32_bf16 v[0:3], v[176:179], v[232:235], v[0:3]
	v_mfma_f32_16x16x32_bf16 v[56:59], v[172:175], v[198:201], v[56:59]
	v_mfma_f32_16x16x32_bf16 v[48:51], v[180:183], v[198:201], v[48:51]
	v_mfma_f32_16x16x32_bf16 v[40:43], v[172:175], v[206:209], v[40:43]
	v_mfma_f32_16x16x32_bf16 v[32:35], v[180:183], v[206:209], v[32:35]
	v_mfma_f32_16x16x32_bf16 v[24:27], v[172:175], v[228:231], v[24:27]
	v_mfma_f32_16x16x32_bf16 v[16:19], v[180:183], v[228:231], v[16:19]
	v_mfma_f32_16x16x32_bf16 v[8:11], v[172:175], v[236:239], v[8:11]
	v_mfma_f32_16x16x32_bf16 v[0:3], v[180:183], v[236:239], v[0:3]
	s_setprio 1
	s_barrier
	s_add_i32 s17, s17, 2
	s_add_u32 s24, s24, 0x100
	s_addc_u32 s25, s25, 0
	s_cmp_gt_u32 s17, 29
	v_lshl_add_u64 v[144:145], v[144:145], 0, s[76:77]
	s_cbranch_scc0 .LBB0_1419
	s_and_b64 vcc, exec, s[6:7]
	s_cbranch_vccz .LBB0_1422
	s_barrier

.LBB0_1491:
	s_add_u32 s14, s12, 0x100
	s_addc_u32 s15, s13, 0
	s_add_i32 s28, 0, 0x10000
	s_cmp_eq_u32 s59, 40
	s_cselect_b32 s17, s53, s15
	s_cselect_b32 s16, s58, s14
	s_cselect_b64 vcc, -1, 0
	s_add_i32 s29, 0, 0x14000
	v_add_u32_e32 v164, s28, v147
	v_add_u32_e32 v180, s29, v147
	ds_read_b128 v[152:155], v164
	ds_read_b128 v[156:159], v164 offset:1024
	ds_read_b128 v[160:163], v164 offset:2048
	ds_read_b128 v[164:167], v164 offset:3072
	ds_read_b128 v[168:171], v180
	ds_read_b128 v[172:175], v180 offset:1024
	ds_read_b128 v[176:179], v180 offset:2048
	ds_read_b128 v[180:183], v180 offset:3072
	v_cndmask_b32_e32 v211, v145, v150, vcc
	v_cndmask_b32_e32 v210, v144, v151, vcc
	v_lshl_add_u64 v[216:217], s[12:13], 0, v[136:137]
	s_add_i32 m0, s40, 0xc000
	ds_read_b128 v[194:197], v149
	ds_read_b128 v[198:201], v149 offset:1024
	ds_read_b128 v[202:205], v149 offset:2048
	ds_read_b128 v[206:209], v149 offset:3072
	ds_read_b128 v[224:227], v149 offset:4096
	ds_read_b128 v[228:231], v149 offset:5120
	ds_read_b128 v[232:235], v149 offset:6144
	ds_read_b128 v[236:239], v149 offset:7168
	global_load_lds_dwordx4 v[216:217], off
	v_lshl_add_u64 v[216:217], s[12:13], 0, v[138:139]
	s_add_i32 m0, s40, 0xe000
	s_nop 0
	global_load_lds_dwordx4 v[216:217], off
	s_waitcnt vmcnt(8)
	s_waitcnt lgkmcnt(0)
	s_barrier
	s_setprio 0
	s_waitcnt lgkmcnt(0)
	v_mfma_f32_16x16x32_bf16 v[124:127], v[152:155], v[194:197], v[124:127]
	v_mfma_f32_16x16x32_bf16 v[120:123], v[160:163], v[194:197], v[120:123]
	v_mfma_f32_16x16x32_bf16 v[116:119], v[152:155], v[202:205], v[116:119]
	v_mfma_f32_16x16x32_bf16 v[108:111], v[160:163], v[202:205], v[108:111]
	v_mfma_f32_16x16x32_bf16 v[100:103], v[152:155], v[224:227], v[100:103]
	v_mfma_f32_16x16x32_bf16 v[92:95], v[160:163], v[224:227], v[92:95]
	v_mfma_f32_16x16x32_bf16 v[80:83], v[152:155], v[232:235], v[80:83]
	v_mfma_f32_16x16x32_bf16 v[72:75], v[160:163], v[232:235], v[72:75]
	v_mfma_f32_16x16x32_bf16 v[124:127], v[156:159], v[198:201], v[124:127]
	v_mfma_f32_16x16x32_bf16 v[120:123], v[164:167], v[198:201], v[120:123]
	v_mfma_f32_16x16x32_bf16 v[116:119], v[156:159], v[206:209], v[116:119]
	v_mfma_f32_16x16x32_bf16 v[108:111], v[164:167], v[206:209], v[108:111]
	v_mfma_f32_16x16x32_bf16 v[100:103], v[156:159], v[228:231], v[100:103]
	v_mfma_f32_16x16x32_bf16 v[92:95], v[164:167], v[228:231], v[92:95]
	v_mfma_f32_16x16x32_bf16 v[80:83], v[156:159], v[236:239], v[80:83]
	v_mfma_f32_16x16x32_bf16 v[72:75], v[164:167], v[236:239], v[72:75]
	s_setprio 1
	s_setprio 0
	v_mfma_f32_16x16x32_bf16 v[112:115], v[168:171], v[194:197], v[112:115]
	v_mfma_f32_16x16x32_bf16 v[104:107], v[176:179], v[194:197], v[104:107]
	v_mfma_f32_16x16x32_bf16 v[96:99], v[168:171], v[202:205], v[96:99]
	v_mfma_f32_16x16x32_bf16 v[88:91], v[176:179], v[202:205], v[88:91]
	v_mfma_f32_16x16x32_bf16 v[84:87], v[168:171], v[224:227], v[84:87]
	v_mfma_f32_16x16x32_bf16 v[76:79], v[176:179], v[224:227], v[76:79]
	v_mfma_f32_16x16x32_bf16 v[68:71], v[168:171], v[232:235], v[68:71]
	v_mfma_f32_16x16x32_bf16 v[64:67], v[176:179], v[232:235], v[64:67]
	v_mfma_f32_16x16x32_bf16 v[112:115], v[172:175], v[198:201], v[112:115]
	v_mfma_f32_16x16x32_bf16 v[104:107], v[180:183], v[198:201], v[104:107]
	v_mfma_f32_16x16x32_bf16 v[96:99], v[172:175], v[206:209], v[96:99]
	v_mfma_f32_16x16x32_bf16 v[88:91], v[180:183], v[206:209], v[88:91]
	v_mfma_f32_16x16x32_bf16 v[84:87], v[172:175], v[228:231], v[84:87]
	v_mfma_f32_16x16x32_bf16 v[76:79], v[180:183], v[228:231], v[76:79]
	v_mfma_f32_16x16x32_bf16 v[68:71], v[172:175], v[236:239], v[68:71]
	v_mfma_f32_16x16x32_bf16 v[64:67], v[180:183], v[236:239], v[64:67]
	s_setprio 1
	s_barrier
	s_add_i32 s12, s28, s30
	v_lshl_add_u64 v[216:217], v[210:211], 0, v[132:133]
	s_mov_b32 m0, s12
	ds_read_b128 v[194:197], v149 offset:16384
	ds_read_b128 v[198:201], v149 offset:17408
	ds_read_b128 v[202:205], v149 offset:18432
	ds_read_b128 v[206:209], v149 offset:19456
	ds_read_b128 v[224:227], v149 offset:20480
	ds_read_b128 v[228:231], v149 offset:21504
	ds_read_b128 v[232:235], v149 offset:22528
	ds_read_b128 v[236:239], v149 offset:23552
	global_load_lds_dwordx4 v[216:217], off
	v_lshl_add_u64 v[218:219], v[210:211], 0, v[128:129]
	s_add_i32 m0, s12, 0x2000
	v_lshl_add_u64 v[220:221], v[210:211], 0, s[72:73]
	s_add_i32 s12, s29, s30
	global_load_lds_dwordx4 v[218:219], off
	v_lshl_add_u64 v[240:241], v[220:221], 0, v[132:133]
	s_mov_b32 m0, s12
	v_lshl_add_u64 v[220:221], v[220:221], 0, v[128:129]
	global_load_lds_dwordx4 v[240:241], off
	s_add_i32 m0, s12, 0x2000
	v_lshl_add_u64 v[240:241], s[16:17], 0, v[130:131]
	global_load_lds_dwordx4 v[220:221], off
	v_lshl_add_u64 v[220:221], s[16:17], 0, v[134:135]
	s_waitcnt vmcnt(6)
	s_waitcnt lgkmcnt(0)
	s_barrier
	s_setprio 0
	s_waitcnt lgkmcnt(0)
	v_mfma_f32_16x16x32_bf16 v[60:63], v[152:155], v[194:197], v[60:63]
	v_mfma_f32_16x16x32_bf16 v[56:59], v[160:163], v[194:197], v[56:59]
	v_mfma_f32_16x16x32_bf16 v[52:55], v[152:155], v[202:205], v[52:55]
	v_mfma_f32_16x16x32_bf16 v[44:47], v[160:163], v[202:205], v[44:47]
	v_mfma_f32_16x16x32_bf16 v[36:39], v[152:155], v[224:227], v[36:39]
	v_mfma_f32_16x16x32_bf16 v[28:31], v[160:163], v[224:227], v[28:31]
	v_mfma_f32_16x16x32_bf16 v[20:23], v[152:155], v[232:235], v[20:23]
	v_mfma_f32_16x16x32_bf16 v[12:15], v[160:163], v[232:235], v[12:15]
	v_mfma_f32_16x16x32_bf16 v[60:63], v[156:159], v[198:201], v[60:63]
	v_mfma_f32_16x16x32_bf16 v[56:59], v[164:167], v[198:201], v[56:59]
	v_mfma_f32_16x16x32_bf16 v[52:55], v[156:159], v[206:209], v[52:55]
	v_mfma_f32_16x16x32_bf16 v[44:47], v[164:167], v[206:209], v[44:47]
	v_mfma_f32_16x16x32_bf16 v[36:39], v[156:159], v[228:231], v[36:39]
	v_mfma_f32_16x16x32_bf16 v[28:31], v[164:167], v[228:231], v[28:31]
	v_mfma_f32_16x16x32_bf16 v[20:23], v[156:159], v[236:239], v[20:23]
	v_mfma_f32_16x16x32_bf16 v[12:15], v[164:167], v[236:239], v[12:15]
	s_setprio 1
	s_setprio 0
	v_mfma_f32_16x16x32_bf16 v[48:51], v[168:171], v[194:197], v[48:51]
	v_mfma_f32_16x16x32_bf16 v[40:43], v[176:179], v[194:197], v[40:43]
	v_mfma_f32_16x16x32_bf16 v[32:35], v[168:171], v[202:205], v[32:35]
	v_mfma_f32_16x16x32_bf16 v[24:27], v[176:179], v[202:205], v[24:27]
	v_mfma_f32_16x16x32_bf16 v[16:19], v[168:171], v[224:227], v[16:19]
	v_mfma_f32_16x16x32_bf16 v[8:11], v[176:179], v[224:227], v[8:11]
	v_mfma_f32_16x16x32_bf16 v[4:7], v[168:171], v[232:235], v[4:7]
	v_mfma_f32_16x16x32_bf16 v[0:3], v[176:179], v[232:235], v[0:3]
	v_mfma_f32_16x16x32_bf16 v[48:51], v[172:175], v[198:201], v[48:51]
	v_mfma_f32_16x16x32_bf16 v[40:43], v[180:183], v[198:201], v[40:43]
	v_mfma_f32_16x16x32_bf16 v[32:35], v[172:175], v[206:209], v[32:35]
	v_mfma_f32_16x16x32_bf16 v[24:27], v[180:183], v[206:209], v[24:27]
	v_mfma_f32_16x16x32_bf16 v[16:19], v[172:175], v[228:231], v[16:19]
	v_mfma_f32_16x16x32_bf16 v[8:11], v[180:183], v[228:231], v[8:11]
	v_mfma_f32_16x16x32_bf16 v[4:7], v[172:175], v[236:239], v[4:7]
	v_mfma_f32_16x16x32_bf16 v[0:3], v[180:183], v[236:239], v[0:3]
	s_setprio 1
	s_barrier
	s_add_i32 s28, 0, 0x18000
	s_add_i32 s29, 0, 0x1c000
	v_add_u32_e32 v164, s28, v147
	v_add_u32_e32 v180, s29, v147
	ds_read_b128 v[152:155], v164
	ds_read_b128 v[156:159], v164 offset:1024
	ds_read_b128 v[160:163], v164 offset:2048
	ds_read_b128 v[164:167], v164 offset:3072
	ds_read_b128 v[168:171], v180
	ds_read_b128 v[172:175], v180 offset:1024
	ds_read_b128 v[176:179], v180 offset:2048
	ds_read_b128 v[180:183], v180 offset:3072
	s_add_u32 s12, s16, 0xb0000
	s_addc_u32 s13, s17, 0
	s_mov_b32 m0, s42
	v_lshl_add_u64 v[242:243], s[12:13], 0, v[134:135]
	ds_read_b128 v[194:197], v149 offset:32768
	ds_read_b128 v[198:201], v149 offset:33792
	ds_read_b128 v[202:205], v149 offset:34816
	ds_read_b128 v[206:209], v149 offset:35840
	ds_read_b128 v[224:227], v149 offset:36864
	ds_read_b128 v[228:231], v149 offset:37888
	ds_read_b128 v[232:235], v149 offset:38912
	ds_read_b128 v[236:239], v149 offset:39936
	global_load_lds_dwordx4 v[242:243], off
	v_lshl_add_u64 v[242:243], s[12:13], 0, v[130:131]
	s_mov_b32 m0, s43
	s_nop 0
	global_load_lds_dwordx4 v[242:243], off
	s_mov_b32 m0, s40
	s_nop 0
	global_load_lds_dwordx4 v[220:221], off
	s_mov_b32 m0, s41
	s_nop 0
	global_load_lds_dwordx4 v[240:241], off
	s_waitcnt vmcnt(8)
	s_waitcnt lgkmcnt(0)
	s_barrier
	s_setprio 0
	s_waitcnt lgkmcnt(0)
	v_mfma_f32_16x16x32_bf16 v[124:127], v[152:155], v[194:197], v[124:127]
	v_mfma_f32_16x16x32_bf16 v[120:123], v[160:163], v[194:197], v[120:123]
	v_mfma_f32_16x16x32_bf16 v[116:119], v[152:155], v[202:205], v[116:119]
	v_mfma_f32_16x16x32_bf16 v[108:111], v[160:163], v[202:205], v[108:111]
	v_mfma_f32_16x16x32_bf16 v[100:103], v[152:155], v[224:227], v[100:103]
	v_mfma_f32_16x16x32_bf16 v[92:95], v[160:163], v[224:227], v[92:95]
	v_mfma_f32_16x16x32_bf16 v[80:83], v[152:155], v[232:235], v[80:83]
	v_mfma_f32_16x16x32_bf16 v[72:75], v[160:163], v[232:235], v[72:75]
	v_mfma_f32_16x16x32_bf16 v[124:127], v[156:159], v[198:201], v[124:127]
	v_mfma_f32_16x16x32_bf16 v[120:123], v[164:167], v[198:201], v[120:123]
	v_mfma_f32_16x16x32_bf16 v[116:119], v[156:159], v[206:209], v[116:119]
	v_mfma_f32_16x16x32_bf16 v[108:111], v[164:167], v[206:209], v[108:111]
	v_mfma_f32_16x16x32_bf16 v[100:103], v[156:159], v[228:231], v[100:103]
	v_mfma_f32_16x16x32_bf16 v[92:95], v[164:167], v[228:231], v[92:95]
	v_mfma_f32_16x16x32_bf16 v[80:83], v[156:159], v[236:239], v[80:83]
	v_mfma_f32_16x16x32_bf16 v[72:75], v[164:167], v[236:239], v[72:75]
	s_setprio 1
	s_setprio 0
	v_mfma_f32_16x16x32_bf16 v[112:115], v[168:171], v[194:197], v[112:115]
	v_mfma_f32_16x16x32_bf16 v[104:107], v[176:179], v[194:197], v[104:107]
	v_mfma_f32_16x16x32_bf16 v[96:99], v[168:171], v[202:205], v[96:99]
	v_mfma_f32_16x16x32_bf16 v[88:91], v[176:179], v[202:205], v[88:91]
	v_mfma_f32_16x16x32_bf16 v[84:87], v[168:171], v[224:227], v[84:87]
	v_mfma_f32_16x16x32_bf16 v[76:79], v[176:179], v[224:227], v[76:79]
	v_mfma_f32_16x16x32_bf16 v[68:71], v[168:171], v[232:235], v[68:71]
	v_mfma_f32_16x16x32_bf16 v[64:67], v[176:179], v[232:235], v[64:67]
	v_mfma_f32_16x16x32_bf16 v[112:115], v[172:175], v[198:201], v[112:115]
	v_mfma_f32_16x16x32_bf16 v[104:107], v[180:183], v[198:201], v[104:107]
	v_mfma_f32_16x16x32_bf16 v[96:99], v[172:175], v[206:209], v[96:99]
	v_mfma_f32_16x16x32_bf16 v[88:91], v[180:183], v[206:209], v[88:91]
	v_mfma_f32_16x16x32_bf16 v[84:87], v[172:175], v[228:231], v[84:87]
	v_mfma_f32_16x16x32_bf16 v[76:79], v[180:183], v[228:231], v[76:79]
	v_mfma_f32_16x16x32_bf16 v[68:71], v[172:175], v[236:239], v[68:71]
	v_mfma_f32_16x16x32_bf16 v[64:67], v[180:183], v[236:239], v[64:67]
	s_setprio 1
	s_barrier
	s_add_i32 s12, s28, s30
	v_lshl_add_u64 v[216:217], v[216:217], 0, s[68:69]
	s_mov_b32 m0, s12
	ds_read_b128 v[194:197], v149 offset:49152
	ds_read_b128 v[198:201], v149 offset:50176
	ds_read_b128 v[202:205], v149 offset:51200
	ds_read_b128 v[206:209], v149 offset:52224
	ds_read_b128 v[224:227], v149 offset:53248
	ds_read_b128 v[228:231], v149 offset:54272
	ds_read_b128 v[232:235], v149 offset:55296
	ds_read_b128 v[236:239], v149 offset:56320
	global_load_lds_dwordx4 v[216:217], off
	v_lshl_add_u64 v[216:217], v[218:219], 0, s[68:69]
	s_add_i32 m0, s12, 0x2000
	v_lshl_add_u64 v[210:211], v[210:211], 0, s[74:75]
	s_add_i32 s12, s29, s30
	global_load_lds_dwordx4 v[216:217], off
	v_lshl_add_u64 v[216:217], v[210:211], 0, v[132:133]
	s_mov_b32 m0, s12
	v_lshl_add_u64 v[210:211], v[210:211], 0, v[128:129]
	global_load_lds_dwordx4 v[216:217], off
	s_add_i32 m0, s12, 0x2000
	s_nop 0
	global_load_lds_dwordx4 v[210:211], off
	v_lshl_add_u64 v[210:211], v[220:221], 0, s[68:69]
	s_mov_b32 m0, s44
	s_nop 0
	global_load_lds_dwordx4 v[210:211], off
	v_lshl_add_u64 v[210:211], v[240:241], 0, s[68:69]
	s_mov_b32 m0, s45
	s_nop 0
	global_load_lds_dwordx4 v[210:211], off
	s_waitcnt vmcnt(6)
	s_waitcnt lgkmcnt(0)
	s_barrier
	s_setprio 0
	s_waitcnt lgkmcnt(0)
	v_mfma_f32_16x16x32_bf16 v[60:63], v[152:155], v[194:197], v[60:63]
	v_mfma_f32_16x16x32_bf16 v[56:59], v[160:163], v[194:197], v[56:59]
	v_mfma_f32_16x16x32_bf16 v[52:55], v[152:155], v[202:205], v[52:55]
	v_mfma_f32_16x16x32_bf16 v[44:47], v[160:163], v[202:205], v[44:47]
	v_mfma_f32_16x16x32_bf16 v[36:39], v[152:155], v[224:227], v[36:39]
	v_mfma_f32_16x16x32_bf16 v[28:31], v[160:163], v[224:227], v[28:31]
	v_mfma_f32_16x16x32_bf16 v[20:23], v[152:155], v[232:235], v[20:23]
	v_mfma_f32_16x16x32_bf16 v[12:15], v[160:163], v[232:235], v[12:15]
	v_mfma_f32_16x16x32_bf16 v[60:63], v[156:159], v[198:201], v[60:63]
	v_mfma_f32_16x16x32_bf16 v[56:59], v[164:167], v[198:201], v[56:59]
	v_mfma_f32_16x16x32_bf16 v[52:55], v[156:159], v[206:209], v[52:55]
	v_mfma_f32_16x16x32_bf16 v[44:47], v[164:167], v[206:209], v[44:47]
	v_mfma_f32_16x16x32_bf16 v[36:39], v[156:159], v[228:231], v[36:39]
	v_mfma_f32_16x16x32_bf16 v[28:31], v[164:167], v[228:231], v[28:31]
	v_mfma_f32_16x16x32_bf16 v[20:23], v[156:159], v[236:239], v[20:23]
	v_mfma_f32_16x16x32_bf16 v[12:15], v[164:167], v[236:239], v[12:15]
	s_setprio 1
	s_setprio 0
	v_mfma_f32_16x16x32_bf16 v[48:51], v[168:171], v[194:197], v[48:51]
	v_mfma_f32_16x16x32_bf16 v[40:43], v[176:179], v[194:197], v[40:43]
	v_mfma_f32_16x16x32_bf16 v[32:35], v[168:171], v[202:205], v[32:35]
	v_mfma_f32_16x16x32_bf16 v[24:27], v[176:179], v[202:205], v[24:27]
	v_mfma_f32_16x16x32_bf16 v[16:19], v[168:171], v[224:227], v[16:19]
	v_mfma_f32_16x16x32_bf16 v[8:11], v[176:179], v[224:227], v[8:11]
	v_mfma_f32_16x16x32_bf16 v[4:7], v[168:171], v[232:235], v[4:7]
	v_mfma_f32_16x16x32_bf16 v[0:3], v[176:179], v[232:235], v[0:3]
	v_mfma_f32_16x16x32_bf16 v[48:51], v[172:175], v[198:201], v[48:51]
	v_mfma_f32_16x16x32_bf16 v[40:43], v[180:183], v[198:201], v[40:43]
	v_mfma_f32_16x16x32_bf16 v[32:35], v[172:175], v[206:209], v[32:35]
	v_mfma_f32_16x16x32_bf16 v[24:27], v[180:183], v[206:209], v[24:27]
	v_mfma_f32_16x16x32_bf16 v[16:19], v[172:175], v[228:231], v[16:19]
	v_mfma_f32_16x16x32_bf16 v[8:11], v[180:183], v[228:231], v[8:11]
	v_mfma_f32_16x16x32_bf16 v[4:7], v[172:175], v[236:239], v[4:7]
	v_mfma_f32_16x16x32_bf16 v[0:3], v[180:183], v[236:239], v[0:3]
	s_setprio 1
	s_barrier
	s_add_i32 s59, s59, 2
	v_lshl_add_u64 v[144:145], v[144:145], 0, s[60:61]
	s_cmp_gt_u32 s59, 41
	s_mov_b64 s[12:13], s[14:15]
	s_cbranch_scc0 .LBB0_1491
	s_mov_b64 s[14:15], 0xb0000
	s_and_b64 vcc, exec, s[6:7]
	s_cbranch_vccz .LBB0_1494
	s_barrier

.LBB0_1587:
	s_add_u32 s28, s24, 0xfff80080
	s_addc_u32 s29, s25, -1
	s_add_i32 s48, 0, 0x10000
	s_cmp_eq_u32 s51, 28
	s_cselect_b32 s39, s9, s29
	s_cselect_b32 s38, s11, s28
	s_cselect_b32 s31, s45, s50
	s_cselect_b32 s30, s46, s47
	s_add_i32 s49, 0, 0x14000
	v_add_u32_e32 v154, s48, v139
	v_add_u32_e32 v170, s49, v139
	ds_read_b128 v[142:145], v154
	ds_read_b128 v[146:149], v154 offset:1024
	ds_read_b128 v[150:153], v154 offset:2048
	ds_read_b128 v[154:157], v154 offset:3072
	ds_read_b128 v[158:161], v170
	ds_read_b128 v[162:165], v170 offset:1024
	ds_read_b128 v[166:169], v170 offset:2048
	ds_read_b128 v[170:173], v170 offset:3072
	v_lshl_add_u64 v[182:183], s[24:25], 0, v[134:135]
	s_add_i32 m0, s20, 0xc000
	ds_read_b128 v[174:177], v141
	ds_read_b128 v[178:181], v141 offset:1024
	ds_read_b128 v[194:197], v141 offset:2048
	ds_read_b128 v[198:201], v141 offset:3072
	ds_read_b128 v[202:205], v141 offset:4096
	ds_read_b128 v[206:209], v141 offset:5120
	ds_read_b128 v[224:227], v141 offset:6144
	ds_read_b128 v[228:231], v141 offset:7168
	global_load_lds_dwordx4 v[182:183], off
	v_lshl_add_u64 v[182:183], s[24:25], 0, v[136:137]
	s_add_i32 m0, s20, 0xe000
	s_nop 0
	global_load_lds_dwordx4 v[182:183], off
	s_waitcnt vmcnt(8)
	s_waitcnt lgkmcnt(0)
	s_barrier
	s_setprio 0
	s_waitcnt lgkmcnt(0)
	v_mfma_f32_16x16x32_bf16 v[124:127], v[142:145], v[174:177], v[124:127]
	v_mfma_f32_16x16x32_bf16 v[116:119], v[150:153], v[174:177], v[116:119]
	v_mfma_f32_16x16x32_bf16 v[108:111], v[142:145], v[194:197], v[108:111]
	v_mfma_f32_16x16x32_bf16 v[100:103], v[150:153], v[194:197], v[100:103]
	v_mfma_f32_16x16x32_bf16 v[92:95], v[142:145], v[202:205], v[92:95]
	v_mfma_f32_16x16x32_bf16 v[84:87], v[150:153], v[202:205], v[84:87]
	v_mfma_f32_16x16x32_bf16 v[76:79], v[142:145], v[224:227], v[76:79]
	v_mfma_f32_16x16x32_bf16 v[68:71], v[150:153], v[224:227], v[68:71]
	v_mfma_f32_16x16x32_bf16 v[124:127], v[146:149], v[178:181], v[124:127]
	v_mfma_f32_16x16x32_bf16 v[116:119], v[154:157], v[178:181], v[116:119]
	v_mfma_f32_16x16x32_bf16 v[108:111], v[146:149], v[198:201], v[108:111]
	v_mfma_f32_16x16x32_bf16 v[100:103], v[154:157], v[198:201], v[100:103]
	v_mfma_f32_16x16x32_bf16 v[92:95], v[146:149], v[206:209], v[92:95]
	v_mfma_f32_16x16x32_bf16 v[84:87], v[154:157], v[206:209], v[84:87]
	v_mfma_f32_16x16x32_bf16 v[76:79], v[146:149], v[228:231], v[76:79]
	v_mfma_f32_16x16x32_bf16 v[68:71], v[154:157], v[228:231], v[68:71]
	s_setprio 1
	s_setprio 0
	v_mfma_f32_16x16x32_bf16 v[120:123], v[158:161], v[174:177], v[120:123]
	v_mfma_f32_16x16x32_bf16 v[112:115], v[166:169], v[174:177], v[112:115]
	v_mfma_f32_16x16x32_bf16 v[104:107], v[158:161], v[194:197], v[104:107]
	v_mfma_f32_16x16x32_bf16 v[96:99], v[166:169], v[194:197], v[96:99]
	v_mfma_f32_16x16x32_bf16 v[88:91], v[158:161], v[202:205], v[88:91]
	v_mfma_f32_16x16x32_bf16 v[80:83], v[166:169], v[202:205], v[80:83]
	v_mfma_f32_16x16x32_bf16 v[72:75], v[158:161], v[224:227], v[72:75]
	v_mfma_f32_16x16x32_bf16 v[64:67], v[166:169], v[224:227], v[64:67]
	v_mfma_f32_16x16x32_bf16 v[120:123], v[162:165], v[178:181], v[120:123]
	v_mfma_f32_16x16x32_bf16 v[112:115], v[170:173], v[178:181], v[112:115]
	v_mfma_f32_16x16x32_bf16 v[104:107], v[162:165], v[198:201], v[104:107]
	v_mfma_f32_16x16x32_bf16 v[96:99], v[170:173], v[198:201], v[96:99]
	v_mfma_f32_16x16x32_bf16 v[88:91], v[162:165], v[206:209], v[88:91]
	v_mfma_f32_16x16x32_bf16 v[80:83], v[170:173], v[206:209], v[80:83]
	v_mfma_f32_16x16x32_bf16 v[72:75], v[162:165], v[228:231], v[72:75]
	v_mfma_f32_16x16x32_bf16 v[64:67], v[170:173], v[228:231], v[64:67]
	s_setprio 1
	s_barrier
	s_add_i32 s28, s48, s4
	v_lshl_add_u64 v[182:183], s[30:31], 0, v[184:185]
	s_mov_b32 m0, s28
	ds_read_b128 v[174:177], v141 offset:16384
	ds_read_b128 v[178:181], v141 offset:17408
	ds_read_b128 v[194:197], v141 offset:18432
	ds_read_b128 v[198:201], v141 offset:19456
	ds_read_b128 v[202:205], v141 offset:20480
	ds_read_b128 v[206:209], v141 offset:21504
	ds_read_b128 v[224:227], v141 offset:22528
	ds_read_b128 v[228:231], v141 offset:23552
	global_load_lds_dwordx4 v[182:183], off
	s_add_i32 m0, s28, 0x2000
	s_add_u32 s28, s30, 0x80000
	v_lshl_add_u64 v[210:211], s[30:31], 0, v[128:129]
	s_addc_u32 s29, s31, 0
	s_add_i32 s48, s49, s4
	global_load_lds_dwordx4 v[210:211], off
	v_lshl_add_u64 v[216:217], s[28:29], 0, v[184:185]
	s_mov_b32 m0, s48
	v_lshl_add_u64 v[218:219], s[38:39], 0, v[130:131]
	global_load_lds_dwordx4 v[216:217], off
	v_lshl_add_u64 v[216:217], s[28:29], 0, v[128:129]
	s_add_i32 m0, s48, 0x2000
	s_nop 0
	global_load_lds_dwordx4 v[216:217], off
	v_lshl_add_u64 v[216:217], s[38:39], 0, v[132:133]
	s_waitcnt vmcnt(6)
	s_waitcnt lgkmcnt(0)
	s_barrier
	s_setprio 0
	s_waitcnt lgkmcnt(0)
	v_mfma_f32_16x16x32_bf16 v[60:63], v[142:145], v[174:177], v[60:63]
	v_mfma_f32_16x16x32_bf16 v[52:55], v[150:153], v[174:177], v[52:55]
	v_mfma_f32_16x16x32_bf16 v[44:47], v[142:145], v[194:197], v[44:47]
	v_mfma_f32_16x16x32_bf16 v[36:39], v[150:153], v[194:197], v[36:39]
	v_mfma_f32_16x16x32_bf16 v[28:31], v[142:145], v[202:205], v[28:31]
	v_mfma_f32_16x16x32_bf16 v[20:23], v[150:153], v[202:205], v[20:23]
	v_mfma_f32_16x16x32_bf16 v[12:15], v[142:145], v[224:227], v[12:15]
	v_mfma_f32_16x16x32_bf16 v[4:7], v[150:153], v[224:227], v[4:7]
	v_mfma_f32_16x16x32_bf16 v[60:63], v[146:149], v[178:181], v[60:63]
	v_mfma_f32_16x16x32_bf16 v[52:55], v[154:157], v[178:181], v[52:55]
	v_mfma_f32_16x16x32_bf16 v[44:47], v[146:149], v[198:201], v[44:47]
	v_mfma_f32_16x16x32_bf16 v[36:39], v[154:157], v[198:201], v[36:39]
	v_mfma_f32_16x16x32_bf16 v[28:31], v[146:149], v[206:209], v[28:31]
	v_mfma_f32_16x16x32_bf16 v[20:23], v[154:157], v[206:209], v[20:23]
	v_mfma_f32_16x16x32_bf16 v[12:15], v[146:149], v[228:231], v[12:15]
	v_mfma_f32_16x16x32_bf16 v[4:7], v[154:157], v[228:231], v[4:7]
	s_setprio 1
	s_setprio 0
	v_mfma_f32_16x16x32_bf16 v[56:59], v[158:161], v[174:177], v[56:59]
	v_mfma_f32_16x16x32_bf16 v[48:51], v[166:169], v[174:177], v[48:51]
	v_mfma_f32_16x16x32_bf16 v[40:43], v[158:161], v[194:197], v[40:43]
	v_mfma_f32_16x16x32_bf16 v[32:35], v[166:169], v[194:197], v[32:35]
	v_mfma_f32_16x16x32_bf16 v[24:27], v[158:161], v[202:205], v[24:27]
	v_mfma_f32_16x16x32_bf16 v[16:19], v[166:169], v[202:205], v[16:19]
	v_mfma_f32_16x16x32_bf16 v[8:11], v[158:161], v[224:227], v[8:11]
	v_mfma_f32_16x16x32_bf16 v[0:3], v[166:169], v[224:227], v[0:3]
	v_mfma_f32_16x16x32_bf16 v[56:59], v[162:165], v[178:181], v[56:59]
	v_mfma_f32_16x16x32_bf16 v[48:51], v[170:173], v[178:181], v[48:51]
	v_mfma_f32_16x16x32_bf16 v[40:43], v[162:165], v[198:201], v[40:43]
	v_mfma_f32_16x16x32_bf16 v[32:35], v[170:173], v[198:201], v[32:35]
	v_mfma_f32_16x16x32_bf16 v[24:27], v[162:165], v[206:209], v[24:27]
	v_mfma_f32_16x16x32_bf16 v[16:19], v[170:173], v[206:209], v[16:19]
	v_mfma_f32_16x16x32_bf16 v[8:11], v[162:165], v[228:231], v[8:11]
	v_mfma_f32_16x16x32_bf16 v[0:3], v[170:173], v[228:231], v[0:3]
	s_setprio 1
	s_barrier
	s_add_i32 s48, 0, 0x18000
	s_add_i32 s49, 0, 0x1c000
	v_add_u32_e32 v154, s48, v139
	v_add_u32_e32 v170, s49, v139
	ds_read_b128 v[142:145], v154
	ds_read_b128 v[146:149], v154 offset:1024
	ds_read_b128 v[150:153], v154 offset:2048
	ds_read_b128 v[154:157], v154 offset:3072
	ds_read_b128 v[158:161], v170
	ds_read_b128 v[162:165], v170 offset:1024
	ds_read_b128 v[166:169], v170 offset:2048
	ds_read_b128 v[170:173], v170 offset:3072
	s_add_u32 s28, s38, 0x80000
	s_addc_u32 s29, s39, 0
	s_mov_b32 m0, s26
	v_lshl_add_u64 v[232:233], s[28:29], 0, v[132:133]
	ds_read_b128 v[174:177], v141 offset:32768
	ds_read_b128 v[178:181], v141 offset:33792
	ds_read_b128 v[194:197], v141 offset:34816
	ds_read_b128 v[198:201], v141 offset:35840
	ds_read_b128 v[202:205], v141 offset:36864
	ds_read_b128 v[206:209], v141 offset:37888
	ds_read_b128 v[224:227], v141 offset:38912
	ds_read_b128 v[228:231], v141 offset:39936
	global_load_lds_dwordx4 v[232:233], off
	v_lshl_add_u64 v[232:233], s[28:29], 0, v[130:131]
	s_mov_b32 m0, s27
	s_nop 0
	global_load_lds_dwordx4 v[232:233], off
	s_mov_b32 m0, s20
	s_nop 0
	global_load_lds_dwordx4 v[216:217], off
	s_mov_b32 m0, s21
	s_nop 0
	global_load_lds_dwordx4 v[218:219], off
	s_waitcnt vmcnt(8)
	s_waitcnt lgkmcnt(0)
	s_barrier
	s_setprio 0
	s_waitcnt lgkmcnt(0)
	v_mfma_f32_16x16x32_bf16 v[124:127], v[142:145], v[174:177], v[124:127]
	v_mfma_f32_16x16x32_bf16 v[116:119], v[150:153], v[174:177], v[116:119]
	v_mfma_f32_16x16x32_bf16 v[108:111], v[142:145], v[194:197], v[108:111]
	v_mfma_f32_16x16x32_bf16 v[100:103], v[150:153], v[194:197], v[100:103]
	v_mfma_f32_16x16x32_bf16 v[92:95], v[142:145], v[202:205], v[92:95]
	v_mfma_f32_16x16x32_bf16 v[84:87], v[150:153], v[202:205], v[84:87]
	v_mfma_f32_16x16x32_bf16 v[76:79], v[142:145], v[224:227], v[76:79]
	v_mfma_f32_16x16x32_bf16 v[68:71], v[150:153], v[224:227], v[68:71]
	v_mfma_f32_16x16x32_bf16 v[124:127], v[146:149], v[178:181], v[124:127]
	v_mfma_f32_16x16x32_bf16 v[116:119], v[154:157], v[178:181], v[116:119]
	v_mfma_f32_16x16x32_bf16 v[108:111], v[146:149], v[198:201], v[108:111]
	v_mfma_f32_16x16x32_bf16 v[100:103], v[154:157], v[198:201], v[100:103]
	v_mfma_f32_16x16x32_bf16 v[92:95], v[146:149], v[206:209], v[92:95]
	v_mfma_f32_16x16x32_bf16 v[84:87], v[154:157], v[206:209], v[84:87]
	v_mfma_f32_16x16x32_bf16 v[76:79], v[146:149], v[228:231], v[76:79]
	v_mfma_f32_16x16x32_bf16 v[68:71], v[154:157], v[228:231], v[68:71]
	s_setprio 1
	s_setprio 0
	v_mfma_f32_16x16x32_bf16 v[120:123], v[158:161], v[174:177], v[120:123]
	v_mfma_f32_16x16x32_bf16 v[112:115], v[166:169], v[174:177], v[112:115]
	v_mfma_f32_16x16x32_bf16 v[104:107], v[158:161], v[194:197], v[104:107]
	v_mfma_f32_16x16x32_bf16 v[96:99], v[166:169], v[194:197], v[96:99]
	v_mfma_f32_16x16x32_bf16 v[88:91], v[158:161], v[202:205], v[88:91]
	v_mfma_f32_16x16x32_bf16 v[80:83], v[166:169], v[202:205], v[80:83]
	v_mfma_f32_16x16x32_bf16 v[72:75], v[158:161], v[224:227], v[72:75]
	v_mfma_f32_16x16x32_bf16 v[64:67], v[166:169], v[224:227], v[64:67]
	v_mfma_f32_16x16x32_bf16 v[120:123], v[162:165], v[178:181], v[120:123]
	v_mfma_f32_16x16x32_bf16 v[112:115], v[170:173], v[178:181], v[112:115]
	v_mfma_f32_16x16x32_bf16 v[104:107], v[162:165], v[198:201], v[104:107]
	v_mfma_f32_16x16x32_bf16 v[96:99], v[170:173], v[198:201], v[96:99]
	v_mfma_f32_16x16x32_bf16 v[88:91], v[162:165], v[206:209], v[88:91]
	v_mfma_f32_16x16x32_bf16 v[80:83], v[170:173], v[206:209], v[80:83]
	v_mfma_f32_16x16x32_bf16 v[72:75], v[162:165], v[228:231], v[72:75]
	v_mfma_f32_16x16x32_bf16 v[64:67], v[170:173], v[228:231], v[64:67]
	s_setprio 1
	s_barrier
	s_add_i32 s28, s48, s4
	v_lshl_add_u64 v[182:183], v[182:183], 0, s[68:69]
	s_mov_b32 m0, s28
	ds_read_b128 v[174:177], v141 offset:49152
	ds_read_b128 v[178:181], v141 offset:50176
	ds_read_b128 v[194:197], v141 offset:51200
	ds_read_b128 v[198:201], v141 offset:52224
	ds_read_b128 v[202:205], v141 offset:53248
	ds_read_b128 v[206:209], v141 offset:54272
	ds_read_b128 v[224:227], v141 offset:55296
	ds_read_b128 v[228:231], v141 offset:56320
	global_load_lds_dwordx4 v[182:183], off
	s_add_i32 m0, s28, 0x2000
	s_add_u32 s28, s30, 0x80080
	v_lshl_add_u64 v[182:183], v[210:211], 0, s[68:69]
	s_addc_u32 s29, s31, 0
	s_add_i32 s30, s49, s4
	global_load_lds_dwordx4 v[182:183], off
	v_lshl_add_u64 v[182:183], s[28:29], 0, v[184:185]
	s_mov_b32 m0, s30
	s_nop 0
	global_load_lds_dwordx4 v[182:183], off
	v_lshl_add_u64 v[182:183], s[28:29], 0, v[128:129]
	s_add_i32 m0, s30, 0x2000
	s_nop 0
	global_load_lds_dwordx4 v[182:183], off
	v_lshl_add_u64 v[182:183], v[216:217], 0, s[68:69]
	s_mov_b32 m0, s40
	s_nop 0
	global_load_lds_dwordx4 v[182:183], off
	v_lshl_add_u64 v[182:183], v[218:219], 0, s[68:69]
	s_mov_b32 m0, s41
	s_nop 0
	global_load_lds_dwordx4 v[182:183], off
	s_waitcnt vmcnt(6)
	s_waitcnt lgkmcnt(0)
	s_barrier
	s_setprio 0
	s_waitcnt lgkmcnt(0)
	v_mfma_f32_16x16x32_bf16 v[60:63], v[142:145], v[174:177], v[60:63]
	v_mfma_f32_16x16x32_bf16 v[52:55], v[150:153], v[174:177], v[52:55]
	v_mfma_f32_16x16x32_bf16 v[44:47], v[142:145], v[194:197], v[44:47]
	v_mfma_f32_16x16x32_bf16 v[36:39], v[150:153], v[194:197], v[36:39]
	v_mfma_f32_16x16x32_bf16 v[28:31], v[142:145], v[202:205], v[28:31]
	v_mfma_f32_16x16x32_bf16 v[20:23], v[150:153], v[202:205], v[20:23]
	v_mfma_f32_16x16x32_bf16 v[12:15], v[142:145], v[224:227], v[12:15]
	v_mfma_f32_16x16x32_bf16 v[4:7], v[150:153], v[224:227], v[4:7]
	v_mfma_f32_16x16x32_bf16 v[60:63], v[146:149], v[178:181], v[60:63]
	v_mfma_f32_16x16x32_bf16 v[52:55], v[154:157], v[178:181], v[52:55]
	v_mfma_f32_16x16x32_bf16 v[44:47], v[146:149], v[198:201], v[44:47]
	v_mfma_f32_16x16x32_bf16 v[36:39], v[154:157], v[198:201], v[36:39]
	v_mfma_f32_16x16x32_bf16 v[28:31], v[146:149], v[206:209], v[28:31]
	v_mfma_f32_16x16x32_bf16 v[20:23], v[154:157], v[206:209], v[20:23]
	v_mfma_f32_16x16x32_bf16 v[12:15], v[146:149], v[228:231], v[12:15]
	v_mfma_f32_16x16x32_bf16 v[4:7], v[154:157], v[228:231], v[4:7]
	s_setprio 1
	s_setprio 0
	v_mfma_f32_16x16x32_bf16 v[56:59], v[158:161], v[174:177], v[56:59]
	v_mfma_f32_16x16x32_bf16 v[48:51], v[166:169], v[174:177], v[48:51]
	v_mfma_f32_16x16x32_bf16 v[40:43], v[158:161], v[194:197], v[40:43]
	v_mfma_f32_16x16x32_bf16 v[32:35], v[166:169], v[194:197], v[32:35]
	v_mfma_f32_16x16x32_bf16 v[24:27], v[158:161], v[202:205], v[24:27]
	v_mfma_f32_16x16x32_bf16 v[16:19], v[166:169], v[202:205], v[16:19]
	v_mfma_f32_16x16x32_bf16 v[8:11], v[158:161], v[224:227], v[8:11]
	v_mfma_f32_16x16x32_bf16 v[0:3], v[166:169], v[224:227], v[0:3]
	v_mfma_f32_16x16x32_bf16 v[56:59], v[162:165], v[178:181], v[56:59]
	v_mfma_f32_16x16x32_bf16 v[48:51], v[170:173], v[178:181], v[48:51]
	v_mfma_f32_16x16x32_bf16 v[40:43], v[162:165], v[198:201], v[40:43]
	v_mfma_f32_16x16x32_bf16 v[32:35], v[170:173], v[198:201], v[32:35]
	v_mfma_f32_16x16x32_bf16 v[24:27], v[162:165], v[206:209], v[24:27]
	v_mfma_f32_16x16x32_bf16 v[16:19], v[170:173], v[206:209], v[16:19]
	v_mfma_f32_16x16x32_bf16 v[8:11], v[162:165], v[228:231], v[8:11]
	v_mfma_f32_16x16x32_bf16 v[0:3], v[170:173], v[228:231], v[0:3]
	s_setprio 1
	s_barrier
	s_add_i32 s51, s51, 2
	s_add_u32 s24, s24, 0x100
	s_addc_u32 s25, s25, 0
	s_add_u32 s47, s47, 0x100
	s_addc_u32 s50, s50, 0
	s_cmp_gt_u32 s51, 29
	s_cbranch_scc0 .LBB0_1587
	s_and_b64 vcc, exec, s[6:7]
	s_cbranch_vccz .LBB0_1590
	s_barrier

.LBB0_1661:
	s_add_u32 s24, s18, 0x100
	s_addc_u32 s25, s19, 0
	s_add_i32 s28, 0, 0x10000
	s_cmpk_eq_i32 s61, 0x54
	s_cselect_b32 s39, s51, s25
	s_cselect_b32 s38, s52, s24
	s_cselect_b32 s31, s53, s60
	s_cselect_b32 s30, s58, s59
	s_add_i32 s29, 0, 0x14000
	s_waitcnt vmcnt(0)
	v_add_u32_e32 v84, s28, v163
	v_add_u32_e32 v170, s29, v163
	ds_read_b128 v[64:67], v84
	ds_read_b128 v[68:71], v84 offset:1024
	ds_read_b128 v[80:83], v84 offset:2048
	ds_read_b128 v[84:87], v84 offset:3072
	ds_read_b128 v[154:157], v170
	ds_read_b128 v[158:161], v170 offset:1024
	ds_read_b128 v[166:169], v170 offset:2048
	ds_read_b128 v[170:173], v170 offset:3072
	v_lshl_add_u64 v[182:183], s[18:19], 0, v[150:151]
	s_add_i32 m0, s20, 0xc000
	ds_read_b128 v[174:177], v165
	ds_read_b128 v[178:181], v165 offset:1024
	ds_read_b128 v[194:197], v165 offset:2048
	ds_read_b128 v[198:201], v165 offset:3072
	ds_read_b128 v[202:205], v165 offset:4096
	ds_read_b128 v[206:209], v165 offset:5120
	ds_read_b128 v[224:227], v165 offset:6144
	ds_read_b128 v[228:231], v165 offset:7168
	global_load_lds_dwordx4 v[182:183], off
	v_lshl_add_u64 v[182:183], s[18:19], 0, v[152:153]
	s_add_i32 m0, s20, 0xe000
	s_nop 0
	global_load_lds_dwordx4 v[182:183], off
	s_waitcnt vmcnt(8)
	s_waitcnt lgkmcnt(0)
	s_barrier
	s_setprio 0
	s_waitcnt lgkmcnt(0)
	v_mfma_f32_16x16x32_bf16 v[140:143], v[64:67], v[174:177], v[140:143]
	v_mfma_f32_16x16x32_bf16 v[136:139], v[80:83], v[174:177], v[136:139]
	v_mfma_f32_16x16x32_bf16 v[124:127], v[64:67], v[194:197], v[124:127]
	v_mfma_f32_16x16x32_bf16 v[120:123], v[80:83], v[194:197], v[120:123]
	v_mfma_f32_16x16x32_bf16 v[108:111], v[64:67], v[202:205], v[108:111]
	v_mfma_f32_16x16x32_bf16 v[104:107], v[80:83], v[202:205], v[104:107]
	v_mfma_f32_16x16x32_bf16 v[92:95], v[64:67], v[224:227], v[92:95]
	v_mfma_f32_16x16x32_bf16 v[88:91], v[80:83], v[224:227], v[88:91]
	v_mfma_f32_16x16x32_bf16 v[140:143], v[68:71], v[178:181], v[140:143]
	v_mfma_f32_16x16x32_bf16 v[136:139], v[84:87], v[178:181], v[136:139]
	v_mfma_f32_16x16x32_bf16 v[124:127], v[68:71], v[198:201], v[124:127]
	v_mfma_f32_16x16x32_bf16 v[120:123], v[84:87], v[198:201], v[120:123]
	v_mfma_f32_16x16x32_bf16 v[108:111], v[68:71], v[206:209], v[108:111]
	v_mfma_f32_16x16x32_bf16 v[104:107], v[84:87], v[206:209], v[104:107]
	v_mfma_f32_16x16x32_bf16 v[92:95], v[68:71], v[228:231], v[92:95]
	v_mfma_f32_16x16x32_bf16 v[88:91], v[84:87], v[228:231], v[88:91]
	s_setprio 1
	s_setprio 0
	v_mfma_f32_16x16x32_bf16 v[132:135], v[154:157], v[174:177], v[132:135]
	v_mfma_f32_16x16x32_bf16 v[128:131], v[166:169], v[174:177], v[128:131]
	v_mfma_f32_16x16x32_bf16 v[116:119], v[154:157], v[194:197], v[116:119]
	v_mfma_f32_16x16x32_bf16 v[112:115], v[166:169], v[194:197], v[112:115]
	v_mfma_f32_16x16x32_bf16 v[100:103], v[154:157], v[202:205], v[100:103]
	v_mfma_f32_16x16x32_bf16 v[96:99], v[166:169], v[202:205], v[96:99]
	v_mfma_f32_16x16x32_bf16 v[76:79], v[154:157], v[224:227], v[76:79]
	v_mfma_f32_16x16x32_bf16 v[72:75], v[166:169], v[224:227], v[72:75]
	v_mfma_f32_16x16x32_bf16 v[132:135], v[158:161], v[178:181], v[132:135]
	v_mfma_f32_16x16x32_bf16 v[128:131], v[170:173], v[178:181], v[128:131]
	v_mfma_f32_16x16x32_bf16 v[116:119], v[158:161], v[198:201], v[116:119]
	v_mfma_f32_16x16x32_bf16 v[112:115], v[170:173], v[198:201], v[112:115]
	v_mfma_f32_16x16x32_bf16 v[100:103], v[158:161], v[206:209], v[100:103]
	v_mfma_f32_16x16x32_bf16 v[96:99], v[170:173], v[206:209], v[96:99]
	v_mfma_f32_16x16x32_bf16 v[76:79], v[158:161], v[228:231], v[76:79]
	v_mfma_f32_16x16x32_bf16 v[72:75], v[170:173], v[228:231], v[72:75]
	s_setprio 1
	s_barrier
	s_add_i32 s18, s28, s4
	v_lshl_add_u64 v[182:183], s[30:31], 0, v[184:185]
	s_mov_b32 m0, s18
	ds_read_b128 v[174:177], v165 offset:16384
	ds_read_b128 v[178:181], v165 offset:17408
	ds_read_b128 v[194:197], v165 offset:18432
	ds_read_b128 v[198:201], v165 offset:19456
	ds_read_b128 v[202:205], v165 offset:20480
	ds_read_b128 v[206:209], v165 offset:21504
	ds_read_b128 v[224:227], v165 offset:22528
	ds_read_b128 v[228:231], v165 offset:23552
	global_load_lds_dwordx4 v[182:183], off
	s_add_i32 m0, s18, 0x2000
	s_add_u32 s18, s30, 0x160000
	v_lshl_add_u64 v[210:211], s[30:31], 0, v[144:145]
	s_addc_u32 s19, s31, 0
	s_add_i32 s28, s29, s4
	global_load_lds_dwordx4 v[210:211], off
	v_lshl_add_u64 v[216:217], s[18:19], 0, v[184:185]
	s_mov_b32 m0, s28
	v_lshl_add_u64 v[218:219], s[38:39], 0, v[146:147]
	global_load_lds_dwordx4 v[216:217], off
	v_lshl_add_u64 v[216:217], s[18:19], 0, v[144:145]
	s_add_i32 m0, s28, 0x2000
	s_nop 0
	global_load_lds_dwordx4 v[216:217], off
	v_lshl_add_u64 v[216:217], s[38:39], 0, v[148:149]
	s_waitcnt vmcnt(6)
	s_waitcnt lgkmcnt(0)
	s_barrier
	s_setprio 0
	s_waitcnt lgkmcnt(0)
	v_mfma_f32_16x16x32_bf16 v[60:63], v[64:67], v[174:177], v[60:63]
	v_mfma_f32_16x16x32_bf16 v[56:59], v[80:83], v[174:177], v[56:59]
	v_mfma_f32_16x16x32_bf16 v[44:47], v[64:67], v[194:197], v[44:47]
	v_mfma_f32_16x16x32_bf16 v[40:43], v[80:83], v[194:197], v[40:43]
	v_mfma_f32_16x16x32_bf16 v[28:31], v[64:67], v[202:205], v[28:31]
	v_mfma_f32_16x16x32_bf16 v[24:27], v[80:83], v[202:205], v[24:27]
	v_mfma_f32_16x16x32_bf16 v[12:15], v[64:67], v[224:227], v[12:15]
	v_mfma_f32_16x16x32_bf16 v[8:11], v[80:83], v[224:227], v[8:11]
	v_mfma_f32_16x16x32_bf16 v[60:63], v[68:71], v[178:181], v[60:63]
	v_mfma_f32_16x16x32_bf16 v[56:59], v[84:87], v[178:181], v[56:59]
	v_mfma_f32_16x16x32_bf16 v[44:47], v[68:71], v[198:201], v[44:47]
	v_mfma_f32_16x16x32_bf16 v[40:43], v[84:87], v[198:201], v[40:43]
	v_mfma_f32_16x16x32_bf16 v[28:31], v[68:71], v[206:209], v[28:31]
	v_mfma_f32_16x16x32_bf16 v[24:27], v[84:87], v[206:209], v[24:27]
	v_mfma_f32_16x16x32_bf16 v[12:15], v[68:71], v[228:231], v[12:15]
	v_mfma_f32_16x16x32_bf16 v[8:11], v[84:87], v[228:231], v[8:11]
	s_setprio 1
	s_setprio 0
	v_mfma_f32_16x16x32_bf16 v[52:55], v[154:157], v[174:177], v[52:55]
	v_mfma_f32_16x16x32_bf16 v[48:51], v[166:169], v[174:177], v[48:51]
	v_mfma_f32_16x16x32_bf16 v[36:39], v[154:157], v[194:197], v[36:39]
	v_mfma_f32_16x16x32_bf16 v[32:35], v[166:169], v[194:197], v[32:35]
	v_mfma_f32_16x16x32_bf16 v[20:23], v[154:157], v[202:205], v[20:23]
	v_mfma_f32_16x16x32_bf16 v[16:19], v[166:169], v[202:205], v[16:19]
	v_mfma_f32_16x16x32_bf16 v[4:7], v[154:157], v[224:227], v[4:7]
	v_mfma_f32_16x16x32_bf16 v[0:3], v[166:169], v[224:227], v[0:3]
	v_mfma_f32_16x16x32_bf16 v[52:55], v[158:161], v[178:181], v[52:55]
	v_mfma_f32_16x16x32_bf16 v[48:51], v[170:173], v[178:181], v[48:51]
	v_mfma_f32_16x16x32_bf16 v[36:39], v[158:161], v[198:201], v[36:39]
	v_mfma_f32_16x16x32_bf16 v[32:35], v[170:173], v[198:201], v[32:35]
	v_mfma_f32_16x16x32_bf16 v[20:23], v[158:161], v[206:209], v[20:23]
	v_mfma_f32_16x16x32_bf16 v[16:19], v[170:173], v[206:209], v[16:19]
	v_mfma_f32_16x16x32_bf16 v[4:7], v[158:161], v[228:231], v[4:7]
	v_mfma_f32_16x16x32_bf16 v[0:3], v[170:173], v[228:231], v[0:3]
	s_setprio 1
	s_barrier
	s_add_i32 s28, 0, 0x18000
	s_add_i32 s29, 0, 0x1c000
	v_add_u32_e32 v84, s28, v163
	v_add_u32_e32 v170, s29, v163
	ds_read_b128 v[64:67], v84
	ds_read_b128 v[68:71], v84 offset:1024
	ds_read_b128 v[80:83], v84 offset:2048
	ds_read_b128 v[84:87], v84 offset:3072
	ds_read_b128 v[154:157], v170
	ds_read_b128 v[158:161], v170 offset:1024
	ds_read_b128 v[166:169], v170 offset:2048
	ds_read_b128 v[170:173], v170 offset:3072
	s_add_u32 s18, s38, 0x160000
	s_addc_u32 s19, s39, 0
	s_mov_b32 m0, s26
	v_lshl_add_u64 v[232:233], s[18:19], 0, v[148:149]
	ds_read_b128 v[174:177], v165 offset:32768
	ds_read_b128 v[178:181], v165 offset:33792
	ds_read_b128 v[194:197], v165 offset:34816
	ds_read_b128 v[198:201], v165 offset:35840
	ds_read_b128 v[202:205], v165 offset:36864
	ds_read_b128 v[206:209], v165 offset:37888
	ds_read_b128 v[224:227], v165 offset:38912
	ds_read_b128 v[228:231], v165 offset:39936
	global_load_lds_dwordx4 v[232:233], off
	v_lshl_add_u64 v[232:233], s[18:19], 0, v[146:147]
	s_mov_b32 m0, s27
	s_nop 0
	global_load_lds_dwordx4 v[232:233], off
	s_mov_b32 m0, s20
	s_nop 0
	global_load_lds_dwordx4 v[216:217], off
	s_mov_b32 m0, s21
	s_nop 0
	global_load_lds_dwordx4 v[218:219], off
	s_waitcnt vmcnt(8)
	s_waitcnt lgkmcnt(0)
	s_barrier
	s_setprio 0
	s_waitcnt lgkmcnt(0)
	v_mfma_f32_16x16x32_bf16 v[140:143], v[64:67], v[174:177], v[140:143]
	v_mfma_f32_16x16x32_bf16 v[136:139], v[80:83], v[174:177], v[136:139]
	v_mfma_f32_16x16x32_bf16 v[124:127], v[64:67], v[194:197], v[124:127]
	v_mfma_f32_16x16x32_bf16 v[120:123], v[80:83], v[194:197], v[120:123]
	v_mfma_f32_16x16x32_bf16 v[108:111], v[64:67], v[202:205], v[108:111]
	v_mfma_f32_16x16x32_bf16 v[104:107], v[80:83], v[202:205], v[104:107]
	v_mfma_f32_16x16x32_bf16 v[92:95], v[64:67], v[224:227], v[92:95]
	v_mfma_f32_16x16x32_bf16 v[88:91], v[80:83], v[224:227], v[88:91]
	v_mfma_f32_16x16x32_bf16 v[140:143], v[68:71], v[178:181], v[140:143]
	v_mfma_f32_16x16x32_bf16 v[136:139], v[84:87], v[178:181], v[136:139]
	v_mfma_f32_16x16x32_bf16 v[124:127], v[68:71], v[198:201], v[124:127]
	v_mfma_f32_16x16x32_bf16 v[120:123], v[84:87], v[198:201], v[120:123]
	v_mfma_f32_16x16x32_bf16 v[108:111], v[68:71], v[206:209], v[108:111]
	v_mfma_f32_16x16x32_bf16 v[104:107], v[84:87], v[206:209], v[104:107]
	v_mfma_f32_16x16x32_bf16 v[92:95], v[68:71], v[228:231], v[92:95]
	v_mfma_f32_16x16x32_bf16 v[88:91], v[84:87], v[228:231], v[88:91]
	s_setprio 1
	s_setprio 0
	v_mfma_f32_16x16x32_bf16 v[132:135], v[154:157], v[174:177], v[132:135]
	v_mfma_f32_16x16x32_bf16 v[128:131], v[166:169], v[174:177], v[128:131]
	v_mfma_f32_16x16x32_bf16 v[116:119], v[154:157], v[194:197], v[116:119]
	v_mfma_f32_16x16x32_bf16 v[112:115], v[166:169], v[194:197], v[112:115]
	v_mfma_f32_16x16x32_bf16 v[100:103], v[154:157], v[202:205], v[100:103]
	v_mfma_f32_16x16x32_bf16 v[96:99], v[166:169], v[202:205], v[96:99]
	v_mfma_f32_16x16x32_bf16 v[76:79], v[154:157], v[224:227], v[76:79]
	v_mfma_f32_16x16x32_bf16 v[72:75], v[166:169], v[224:227], v[72:75]
	v_mfma_f32_16x16x32_bf16 v[132:135], v[158:161], v[178:181], v[132:135]
	v_mfma_f32_16x16x32_bf16 v[128:131], v[170:173], v[178:181], v[128:131]
	v_mfma_f32_16x16x32_bf16 v[116:119], v[158:161], v[198:201], v[116:119]
	v_mfma_f32_16x16x32_bf16 v[112:115], v[170:173], v[198:201], v[112:115]
	v_mfma_f32_16x16x32_bf16 v[100:103], v[158:161], v[206:209], v[100:103]
	v_mfma_f32_16x16x32_bf16 v[96:99], v[170:173], v[206:209], v[96:99]
	v_mfma_f32_16x16x32_bf16 v[76:79], v[158:161], v[228:231], v[76:79]
	v_mfma_f32_16x16x32_bf16 v[72:75], v[170:173], v[228:231], v[72:75]
	s_setprio 1
	s_barrier
	s_add_i32 s18, s28, s4
	v_lshl_add_u64 v[182:183], v[182:183], 0, s[68:69]
	s_mov_b32 m0, s18
	ds_read_b128 v[174:177], v165 offset:49152
	ds_read_b128 v[178:181], v165 offset:50176
	ds_read_b128 v[194:197], v165 offset:51200
	ds_read_b128 v[198:201], v165 offset:52224
	ds_read_b128 v[202:205], v165 offset:53248
	ds_read_b128 v[206:209], v165 offset:54272
	ds_read_b128 v[224:227], v165 offset:55296
	ds_read_b128 v[228:231], v165 offset:56320
	global_load_lds_dwordx4 v[182:183], off
	s_add_i32 m0, s18, 0x2000
	s_add_u32 s18, s30, 0x160080
	v_lshl_add_u64 v[182:183], v[210:211], 0, s[68:69]
	s_addc_u32 s19, s31, 0
	s_add_i32 s28, s29, s4
	global_load_lds_dwordx4 v[182:183], off
	v_lshl_add_u64 v[182:183], s[18:19], 0, v[184:185]
	s_mov_b32 m0, s28
	s_nop 0
	global_load_lds_dwordx4 v[182:183], off
	v_lshl_add_u64 v[182:183], s[18:19], 0, v[144:145]
	s_add_i32 m0, s28, 0x2000
	s_nop 0
	global_load_lds_dwordx4 v[182:183], off
	v_lshl_add_u64 v[182:183], v[216:217], 0, s[68:69]
	s_mov_b32 m0, s42
	s_nop 0
	global_load_lds_dwordx4 v[182:183], off
	v_lshl_add_u64 v[182:183], v[218:219], 0, s[68:69]
	s_mov_b32 m0, s43
	s_nop 0
	global_load_lds_dwordx4 v[182:183], off
	s_waitcnt vmcnt(6)
	s_waitcnt lgkmcnt(0)
	s_barrier
	s_setprio 0
	s_waitcnt lgkmcnt(0)
	v_mfma_f32_16x16x32_bf16 v[60:63], v[64:67], v[174:177], v[60:63]
	v_mfma_f32_16x16x32_bf16 v[56:59], v[80:83], v[174:177], v[56:59]
	v_mfma_f32_16x16x32_bf16 v[44:47], v[64:67], v[194:197], v[44:47]
	v_mfma_f32_16x16x32_bf16 v[40:43], v[80:83], v[194:197], v[40:43]
	v_mfma_f32_16x16x32_bf16 v[28:31], v[64:67], v[202:205], v[28:31]
	v_mfma_f32_16x16x32_bf16 v[24:27], v[80:83], v[202:205], v[24:27]
	v_mfma_f32_16x16x32_bf16 v[12:15], v[64:67], v[224:227], v[12:15]
	v_mfma_f32_16x16x32_bf16 v[8:11], v[80:83], v[224:227], v[8:11]
	v_mfma_f32_16x16x32_bf16 v[60:63], v[68:71], v[178:181], v[60:63]
	v_mfma_f32_16x16x32_bf16 v[56:59], v[84:87], v[178:181], v[56:59]
	v_mfma_f32_16x16x32_bf16 v[44:47], v[68:71], v[198:201], v[44:47]
	v_mfma_f32_16x16x32_bf16 v[40:43], v[84:87], v[198:201], v[40:43]
	v_mfma_f32_16x16x32_bf16 v[28:31], v[68:71], v[206:209], v[28:31]
	v_mfma_f32_16x16x32_bf16 v[24:27], v[84:87], v[206:209], v[24:27]
	v_mfma_f32_16x16x32_bf16 v[12:15], v[68:71], v[228:231], v[12:15]
	v_mfma_f32_16x16x32_bf16 v[8:11], v[84:87], v[228:231], v[8:11]
	s_setprio 1
	s_setprio 0
	v_mfma_f32_16x16x32_bf16 v[52:55], v[154:157], v[174:177], v[52:55]
	v_mfma_f32_16x16x32_bf16 v[48:51], v[166:169], v[174:177], v[48:51]
	v_mfma_f32_16x16x32_bf16 v[36:39], v[154:157], v[194:197], v[36:39]
	v_mfma_f32_16x16x32_bf16 v[32:35], v[166:169], v[194:197], v[32:35]
	v_mfma_f32_16x16x32_bf16 v[20:23], v[154:157], v[202:205], v[20:23]
	v_mfma_f32_16x16x32_bf16 v[16:19], v[166:169], v[202:205], v[16:19]
	v_mfma_f32_16x16x32_bf16 v[4:7], v[154:157], v[224:227], v[4:7]
	v_mfma_f32_16x16x32_bf16 v[0:3], v[166:169], v[224:227], v[0:3]
	v_mfma_f32_16x16x32_bf16 v[52:55], v[158:161], v[178:181], v[52:55]
	v_mfma_f32_16x16x32_bf16 v[48:51], v[170:173], v[178:181], v[48:51]
	v_mfma_f32_16x16x32_bf16 v[36:39], v[158:161], v[198:201], v[36:39]
	v_mfma_f32_16x16x32_bf16 v[32:35], v[170:173], v[198:201], v[32:35]
	v_mfma_f32_16x16x32_bf16 v[20:23], v[158:161], v[206:209], v[20:23]
	v_mfma_f32_16x16x32_bf16 v[16:19], v[170:173], v[206:209], v[16:19]
	v_mfma_f32_16x16x32_bf16 v[4:7], v[158:161], v[228:231], v[4:7]
	v_mfma_f32_16x16x32_bf16 v[0:3], v[170:173], v[228:231], v[0:3]
	s_setprio 1
	s_barrier
	s_add_i32 s61, s61, 2
	s_add_u32 s59, s59, 0x100
	s_addc_u32 s60, s60, 0
	s_cmpk_gt_u32 s61, 0x55
	s_mov_b64 s[18:19], s[24:25]
	s_cbranch_scc0 .LBB0_1661
	s_and_b64 vcc, exec, s[8:9]
	s_cbranch_vccz .LBB0_1664
	s_barrier

.LBB0_1741:
	s_add_u32 s38, s36, 0x100
	s_addc_u32 s39, s37, 0
	s_add_i32 s28, 0, 0x10000
	s_cmp_eq_u32 s59, 4
	s_cselect_b32 s43, s11, s39
	s_cselect_b32 s42, s50, s38
	s_cselect_b32 s41, s51, s58
	s_cselect_b32 s40, s52, s53
	s_add_i32 s48, 0, 0x14000
	v_add_u32_e32 v124, s28, v172
	v_add_u32_e32 v170, s48, v172
	ds_read_b128 v[112:115], v124
	ds_read_b128 v[116:119], v124 offset:1024
	ds_read_b128 v[120:123], v124 offset:2048
	ds_read_b128 v[124:127], v124 offset:3072
	ds_read_b128 v[176:179], v170
	ds_read_b128 v[180:183], v170 offset:1024
	ds_read_b128 v[194:197], v170 offset:2048
	ds_read_b128 v[198:201], v170 offset:3072
	v_lshl_add_u64 v[170:171], s[36:37], 0, v[166:167]
	s_add_i32 m0, s20, 0xc000
	ds_read_b128 v[202:205], v174
	ds_read_b128 v[206:209], v174 offset:1024
	ds_read_b128 v[224:227], v174 offset:2048
	ds_read_b128 v[228:231], v174 offset:3072
	ds_read_b128 v[232:235], v174 offset:4096
	ds_read_b128 v[236:239], v174 offset:5120
	ds_read_b128 v[240:243], v174 offset:6144
	ds_read_b128 v[244:247], v174 offset:7168
	global_load_lds_dwordx4 v[170:171], off
	v_lshl_add_u64 v[170:171], s[36:37], 0, v[168:169]
	s_add_i32 m0, s20, 0xe000
	s_nop 0
	global_load_lds_dwordx4 v[170:171], off
	s_waitcnt vmcnt(8)
	s_waitcnt lgkmcnt(0)
	s_barrier
	s_setprio 0
	s_waitcnt lgkmcnt(0)
	v_mfma_f32_16x16x32_bf16 v[140:143], v[112:115], v[202:205], v[140:143]
	v_mfma_f32_16x16x32_bf16 v[136:139], v[120:123], v[202:205], v[136:139]
	v_mfma_f32_16x16x32_bf16 v[108:111], v[112:115], v[224:227], v[108:111]
	v_mfma_f32_16x16x32_bf16 v[104:107], v[120:123], v[224:227], v[104:107]
	v_mfma_f32_16x16x32_bf16 v[92:95], v[112:115], v[232:235], v[92:95]
	v_mfma_f32_16x16x32_bf16 v[88:91], v[120:123], v[232:235], v[88:91]
	v_mfma_f32_16x16x32_bf16 v[76:79], v[112:115], v[240:243], v[76:79]
	v_mfma_f32_16x16x32_bf16 v[72:75], v[120:123], v[240:243], v[72:75]
	v_mfma_f32_16x16x32_bf16 v[140:143], v[116:119], v[206:209], v[140:143]
	v_mfma_f32_16x16x32_bf16 v[136:139], v[124:127], v[206:209], v[136:139]
	v_mfma_f32_16x16x32_bf16 v[108:111], v[116:119], v[228:231], v[108:111]
	v_mfma_f32_16x16x32_bf16 v[104:107], v[124:127], v[228:231], v[104:107]
	v_mfma_f32_16x16x32_bf16 v[92:95], v[116:119], v[236:239], v[92:95]
	v_mfma_f32_16x16x32_bf16 v[88:91], v[124:127], v[236:239], v[88:91]
	v_mfma_f32_16x16x32_bf16 v[76:79], v[116:119], v[244:247], v[76:79]
	v_mfma_f32_16x16x32_bf16 v[72:75], v[124:127], v[244:247], v[72:75]
	s_setprio 1
	s_setprio 0
	v_mfma_f32_16x16x32_bf16 v[132:135], v[176:179], v[202:205], v[132:135]
	v_mfma_f32_16x16x32_bf16 v[128:131], v[194:197], v[202:205], v[128:131]
	v_mfma_f32_16x16x32_bf16 v[100:103], v[176:179], v[224:227], v[100:103]
	v_mfma_f32_16x16x32_bf16 v[96:99], v[194:197], v[224:227], v[96:99]
	v_mfma_f32_16x16x32_bf16 v[84:87], v[176:179], v[232:235], v[84:87]
	v_mfma_f32_16x16x32_bf16 v[80:83], v[194:197], v[232:235], v[80:83]
	v_mfma_f32_16x16x32_bf16 v[68:71], v[176:179], v[240:243], v[68:71]
	v_mfma_f32_16x16x32_bf16 v[64:67], v[194:197], v[240:243], v[64:67]
	v_mfma_f32_16x16x32_bf16 v[132:135], v[180:183], v[206:209], v[132:135]
	v_mfma_f32_16x16x32_bf16 v[128:131], v[198:201], v[206:209], v[128:131]
	v_mfma_f32_16x16x32_bf16 v[100:103], v[180:183], v[228:231], v[100:103]
	v_mfma_f32_16x16x32_bf16 v[96:99], v[198:201], v[228:231], v[96:99]
	v_mfma_f32_16x16x32_bf16 v[84:87], v[180:183], v[236:239], v[84:87]
	v_mfma_f32_16x16x32_bf16 v[80:83], v[198:201], v[236:239], v[80:83]
	v_mfma_f32_16x16x32_bf16 v[68:71], v[180:183], v[244:247], v[68:71]
	v_mfma_f32_16x16x32_bf16 v[64:67], v[198:201], v[244:247], v[64:67]
	s_setprio 1
	s_barrier
	s_add_i32 s28, s28, s4
	v_lshl_add_u64 v[170:171], s[40:41], 0, v[184:185]
	s_mov_b32 m0, s28
	ds_read_b128 v[202:205], v174 offset:16384
	ds_read_b128 v[206:209], v174 offset:17408
	ds_read_b128 v[224:227], v174 offset:18432
	ds_read_b128 v[228:231], v174 offset:19456
	ds_read_b128 v[232:235], v174 offset:20480
	ds_read_b128 v[236:239], v174 offset:21504
	ds_read_b128 v[240:243], v174 offset:22528
	ds_read_b128 v[244:247], v174 offset:23552
	global_load_lds_dwordx4 v[170:171], off
	s_add_i32 m0, s28, 0x2000
	s_add_u32 s28, s40, 0x160000
	v_lshl_add_u64 v[210:211], s[40:41], 0, v[144:145]
	s_addc_u32 s29, s41, 0
	s_add_i32 s36, s48, s4
	global_load_lds_dwordx4 v[210:211], off
	v_lshl_add_u64 v[216:217], s[28:29], 0, v[184:185]
	s_mov_b32 m0, s36
	v_lshl_add_u64 v[218:219], s[42:43], 0, v[146:147]
	global_load_lds_dwordx4 v[216:217], off
	v_lshl_add_u64 v[216:217], s[28:29], 0, v[144:145]
	s_add_i32 m0, s36, 0x2000
	s_nop 0
	global_load_lds_dwordx4 v[216:217], off
	v_lshl_add_u64 v[216:217], s[42:43], 0, v[148:149]
	s_waitcnt vmcnt(6)
	s_waitcnt lgkmcnt(0)
	s_barrier
	s_setprio 0
	s_waitcnt lgkmcnt(0)
	v_mfma_f32_16x16x32_bf16 v[60:63], v[112:115], v[202:205], v[60:63]
	v_mfma_f32_16x16x32_bf16 v[56:59], v[120:123], v[202:205], v[56:59]
	v_mfma_f32_16x16x32_bf16 v[44:47], v[112:115], v[224:227], v[44:47]
	v_mfma_f32_16x16x32_bf16 v[40:43], v[120:123], v[224:227], v[40:43]
	v_mfma_f32_16x16x32_bf16 v[36:39], v[112:115], v[232:235], v[36:39]
	v_mfma_f32_16x16x32_bf16 v[28:31], v[120:123], v[232:235], v[28:31]
	v_mfma_f32_16x16x32_bf16 v[20:23], v[112:115], v[240:243], v[20:23]
	v_mfma_f32_16x16x32_bf16 v[12:15], v[120:123], v[240:243], v[12:15]
	v_mfma_f32_16x16x32_bf16 v[60:63], v[116:119], v[206:209], v[60:63]
	v_mfma_f32_16x16x32_bf16 v[56:59], v[124:127], v[206:209], v[56:59]
	v_mfma_f32_16x16x32_bf16 v[44:47], v[116:119], v[228:231], v[44:47]
	v_mfma_f32_16x16x32_bf16 v[40:43], v[124:127], v[228:231], v[40:43]
	v_mfma_f32_16x16x32_bf16 v[36:39], v[116:119], v[236:239], v[36:39]
	v_mfma_f32_16x16x32_bf16 v[28:31], v[124:127], v[236:239], v[28:31]
	v_mfma_f32_16x16x32_bf16 v[20:23], v[116:119], v[244:247], v[20:23]
	v_mfma_f32_16x16x32_bf16 v[12:15], v[124:127], v[244:247], v[12:15]
	s_setprio 1
	s_setprio 0
	v_mfma_f32_16x16x32_bf16 v[52:55], v[176:179], v[202:205], v[52:55]
	v_mfma_f32_16x16x32_bf16 v[48:51], v[194:197], v[202:205], v[48:51]
	v_mfma_f32_16x16x32_bf16 v[32:35], v[176:179], v[224:227], v[32:35]
	v_mfma_f32_16x16x32_bf16 v[24:27], v[194:197], v[224:227], v[24:27]
	v_mfma_f32_16x16x32_bf16 v[16:19], v[176:179], v[232:235], v[16:19]
	v_mfma_f32_16x16x32_bf16 v[8:11], v[194:197], v[232:235], v[8:11]
	v_mfma_f32_16x16x32_bf16 v[4:7], v[176:179], v[240:243], v[4:7]
	v_mfma_f32_16x16x32_bf16 v[0:3], v[194:197], v[240:243], v[0:3]
	v_mfma_f32_16x16x32_bf16 v[52:55], v[180:183], v[206:209], v[52:55]
	v_mfma_f32_16x16x32_bf16 v[48:51], v[198:201], v[206:209], v[48:51]
	v_mfma_f32_16x16x32_bf16 v[32:35], v[180:183], v[228:231], v[32:35]
	v_mfma_f32_16x16x32_bf16 v[24:27], v[198:201], v[228:231], v[24:27]
	v_mfma_f32_16x16x32_bf16 v[16:19], v[180:183], v[236:239], v[16:19]
	v_mfma_f32_16x16x32_bf16 v[8:11], v[198:201], v[236:239], v[8:11]
	v_mfma_f32_16x16x32_bf16 v[4:7], v[180:183], v[244:247], v[4:7]
	v_mfma_f32_16x16x32_bf16 v[0:3], v[198:201], v[244:247], v[0:3]
	s_setprio 1
	s_barrier
	s_add_i32 s36, 0, 0x18000
	s_add_i32 s37, 0, 0x1c000
	v_add_u32_e32 v124, s36, v172
	v_add_u32_e32 v175, s37, v172
	ds_read_b128 v[112:115], v124
	ds_read_b128 v[116:119], v124 offset:1024
	ds_read_b128 v[120:123], v124 offset:2048
	ds_read_b128 v[124:127], v124 offset:3072
	ds_read_b128 v[176:179], v175
	ds_read_b128 v[180:183], v175 offset:1024
	ds_read_b128 v[194:197], v175 offset:2048
	ds_read_b128 v[198:201], v175 offset:3072
	s_add_u32 s28, s42, 0x160000
	s_addc_u32 s29, s43, 0
	s_mov_b32 m0, s26
	v_lshl_add_u64 v[220:221], s[28:29], 0, v[148:149]
	ds_read_b128 v[202:205], v174 offset:32768
	ds_read_b128 v[206:209], v174 offset:33792
	ds_read_b128 v[224:227], v174 offset:34816
	ds_read_b128 v[228:231], v174 offset:35840
	ds_read_b128 v[232:235], v174 offset:36864
	ds_read_b128 v[236:239], v174 offset:37888
	ds_read_b128 v[240:243], v174 offset:38912
	ds_read_b128 v[244:247], v174 offset:39936
	global_load_lds_dwordx4 v[220:221], off
	v_lshl_add_u64 v[220:221], s[28:29], 0, v[146:147]
	s_mov_b32 m0, s27
	s_nop 0
	global_load_lds_dwordx4 v[220:221], off
	s_mov_b32 m0, s20
	s_nop 0
	global_load_lds_dwordx4 v[216:217], off
	s_mov_b32 m0, s21
	s_nop 0
	global_load_lds_dwordx4 v[218:219], off
	s_waitcnt vmcnt(8)
	s_waitcnt lgkmcnt(0)
	s_barrier
	s_setprio 0
	s_waitcnt lgkmcnt(0)
	v_mfma_f32_16x16x32_bf16 v[140:143], v[112:115], v[202:205], v[140:143]
	v_mfma_f32_16x16x32_bf16 v[136:139], v[120:123], v[202:205], v[136:139]
	v_mfma_f32_16x16x32_bf16 v[108:111], v[112:115], v[224:227], v[108:111]
	v_mfma_f32_16x16x32_bf16 v[104:107], v[120:123], v[224:227], v[104:107]
	v_mfma_f32_16x16x32_bf16 v[92:95], v[112:115], v[232:235], v[92:95]
	v_mfma_f32_16x16x32_bf16 v[88:91], v[120:123], v[232:235], v[88:91]
	v_mfma_f32_16x16x32_bf16 v[76:79], v[112:115], v[240:243], v[76:79]
	v_mfma_f32_16x16x32_bf16 v[72:75], v[120:123], v[240:243], v[72:75]
	v_mfma_f32_16x16x32_bf16 v[140:143], v[116:119], v[206:209], v[140:143]
	v_mfma_f32_16x16x32_bf16 v[136:139], v[124:127], v[206:209], v[136:139]
	v_mfma_f32_16x16x32_bf16 v[108:111], v[116:119], v[228:231], v[108:111]
	v_mfma_f32_16x16x32_bf16 v[104:107], v[124:127], v[228:231], v[104:107]
	v_mfma_f32_16x16x32_bf16 v[92:95], v[116:119], v[236:239], v[92:95]
	v_mfma_f32_16x16x32_bf16 v[88:91], v[124:127], v[236:239], v[88:91]
	v_mfma_f32_16x16x32_bf16 v[76:79], v[116:119], v[244:247], v[76:79]
	v_mfma_f32_16x16x32_bf16 v[72:75], v[124:127], v[244:247], v[72:75]
	s_setprio 1
	s_setprio 0
	v_mfma_f32_16x16x32_bf16 v[132:135], v[176:179], v[202:205], v[132:135]
	v_mfma_f32_16x16x32_bf16 v[128:131], v[194:197], v[202:205], v[128:131]
	v_mfma_f32_16x16x32_bf16 v[100:103], v[176:179], v[224:227], v[100:103]
	v_mfma_f32_16x16x32_bf16 v[96:99], v[194:197], v[224:227], v[96:99]
	v_mfma_f32_16x16x32_bf16 v[84:87], v[176:179], v[232:235], v[84:87]
	v_mfma_f32_16x16x32_bf16 v[80:83], v[194:197], v[232:235], v[80:83]
	v_mfma_f32_16x16x32_bf16 v[68:71], v[176:179], v[240:243], v[68:71]
	v_mfma_f32_16x16x32_bf16 v[64:67], v[194:197], v[240:243], v[64:67]
	v_mfma_f32_16x16x32_bf16 v[132:135], v[180:183], v[206:209], v[132:135]
	v_mfma_f32_16x16x32_bf16 v[128:131], v[198:201], v[206:209], v[128:131]
	v_mfma_f32_16x16x32_bf16 v[100:103], v[180:183], v[228:231], v[100:103]
	v_mfma_f32_16x16x32_bf16 v[96:99], v[198:201], v[228:231], v[96:99]
	v_mfma_f32_16x16x32_bf16 v[84:87], v[180:183], v[236:239], v[84:87]
	v_mfma_f32_16x16x32_bf16 v[80:83], v[198:201], v[236:239], v[80:83]
	v_mfma_f32_16x16x32_bf16 v[68:71], v[180:183], v[244:247], v[68:71]
	v_mfma_f32_16x16x32_bf16 v[64:67], v[198:201], v[244:247], v[64:67]
	s_setprio 1
	s_barrier
	s_add_i32 s28, s36, s4
	v_lshl_add_u64 v[170:171], v[170:171], 0, s[68:69]
	s_mov_b32 m0, s28
	ds_read_b128 v[202:205], v174 offset:49152
	ds_read_b128 v[206:209], v174 offset:50176
	ds_read_b128 v[224:227], v174 offset:51200
	ds_read_b128 v[228:231], v174 offset:52224
	ds_read_b128 v[232:235], v174 offset:53248
	ds_read_b128 v[236:239], v174 offset:54272
	ds_read_b128 v[240:243], v174 offset:55296
	ds_read_b128 v[244:247], v174 offset:56320
	global_load_lds_dwordx4 v[170:171], off
	s_add_i32 m0, s28, 0x2000
	s_add_u32 s28, s40, 0x160080
	v_lshl_add_u64 v[170:171], v[210:211], 0, s[68:69]
	s_addc_u32 s29, s41, 0
	s_add_i32 s36, s37, s4
	global_load_lds_dwordx4 v[170:171], off
	v_lshl_add_u64 v[170:171], s[28:29], 0, v[184:185]
	s_mov_b32 m0, s36
	s_nop 0
	global_load_lds_dwordx4 v[170:171], off
	v_lshl_add_u64 v[170:171], s[28:29], 0, v[144:145]
	s_add_i32 m0, s36, 0x2000
	s_nop 0
	global_load_lds_dwordx4 v[170:171], off
	v_lshl_add_u64 v[170:171], v[216:217], 0, s[68:69]
	s_mov_b32 m0, s44
	s_nop 0
	global_load_lds_dwordx4 v[170:171], off
	v_lshl_add_u64 v[170:171], v[218:219], 0, s[68:69]
	s_mov_b32 m0, s45
	s_nop 0
	global_load_lds_dwordx4 v[170:171], off
	s_waitcnt vmcnt(6)
	s_waitcnt lgkmcnt(0)
	s_barrier
	s_setprio 0
	s_waitcnt lgkmcnt(0)
	v_mfma_f32_16x16x32_bf16 v[60:63], v[112:115], v[202:205], v[60:63]
	v_mfma_f32_16x16x32_bf16 v[56:59], v[120:123], v[202:205], v[56:59]
	v_mfma_f32_16x16x32_bf16 v[44:47], v[112:115], v[224:227], v[44:47]
	v_mfma_f32_16x16x32_bf16 v[40:43], v[120:123], v[224:227], v[40:43]
	v_mfma_f32_16x16x32_bf16 v[36:39], v[112:115], v[232:235], v[36:39]
	v_mfma_f32_16x16x32_bf16 v[28:31], v[120:123], v[232:235], v[28:31]
	v_mfma_f32_16x16x32_bf16 v[20:23], v[112:115], v[240:243], v[20:23]
	v_mfma_f32_16x16x32_bf16 v[12:15], v[120:123], v[240:243], v[12:15]
	v_mfma_f32_16x16x32_bf16 v[60:63], v[116:119], v[206:209], v[60:63]
	v_mfma_f32_16x16x32_bf16 v[56:59], v[124:127], v[206:209], v[56:59]
	v_mfma_f32_16x16x32_bf16 v[44:47], v[116:119], v[228:231], v[44:47]
	v_mfma_f32_16x16x32_bf16 v[40:43], v[124:127], v[228:231], v[40:43]
	v_mfma_f32_16x16x32_bf16 v[36:39], v[116:119], v[236:239], v[36:39]
	v_mfma_f32_16x16x32_bf16 v[28:31], v[124:127], v[236:239], v[28:31]
	v_mfma_f32_16x16x32_bf16 v[20:23], v[116:119], v[244:247], v[20:23]
	v_mfma_f32_16x16x32_bf16 v[12:15], v[124:127], v[244:247], v[12:15]
	s_setprio 1
	s_setprio 0
	v_mfma_f32_16x16x32_bf16 v[52:55], v[176:179], v[202:205], v[52:55]
	v_mfma_f32_16x16x32_bf16 v[48:51], v[194:197], v[202:205], v[48:51]
	v_mfma_f32_16x16x32_bf16 v[32:35], v[176:179], v[224:227], v[32:35]
	v_mfma_f32_16x16x32_bf16 v[24:27], v[194:197], v[224:227], v[24:27]
	v_mfma_f32_16x16x32_bf16 v[16:19], v[176:179], v[232:235], v[16:19]
	v_mfma_f32_16x16x32_bf16 v[8:11], v[194:197], v[232:235], v[8:11]
	v_mfma_f32_16x16x32_bf16 v[4:7], v[176:179], v[240:243], v[4:7]
	v_mfma_f32_16x16x32_bf16 v[0:3], v[194:197], v[240:243], v[0:3]
	v_mfma_f32_16x16x32_bf16 v[52:55], v[180:183], v[206:209], v[52:55]
	v_mfma_f32_16x16x32_bf16 v[48:51], v[198:201], v[206:209], v[48:51]
	v_mfma_f32_16x16x32_bf16 v[32:35], v[180:183], v[228:231], v[32:35]
	v_mfma_f32_16x16x32_bf16 v[24:27], v[198:201], v[228:231], v[24:27]
	v_mfma_f32_16x16x32_bf16 v[16:19], v[180:183], v[236:239], v[16:19]
	v_mfma_f32_16x16x32_bf16 v[8:11], v[198:201], v[236:239], v[8:11]
	v_mfma_f32_16x16x32_bf16 v[4:7], v[180:183], v[244:247], v[4:7]
	v_mfma_f32_16x16x32_bf16 v[0:3], v[198:201], v[244:247], v[0:3]
	s_setprio 1
	s_barrier
	s_add_i32 s59, s59, 2
	s_add_u32 s53, s53, 0x100
	s_addc_u32 s58, s58, 0
	s_cmp_gt_u32 s59, 5
	s_mov_b64 s[36:37], s[38:39]
	s_cbranch_scc0 .LBB0_1741
	s_and_b64 vcc, exec, s[8:9]
	s_cbranch_vccz .LBB0_1744
	s_barrier
